# hand-off trim: s_setprio 0 moved behind the segment-end barrier, redundant lgkmcnt wait after the barrier removed (all GEMM MFMA segments)
# speedup vs baseline: 1.0255x; 1.0255x over previous
.LBB0_809:
	s_andn2_b64 vcc, exec, s[52:53]
	s_waitcnt vmcnt(0)
	s_cbranch_vccnz .LBB0_812
	s_add_u32 s26, s26, 0x80
	s_addc_u32 s27, s27, 0
	s_add_u32 s19, s30, 0x100
	s_addc_u32 s20, s31, 0
	s_mov_b32 s21, 0
	s_add_i32 s22, s21, 2
	s_add_u32 s23, s26, 0x80
	s_addc_u32 s28, s27, 0
	s_add_i32 s34, 0, 0x10000
	s_cmp_eq_u32 s81, s21
	s_cselect_b32 s31, s3, s28
	s_cselect_b32 s30, s2, s23
	v_add_u32_e32 v2, s34, v231
	s_cselect_b32 s29, s61, s20
	s_cselect_b32 s28, s60, s19
	s_add_i32 s21, 0, 0x14000
	ds_read_b128 v[100:103], v2
	ds_read_b128 v[104:107], v2 offset:1024
	ds_read_b128 v[108:111], v2 offset:2048
	ds_read_b128 v[112:115], v2 offset:3072
	v_add_u32_e32 v2, s21, v231
	ds_read_b128 v[132:135], v2
	ds_read_b128 v[136:139], v2 offset:1024
	ds_read_b128 v[140:143], v2 offset:2048
	ds_read_b128 v[144:147], v2 offset:3072
	v_lshl_add_u64 v[208:209], s[26:27], 0, v[204:205]
	s_add_i32 m0, s72, 0xc000
	ds_read_b128 v[164:167], v240
	ds_read_b128 v[168:171], v240 offset:1024
	ds_read_b128 v[172:175], v240 offset:2048
	ds_read_b128 v[176:179], v240 offset:3072
	ds_read_b128 v[180:183], v240 offset:4096
	ds_read_b128 v[184:187], v240 offset:5120
	ds_read_b128 v[188:191], v240 offset:6144
	ds_read_b128 v[192:195], v240 offset:7168
	global_load_lds_dwordx4 v[208:209], off
	v_lshl_add_u64 v[208:209], s[26:27], 0, v[206:207]
	s_add_i32 m0, s72, 0xe000
	s_nop 0
	global_load_lds_dwordx4 v[208:209], off
	s_waitcnt vmcnt(8)
	s_waitcnt lgkmcnt(0)
	s_barrier
	s_setprio 1
	v_mfma_f32_16x16x32_bf16 v[160:163], v[100:103], v[164:167], 0
	v_mfma_f32_16x16x32_bf16 v[156:159], v[108:111], v[164:167], 0
	v_mfma_f32_16x16x32_bf16 v[128:131], v[100:103], v[172:175], 0
	v_mfma_f32_16x16x32_bf16 v[124:127], v[108:111], v[172:175], 0
	v_mfma_f32_16x16x32_bf16 v[96:99], v[100:103], v[180:183], 0
	v_mfma_f32_16x16x32_bf16 v[92:95], v[108:111], v[180:183], 0
	v_mfma_f32_16x16x32_bf16 v[80:83], v[100:103], v[188:191], 0
	v_mfma_f32_16x16x32_bf16 v[76:79], v[108:111], v[188:191], 0
	v_mfma_f32_16x16x32_bf16 v[160:163], v[104:107], v[168:171], v[160:163]
	v_mfma_f32_16x16x32_bf16 v[156:159], v[112:115], v[168:171], v[156:159]
	v_mfma_f32_16x16x32_bf16 v[128:131], v[104:107], v[176:179], v[128:131]
	v_mfma_f32_16x16x32_bf16 v[124:127], v[112:115], v[176:179], v[124:127]
	v_mfma_f32_16x16x32_bf16 v[96:99], v[104:107], v[184:187], v[96:99]
	v_mfma_f32_16x16x32_bf16 v[92:95], v[112:115], v[184:187], v[92:95]
	v_mfma_f32_16x16x32_bf16 v[80:83], v[104:107], v[192:195], v[80:83]
	v_mfma_f32_16x16x32_bf16 v[76:79], v[112:115], v[192:195], v[76:79]
	s_setprio 0
	s_setprio 1
	v_mfma_f32_16x16x32_bf16 v[152:155], v[132:135], v[164:167], 0
	v_mfma_f32_16x16x32_bf16 v[148:151], v[140:143], v[164:167], 0
	v_mfma_f32_16x16x32_bf16 v[120:123], v[132:135], v[172:175], 0
	v_mfma_f32_16x16x32_bf16 v[116:119], v[140:143], v[172:175], 0
	v_mfma_f32_16x16x32_bf16 v[88:91], v[132:135], v[180:183], 0
	v_mfma_f32_16x16x32_bf16 v[84:87], v[140:143], v[180:183], 0
	v_mfma_f32_16x16x32_bf16 v[72:75], v[132:135], v[188:191], 0
	v_mfma_f32_16x16x32_bf16 v[68:71], v[140:143], v[188:191], 0
	v_mfma_f32_16x16x32_bf16 v[152:155], v[136:139], v[168:171], v[152:155]
	v_mfma_f32_16x16x32_bf16 v[148:151], v[144:147], v[168:171], v[148:151]
	v_mfma_f32_16x16x32_bf16 v[120:123], v[136:139], v[176:179], v[120:123]
	v_mfma_f32_16x16x32_bf16 v[116:119], v[144:147], v[176:179], v[116:119]
	v_mfma_f32_16x16x32_bf16 v[88:91], v[136:139], v[184:187], v[88:91]
	v_mfma_f32_16x16x32_bf16 v[84:87], v[144:147], v[184:187], v[84:87]
	v_mfma_f32_16x16x32_bf16 v[72:75], v[136:139], v[192:195], v[72:75]
	v_mfma_f32_16x16x32_bf16 v[68:71], v[144:147], v[192:195], v[68:71]
	s_barrier
	s_setprio 0
	s_add_i32 s23, s34, s69
	v_lshl_add_u64 v[208:209], s[28:29], 0, v[200:201]
	s_mov_b32 m0, s23
	ds_read_b128 v[164:167], v240 offset:16384
	ds_read_b128 v[168:171], v240 offset:17408
	ds_read_b128 v[172:175], v240 offset:18432
	ds_read_b128 v[176:179], v240 offset:19456
	ds_read_b128 v[180:183], v240 offset:20480
	ds_read_b128 v[184:187], v240 offset:21504
	ds_read_b128 v[188:191], v240 offset:22528
	ds_read_b128 v[192:195], v240 offset:23552
	global_load_lds_dwordx4 v[208:209], off
	s_add_i32 m0, s23, 0x2000
	v_lshl_add_u64 v[210:211], s[28:29], 0, v[196:197]
	s_add_u32 s28, s28, s6
	s_addc_u32 s29, s29, s7
	s_add_i32 s21, s21, s69
	global_load_lds_dwordx4 v[210:211], off
	v_lshl_add_u64 v[218:219], s[28:29], 0, v[200:201]
	s_mov_b32 m0, s21
	v_lshl_add_u64 v[220:221], s[28:29], 0, v[196:197]
	global_load_lds_dwordx4 v[218:219], off
	s_add_i32 m0, s21, 0x2000
	v_lshl_add_u64 v[222:223], s[30:31], 0, v[202:203]
	global_load_lds_dwordx4 v[220:221], off
	s_mov_b32 m0, s72
	v_lshl_add_u64 v[224:225], s[30:31], 0, v[198:199]
	global_load_lds_dwordx4 v[222:223], off
	s_mov_b32 m0, s73
	s_nop 0
	global_load_lds_dwordx4 v[224:225], off
	s_waitcnt vmcnt(8)
	s_waitcnt lgkmcnt(0)
	s_barrier
	s_setprio 1
	v_mfma_f32_16x16x32_bf16 v[64:67], v[100:103], v[164:167], 0
	v_mfma_f32_16x16x32_bf16 v[60:63], v[108:111], v[164:167], 0
	v_mfma_f32_16x16x32_bf16 v[48:51], v[100:103], v[172:175], 0
	v_mfma_f32_16x16x32_bf16 v[44:47], v[108:111], v[172:175], 0
	v_mfma_f32_16x16x32_bf16 v[32:35], v[100:103], v[180:183], 0
	v_mfma_f32_16x16x32_bf16 v[28:31], v[108:111], v[180:183], 0
	v_mfma_f32_16x16x32_bf16 v[16:19], v[100:103], v[188:191], 0
	v_mfma_f32_16x16x32_bf16 v[12:15], v[108:111], v[188:191], 0
	v_mfma_f32_16x16x32_bf16 v[64:67], v[104:107], v[168:171], v[64:67]
	v_mfma_f32_16x16x32_bf16 v[60:63], v[112:115], v[168:171], v[60:63]
	v_mfma_f32_16x16x32_bf16 v[48:51], v[104:107], v[176:179], v[48:51]
	v_mfma_f32_16x16x32_bf16 v[44:47], v[112:115], v[176:179], v[44:47]
	v_mfma_f32_16x16x32_bf16 v[32:35], v[104:107], v[184:187], v[32:35]
	v_mfma_f32_16x16x32_bf16 v[28:31], v[112:115], v[184:187], v[28:31]
	v_mfma_f32_16x16x32_bf16 v[16:19], v[104:107], v[192:195], v[16:19]
	v_mfma_f32_16x16x32_bf16 v[12:15], v[112:115], v[192:195], v[12:15]
	s_setprio 0
	s_setprio 1
	v_mfma_f32_16x16x32_bf16 v[56:59], v[132:135], v[164:167], 0
	v_mfma_f32_16x16x32_bf16 v[52:55], v[140:143], v[164:167], 0
	v_mfma_f32_16x16x32_bf16 v[40:43], v[132:135], v[172:175], 0
	v_mfma_f32_16x16x32_bf16 v[36:39], v[140:143], v[172:175], 0
	v_mfma_f32_16x16x32_bf16 v[24:27], v[132:135], v[180:183], 0
	v_mfma_f32_16x16x32_bf16 v[20:23], v[140:143], v[180:183], 0
	v_mfma_f32_16x16x32_bf16 v[8:11], v[132:135], v[188:191], 0
	v_mfma_f32_16x16x32_bf16 v[4:7], v[140:143], v[188:191], 0
	v_mfma_f32_16x16x32_bf16 v[56:59], v[136:139], v[168:171], v[56:59]
	v_mfma_f32_16x16x32_bf16 v[52:55], v[144:147], v[168:171], v[52:55]
	v_mfma_f32_16x16x32_bf16 v[40:43], v[136:139], v[176:179], v[40:43]
	v_mfma_f32_16x16x32_bf16 v[36:39], v[144:147], v[176:179], v[36:39]
	v_mfma_f32_16x16x32_bf16 v[24:27], v[136:139], v[184:187], v[24:27]
	v_mfma_f32_16x16x32_bf16 v[20:23], v[144:147], v[184:187], v[20:23]
	v_mfma_f32_16x16x32_bf16 v[8:11], v[136:139], v[192:195], v[8:11]
	v_mfma_f32_16x16x32_bf16 v[4:7], v[144:147], v[192:195], v[4:7]
	s_barrier
	s_setprio 0
	s_add_i32 s21, 0, 0x18000
	v_add_u32_e32 v2, s21, v231
	s_add_i32 s23, 0, 0x1c000
	ds_read_b128 v[100:103], v2
	ds_read_b128 v[104:107], v2 offset:1024
	ds_read_b128 v[108:111], v2 offset:2048
	ds_read_b128 v[112:115], v2 offset:3072
	v_add_u32_e32 v2, s23, v231
	ds_read_b128 v[132:135], v2
	ds_read_b128 v[136:139], v2 offset:1024
	ds_read_b128 v[140:143], v2 offset:2048
	ds_read_b128 v[144:147], v2 offset:3072
	s_add_u32 s28, s30, s6
	s_addc_u32 s29, s31, s7
	s_mov_b32 m0, s74
	v_lshl_add_u64 v[226:227], s[28:29], 0, v[202:203]
	ds_read_b128 v[164:167], v240 offset:32768
	ds_read_b128 v[168:171], v240 offset:33792
	ds_read_b128 v[172:175], v240 offset:34816
	ds_read_b128 v[176:179], v240 offset:35840
	ds_read_b128 v[180:183], v240 offset:36864
	ds_read_b128 v[184:187], v240 offset:37888
	ds_read_b128 v[188:191], v240 offset:38912
	ds_read_b128 v[192:195], v240 offset:39936
	global_load_lds_dwordx4 v[226:227], off
	v_lshl_add_u64 v[226:227], s[28:29], 0, v[198:199]
	s_mov_b32 m0, s75
	s_nop 0
	global_load_lds_dwordx4 v[226:227], off
	s_waitcnt vmcnt(8)
	s_waitcnt lgkmcnt(0)
	s_barrier
	s_setprio 1
	v_mfma_f32_16x16x32_bf16 v[160:163], v[100:103], v[164:167], v[160:163]
	v_mfma_f32_16x16x32_bf16 v[156:159], v[108:111], v[164:167], v[156:159]
	v_mfma_f32_16x16x32_bf16 v[128:131], v[100:103], v[172:175], v[128:131]
	v_mfma_f32_16x16x32_bf16 v[124:127], v[108:111], v[172:175], v[124:127]
	v_mfma_f32_16x16x32_bf16 v[96:99], v[100:103], v[180:183], v[96:99]
	v_mfma_f32_16x16x32_bf16 v[92:95], v[108:111], v[180:183], v[92:95]
	v_mfma_f32_16x16x32_bf16 v[80:83], v[100:103], v[188:191], v[80:83]
	v_mfma_f32_16x16x32_bf16 v[76:79], v[108:111], v[188:191], v[76:79]
	v_mfma_f32_16x16x32_bf16 v[160:163], v[104:107], v[168:171], v[160:163]
	v_mfma_f32_16x16x32_bf16 v[156:159], v[112:115], v[168:171], v[156:159]
	v_mfma_f32_16x16x32_bf16 v[128:131], v[104:107], v[176:179], v[128:131]
	v_mfma_f32_16x16x32_bf16 v[124:127], v[112:115], v[176:179], v[124:127]
	v_mfma_f32_16x16x32_bf16 v[96:99], v[104:107], v[184:187], v[96:99]
	v_mfma_f32_16x16x32_bf16 v[92:95], v[112:115], v[184:187], v[92:95]
	v_mfma_f32_16x16x32_bf16 v[80:83], v[104:107], v[192:195], v[80:83]
	v_mfma_f32_16x16x32_bf16 v[76:79], v[112:115], v[192:195], v[76:79]
	s_setprio 0
	s_setprio 1
	v_mfma_f32_16x16x32_bf16 v[152:155], v[132:135], v[164:167], v[152:155]
	v_mfma_f32_16x16x32_bf16 v[148:151], v[140:143], v[164:167], v[148:151]
	v_mfma_f32_16x16x32_bf16 v[120:123], v[132:135], v[172:175], v[120:123]
	v_mfma_f32_16x16x32_bf16 v[116:119], v[140:143], v[172:175], v[116:119]
	v_mfma_f32_16x16x32_bf16 v[88:91], v[132:135], v[180:183], v[88:91]
	v_mfma_f32_16x16x32_bf16 v[84:87], v[140:143], v[180:183], v[84:87]
	v_mfma_f32_16x16x32_bf16 v[72:75], v[132:135], v[188:191], v[72:75]
	v_mfma_f32_16x16x32_bf16 v[68:71], v[140:143], v[188:191], v[68:71]
	v_mfma_f32_16x16x32_bf16 v[152:155], v[136:139], v[168:171], v[152:155]
	v_mfma_f32_16x16x32_bf16 v[148:151], v[144:147], v[168:171], v[148:151]
	v_mfma_f32_16x16x32_bf16 v[120:123], v[136:139], v[176:179], v[120:123]
	v_mfma_f32_16x16x32_bf16 v[116:119], v[144:147], v[176:179], v[116:119]
	v_mfma_f32_16x16x32_bf16 v[88:91], v[136:139], v[184:187], v[88:91]
	v_mfma_f32_16x16x32_bf16 v[84:87], v[144:147], v[184:187], v[84:87]
	v_mfma_f32_16x16x32_bf16 v[72:75], v[136:139], v[192:195], v[72:75]
	v_mfma_f32_16x16x32_bf16 v[68:71], v[144:147], v[192:195], v[68:71]
	s_barrier
	s_setprio 0
	s_add_i32 s21, s21, s69
	v_lshl_add_u64 v[208:209], v[208:209], 0, s[24:25]
	s_mov_b32 m0, s21
	ds_read_b128 v[164:167], v240 offset:49152
	ds_read_b128 v[168:171], v240 offset:50176
	ds_read_b128 v[172:175], v240 offset:51200
	ds_read_b128 v[176:179], v240 offset:52224
	ds_read_b128 v[180:183], v240 offset:53248
	ds_read_b128 v[184:187], v240 offset:54272
	ds_read_b128 v[188:191], v240 offset:55296
	ds_read_b128 v[192:195], v240 offset:56320
	global_load_lds_dwordx4 v[208:209], off
	v_lshl_add_u64 v[208:209], v[210:211], 0, s[24:25]
	s_add_i32 m0, s21, 0x2000
	s_add_i32 s21, s23, s69
	global_load_lds_dwordx4 v[208:209], off
	v_lshl_add_u64 v[208:209], v[218:219], 0, s[24:25]
	s_mov_b32 m0, s21
	s_nop 0
	global_load_lds_dwordx4 v[208:209], off
	v_lshl_add_u64 v[208:209], v[220:221], 0, s[24:25]
	s_add_i32 m0, s21, 0x2000
	s_nop 0
	global_load_lds_dwordx4 v[208:209], off
	v_lshl_add_u64 v[208:209], v[222:223], 0, s[24:25]
	s_mov_b32 m0, s79
	s_nop 0
	global_load_lds_dwordx4 v[208:209], off
	v_lshl_add_u64 v[208:209], v[224:225], 0, s[24:25]
	s_mov_b32 m0, s80
	s_nop 0
	global_load_lds_dwordx4 v[208:209], off
	s_waitcnt vmcnt(8)
	s_waitcnt lgkmcnt(0)
	s_barrier
	s_setprio 1
	v_mfma_f32_16x16x32_bf16 v[64:67], v[100:103], v[164:167], v[64:67]
	v_mfma_f32_16x16x32_bf16 v[60:63], v[108:111], v[164:167], v[60:63]
	v_mfma_f32_16x16x32_bf16 v[48:51], v[100:103], v[172:175], v[48:51]
	v_mfma_f32_16x16x32_bf16 v[44:47], v[108:111], v[172:175], v[44:47]
	v_mfma_f32_16x16x32_bf16 v[32:35], v[100:103], v[180:183], v[32:35]
	v_mfma_f32_16x16x32_bf16 v[28:31], v[108:111], v[180:183], v[28:31]
	v_mfma_f32_16x16x32_bf16 v[16:19], v[100:103], v[188:191], v[16:19]
	v_mfma_f32_16x16x32_bf16 v[12:15], v[108:111], v[188:191], v[12:15]
	v_mfma_f32_16x16x32_bf16 v[64:67], v[104:107], v[168:171], v[64:67]
	v_mfma_f32_16x16x32_bf16 v[60:63], v[112:115], v[168:171], v[60:63]
	v_mfma_f32_16x16x32_bf16 v[48:51], v[104:107], v[176:179], v[48:51]
	v_mfma_f32_16x16x32_bf16 v[44:47], v[112:115], v[176:179], v[44:47]
	v_mfma_f32_16x16x32_bf16 v[32:35], v[104:107], v[184:187], v[32:35]
	v_mfma_f32_16x16x32_bf16 v[28:31], v[112:115], v[184:187], v[28:31]
	v_mfma_f32_16x16x32_bf16 v[16:19], v[104:107], v[192:195], v[16:19]
	v_mfma_f32_16x16x32_bf16 v[12:15], v[112:115], v[192:195], v[12:15]
	s_setprio 0
	s_setprio 1
	v_mfma_f32_16x16x32_bf16 v[56:59], v[132:135], v[164:167], v[56:59]
	v_mfma_f32_16x16x32_bf16 v[52:55], v[140:143], v[164:167], v[52:55]
	v_mfma_f32_16x16x32_bf16 v[40:43], v[132:135], v[172:175], v[40:43]
	v_mfma_f32_16x16x32_bf16 v[36:39], v[140:143], v[172:175], v[36:39]
	v_mfma_f32_16x16x32_bf16 v[24:27], v[132:135], v[180:183], v[24:27]
	v_mfma_f32_16x16x32_bf16 v[20:23], v[140:143], v[180:183], v[20:23]
	v_mfma_f32_16x16x32_bf16 v[8:11], v[132:135], v[188:191], v[8:11]
	v_mfma_f32_16x16x32_bf16 v[4:7], v[140:143], v[188:191], v[4:7]
	v_mfma_f32_16x16x32_bf16 v[56:59], v[136:139], v[168:171], v[56:59]
	v_mfma_f32_16x16x32_bf16 v[52:55], v[144:147], v[168:171], v[52:55]
	v_mfma_f32_16x16x32_bf16 v[40:43], v[136:139], v[176:179], v[40:43]
	v_mfma_f32_16x16x32_bf16 v[36:39], v[144:147], v[176:179], v[36:39]
	v_mfma_f32_16x16x32_bf16 v[24:27], v[136:139], v[184:187], v[24:27]
	v_mfma_f32_16x16x32_bf16 v[20:23], v[144:147], v[184:187], v[20:23]
	v_mfma_f32_16x16x32_bf16 v[8:11], v[136:139], v[192:195], v[8:11]
	v_mfma_f32_16x16x32_bf16 v[4:7], v[144:147], v[192:195], v[4:7]
	s_barrier
	s_setprio 0
	s_add_u32 s26, s26, 0x100
	s_addc_u32 s27, s27, 0
	s_add_u32 s19, s19, 0x100
	s_addc_u32 s20, s20, 0
	s_cmp_ge_i32 s22, s78
	s_mov_b32 s21, s22
	s_cbranch_scc1 .LBB0_812
.LBB0_811:
	s_add_i32 s22, s21, 2
	s_add_u32 s23, s26, 0x80
	s_addc_u32 s28, s27, 0
	s_add_i32 s34, 0, 0x10000
	s_cmp_eq_u32 s81, s21
	s_cselect_b32 s31, s3, s28
	s_cselect_b32 s30, s2, s23
	v_add_u32_e32 v2, s34, v231
	s_cselect_b32 s29, s61, s20
	s_cselect_b32 s28, s60, s19
	s_add_i32 s21, 0, 0x14000
	ds_read_b128 v[100:103], v2
	ds_read_b128 v[104:107], v2 offset:1024
	ds_read_b128 v[108:111], v2 offset:2048
	ds_read_b128 v[112:115], v2 offset:3072
	v_add_u32_e32 v2, s21, v231
	ds_read_b128 v[132:135], v2
	ds_read_b128 v[136:139], v2 offset:1024
	ds_read_b128 v[140:143], v2 offset:2048
	ds_read_b128 v[144:147], v2 offset:3072
	v_lshl_add_u64 v[208:209], s[26:27], 0, v[204:205]
	s_add_i32 m0, s72, 0xc000
	ds_read_b128 v[164:167], v240
	ds_read_b128 v[168:171], v240 offset:1024
	ds_read_b128 v[172:175], v240 offset:2048
	ds_read_b128 v[176:179], v240 offset:3072
	ds_read_b128 v[180:183], v240 offset:4096
	ds_read_b128 v[184:187], v240 offset:5120
	ds_read_b128 v[188:191], v240 offset:6144
	ds_read_b128 v[192:195], v240 offset:7168
	global_load_lds_dwordx4 v[208:209], off
	v_lshl_add_u64 v[208:209], s[26:27], 0, v[206:207]
	s_add_i32 m0, s72, 0xe000
	s_nop 0
	global_load_lds_dwordx4 v[208:209], off
	s_waitcnt vmcnt(8)
	s_waitcnt lgkmcnt(0)
	s_barrier
	s_setprio 1
	v_mfma_f32_16x16x32_bf16 v[160:163], v[100:103], v[164:167], v[160:163]
	v_mfma_f32_16x16x32_bf16 v[156:159], v[108:111], v[164:167], v[156:159]
	v_mfma_f32_16x16x32_bf16 v[128:131], v[100:103], v[172:175], v[128:131]
	v_mfma_f32_16x16x32_bf16 v[124:127], v[108:111], v[172:175], v[124:127]
	v_mfma_f32_16x16x32_bf16 v[96:99], v[100:103], v[180:183], v[96:99]
	v_mfma_f32_16x16x32_bf16 v[92:95], v[108:111], v[180:183], v[92:95]
	v_mfma_f32_16x16x32_bf16 v[80:83], v[100:103], v[188:191], v[80:83]
	v_mfma_f32_16x16x32_bf16 v[76:79], v[108:111], v[188:191], v[76:79]
	v_mfma_f32_16x16x32_bf16 v[160:163], v[104:107], v[168:171], v[160:163]
	v_mfma_f32_16x16x32_bf16 v[156:159], v[112:115], v[168:171], v[156:159]
	v_mfma_f32_16x16x32_bf16 v[128:131], v[104:107], v[176:179], v[128:131]
	v_mfma_f32_16x16x32_bf16 v[124:127], v[112:115], v[176:179], v[124:127]
	v_mfma_f32_16x16x32_bf16 v[96:99], v[104:107], v[184:187], v[96:99]
	v_mfma_f32_16x16x32_bf16 v[92:95], v[112:115], v[184:187], v[92:95]
	v_mfma_f32_16x16x32_bf16 v[80:83], v[104:107], v[192:195], v[80:83]
	v_mfma_f32_16x16x32_bf16 v[76:79], v[112:115], v[192:195], v[76:79]
	s_setprio 0
	s_setprio 1
	v_mfma_f32_16x16x32_bf16 v[152:155], v[132:135], v[164:167], v[152:155]
	v_mfma_f32_16x16x32_bf16 v[148:151], v[140:143], v[164:167], v[148:151]
	v_mfma_f32_16x16x32_bf16 v[120:123], v[132:135], v[172:175], v[120:123]
	v_mfma_f32_16x16x32_bf16 v[116:119], v[140:143], v[172:175], v[116:119]
	v_mfma_f32_16x16x32_bf16 v[88:91], v[132:135], v[180:183], v[88:91]
	v_mfma_f32_16x16x32_bf16 v[84:87], v[140:143], v[180:183], v[84:87]
	v_mfma_f32_16x16x32_bf16 v[72:75], v[132:135], v[188:191], v[72:75]
	v_mfma_f32_16x16x32_bf16 v[68:71], v[140:143], v[188:191], v[68:71]
	v_mfma_f32_16x16x32_bf16 v[152:155], v[136:139], v[168:171], v[152:155]
	v_mfma_f32_16x16x32_bf16 v[148:151], v[144:147], v[168:171], v[148:151]
	v_mfma_f32_16x16x32_bf16 v[120:123], v[136:139], v[176:179], v[120:123]
	v_mfma_f32_16x16x32_bf16 v[116:119], v[144:147], v[176:179], v[116:119]
	v_mfma_f32_16x16x32_bf16 v[88:91], v[136:139], v[184:187], v[88:91]
	v_mfma_f32_16x16x32_bf16 v[84:87], v[144:147], v[184:187], v[84:87]
	v_mfma_f32_16x16x32_bf16 v[72:75], v[136:139], v[192:195], v[72:75]
	v_mfma_f32_16x16x32_bf16 v[68:71], v[144:147], v[192:195], v[68:71]
	s_barrier
	s_setprio 0
	s_add_i32 s23, s34, s69
	v_lshl_add_u64 v[208:209], s[28:29], 0, v[200:201]
	s_mov_b32 m0, s23
	ds_read_b128 v[164:167], v240 offset:16384
	ds_read_b128 v[168:171], v240 offset:17408
	ds_read_b128 v[172:175], v240 offset:18432
	ds_read_b128 v[176:179], v240 offset:19456
	ds_read_b128 v[180:183], v240 offset:20480
	ds_read_b128 v[184:187], v240 offset:21504
	ds_read_b128 v[188:191], v240 offset:22528
	ds_read_b128 v[192:195], v240 offset:23552
	global_load_lds_dwordx4 v[208:209], off
	s_add_i32 m0, s23, 0x2000
	v_lshl_add_u64 v[210:211], s[28:29], 0, v[196:197]
	s_add_u32 s28, s28, s6
	s_addc_u32 s29, s29, s7
	s_add_i32 s21, s21, s69
	global_load_lds_dwordx4 v[210:211], off
	v_lshl_add_u64 v[218:219], s[28:29], 0, v[200:201]
	s_mov_b32 m0, s21
	v_lshl_add_u64 v[220:221], s[28:29], 0, v[196:197]
	global_load_lds_dwordx4 v[218:219], off
	s_add_i32 m0, s21, 0x2000
	v_lshl_add_u64 v[222:223], s[30:31], 0, v[202:203]
	global_load_lds_dwordx4 v[220:221], off
	s_mov_b32 m0, s72
	v_lshl_add_u64 v[224:225], s[30:31], 0, v[198:199]
	global_load_lds_dwordx4 v[222:223], off
	s_mov_b32 m0, s73
	s_nop 0
	global_load_lds_dwordx4 v[224:225], off
	s_waitcnt vmcnt(8)
	s_waitcnt lgkmcnt(0)
	s_barrier
	s_setprio 1
	v_mfma_f32_16x16x32_bf16 v[64:67], v[100:103], v[164:167], v[64:67]
	v_mfma_f32_16x16x32_bf16 v[60:63], v[108:111], v[164:167], v[60:63]
	v_mfma_f32_16x16x32_bf16 v[48:51], v[100:103], v[172:175], v[48:51]
	v_mfma_f32_16x16x32_bf16 v[44:47], v[108:111], v[172:175], v[44:47]
	v_mfma_f32_16x16x32_bf16 v[32:35], v[100:103], v[180:183], v[32:35]
	v_mfma_f32_16x16x32_bf16 v[28:31], v[108:111], v[180:183], v[28:31]
	v_mfma_f32_16x16x32_bf16 v[16:19], v[100:103], v[188:191], v[16:19]
	v_mfma_f32_16x16x32_bf16 v[12:15], v[108:111], v[188:191], v[12:15]
	v_mfma_f32_16x16x32_bf16 v[64:67], v[104:107], v[168:171], v[64:67]
	v_mfma_f32_16x16x32_bf16 v[60:63], v[112:115], v[168:171], v[60:63]
	v_mfma_f32_16x16x32_bf16 v[48:51], v[104:107], v[176:179], v[48:51]
	v_mfma_f32_16x16x32_bf16 v[44:47], v[112:115], v[176:179], v[44:47]
	v_mfma_f32_16x16x32_bf16 v[32:35], v[104:107], v[184:187], v[32:35]
	v_mfma_f32_16x16x32_bf16 v[28:31], v[112:115], v[184:187], v[28:31]
	v_mfma_f32_16x16x32_bf16 v[16:19], v[104:107], v[192:195], v[16:19]
	v_mfma_f32_16x16x32_bf16 v[12:15], v[112:115], v[192:195], v[12:15]
	s_setprio 0
	s_setprio 1
	v_mfma_f32_16x16x32_bf16 v[56:59], v[132:135], v[164:167], v[56:59]
	v_mfma_f32_16x16x32_bf16 v[52:55], v[140:143], v[164:167], v[52:55]
	v_mfma_f32_16x16x32_bf16 v[40:43], v[132:135], v[172:175], v[40:43]
	v_mfma_f32_16x16x32_bf16 v[36:39], v[140:143], v[172:175], v[36:39]
	v_mfma_f32_16x16x32_bf16 v[24:27], v[132:135], v[180:183], v[24:27]
	v_mfma_f32_16x16x32_bf16 v[20:23], v[140:143], v[180:183], v[20:23]
	v_mfma_f32_16x16x32_bf16 v[8:11], v[132:135], v[188:191], v[8:11]
	v_mfma_f32_16x16x32_bf16 v[4:7], v[140:143], v[188:191], v[4:7]
	v_mfma_f32_16x16x32_bf16 v[56:59], v[136:139], v[168:171], v[56:59]
	v_mfma_f32_16x16x32_bf16 v[52:55], v[144:147], v[168:171], v[52:55]
	v_mfma_f32_16x16x32_bf16 v[40:43], v[136:139], v[176:179], v[40:43]
	v_mfma_f32_16x16x32_bf16 v[36:39], v[144:147], v[176:179], v[36:39]
	v_mfma_f32_16x16x32_bf16 v[24:27], v[136:139], v[184:187], v[24:27]
	v_mfma_f32_16x16x32_bf16 v[20:23], v[144:147], v[184:187], v[20:23]
	v_mfma_f32_16x16x32_bf16 v[8:11], v[136:139], v[192:195], v[8:11]
	v_mfma_f32_16x16x32_bf16 v[4:7], v[144:147], v[192:195], v[4:7]
	s_barrier
	s_setprio 0
	s_add_i32 s21, 0, 0x18000
	v_add_u32_e32 v2, s21, v231
	s_add_i32 s23, 0, 0x1c000
	ds_read_b128 v[100:103], v2
	ds_read_b128 v[104:107], v2 offset:1024
	ds_read_b128 v[108:111], v2 offset:2048
	ds_read_b128 v[112:115], v2 offset:3072
	v_add_u32_e32 v2, s23, v231
	ds_read_b128 v[132:135], v2
	ds_read_b128 v[136:139], v2 offset:1024
	ds_read_b128 v[140:143], v2 offset:2048
	ds_read_b128 v[144:147], v2 offset:3072
	s_add_u32 s28, s30, s6
	s_addc_u32 s29, s31, s7
	s_mov_b32 m0, s74
	v_lshl_add_u64 v[226:227], s[28:29], 0, v[202:203]
	ds_read_b128 v[164:167], v240 offset:32768
	ds_read_b128 v[168:171], v240 offset:33792
	ds_read_b128 v[172:175], v240 offset:34816
	ds_read_b128 v[176:179], v240 offset:35840
	ds_read_b128 v[180:183], v240 offset:36864
	ds_read_b128 v[184:187], v240 offset:37888
	ds_read_b128 v[188:191], v240 offset:38912
	ds_read_b128 v[192:195], v240 offset:39936
	global_load_lds_dwordx4 v[226:227], off
	v_lshl_add_u64 v[226:227], s[28:29], 0, v[198:199]
	s_mov_b32 m0, s75
	s_nop 0
	global_load_lds_dwordx4 v[226:227], off
	s_waitcnt vmcnt(8)
	s_waitcnt lgkmcnt(0)
	s_barrier
	s_setprio 1
	v_mfma_f32_16x16x32_bf16 v[160:163], v[100:103], v[164:167], v[160:163]
	v_mfma_f32_16x16x32_bf16 v[156:159], v[108:111], v[164:167], v[156:159]
	v_mfma_f32_16x16x32_bf16 v[128:131], v[100:103], v[172:175], v[128:131]
	v_mfma_f32_16x16x32_bf16 v[124:127], v[108:111], v[172:175], v[124:127]
	v_mfma_f32_16x16x32_bf16 v[96:99], v[100:103], v[180:183], v[96:99]
	v_mfma_f32_16x16x32_bf16 v[92:95], v[108:111], v[180:183], v[92:95]
	v_mfma_f32_16x16x32_bf16 v[80:83], v[100:103], v[188:191], v[80:83]
	v_mfma_f32_16x16x32_bf16 v[76:79], v[108:111], v[188:191], v[76:79]
	v_mfma_f32_16x16x32_bf16 v[160:163], v[104:107], v[168:171], v[160:163]
	v_mfma_f32_16x16x32_bf16 v[156:159], v[112:115], v[168:171], v[156:159]
	v_mfma_f32_16x16x32_bf16 v[128:131], v[104:107], v[176:179], v[128:131]
	v_mfma_f32_16x16x32_bf16 v[124:127], v[112:115], v[176:179], v[124:127]
	v_mfma_f32_16x16x32_bf16 v[96:99], v[104:107], v[184:187], v[96:99]
	v_mfma_f32_16x16x32_bf16 v[92:95], v[112:115], v[184:187], v[92:95]
	v_mfma_f32_16x16x32_bf16 v[80:83], v[104:107], v[192:195], v[80:83]
	v_mfma_f32_16x16x32_bf16 v[76:79], v[112:115], v[192:195], v[76:79]
	s_setprio 0
	s_setprio 1
	v_mfma_f32_16x16x32_bf16 v[152:155], v[132:135], v[164:167], v[152:155]
	v_mfma_f32_16x16x32_bf16 v[148:151], v[140:143], v[164:167], v[148:151]
	v_mfma_f32_16x16x32_bf16 v[120:123], v[132:135], v[172:175], v[120:123]
	v_mfma_f32_16x16x32_bf16 v[116:119], v[140:143], v[172:175], v[116:119]
	v_mfma_f32_16x16x32_bf16 v[88:91], v[132:135], v[180:183], v[88:91]
	v_mfma_f32_16x16x32_bf16 v[84:87], v[140:143], v[180:183], v[84:87]
	v_mfma_f32_16x16x32_bf16 v[72:75], v[132:135], v[188:191], v[72:75]
	v_mfma_f32_16x16x32_bf16 v[68:71], v[140:143], v[188:191], v[68:71]
	v_mfma_f32_16x16x32_bf16 v[152:155], v[136:139], v[168:171], v[152:155]
	v_mfma_f32_16x16x32_bf16 v[148:151], v[144:147], v[168:171], v[148:151]
	v_mfma_f32_16x16x32_bf16 v[120:123], v[136:139], v[176:179], v[120:123]
	v_mfma_f32_16x16x32_bf16 v[116:119], v[144:147], v[176:179], v[116:119]
	v_mfma_f32_16x16x32_bf16 v[88:91], v[136:139], v[184:187], v[88:91]
	v_mfma_f32_16x16x32_bf16 v[84:87], v[144:147], v[184:187], v[84:87]
	v_mfma_f32_16x16x32_bf16 v[72:75], v[136:139], v[192:195], v[72:75]
	v_mfma_f32_16x16x32_bf16 v[68:71], v[144:147], v[192:195], v[68:71]
	s_barrier
	s_setprio 0
	s_add_i32 s21, s21, s69
	v_lshl_add_u64 v[208:209], v[208:209], 0, s[24:25]
	s_mov_b32 m0, s21
	ds_read_b128 v[164:167], v240 offset:49152
	ds_read_b128 v[168:171], v240 offset:50176
	ds_read_b128 v[172:175], v240 offset:51200
	ds_read_b128 v[176:179], v240 offset:52224
	ds_read_b128 v[180:183], v240 offset:53248
	ds_read_b128 v[184:187], v240 offset:54272
	ds_read_b128 v[188:191], v240 offset:55296
	ds_read_b128 v[192:195], v240 offset:56320
	global_load_lds_dwordx4 v[208:209], off
	v_lshl_add_u64 v[208:209], v[210:211], 0, s[24:25]
	s_add_i32 m0, s21, 0x2000
	s_add_i32 s21, s23, s69
	global_load_lds_dwordx4 v[208:209], off
	v_lshl_add_u64 v[208:209], v[218:219], 0, s[24:25]
	s_mov_b32 m0, s21
	s_nop 0
	global_load_lds_dwordx4 v[208:209], off
	v_lshl_add_u64 v[208:209], v[220:221], 0, s[24:25]
	s_add_i32 m0, s21, 0x2000
	s_nop 0
	global_load_lds_dwordx4 v[208:209], off
	v_lshl_add_u64 v[208:209], v[222:223], 0, s[24:25]
	s_mov_b32 m0, s79
	s_nop 0
	global_load_lds_dwordx4 v[208:209], off
	v_lshl_add_u64 v[208:209], v[224:225], 0, s[24:25]
	s_mov_b32 m0, s80
	s_nop 0
	global_load_lds_dwordx4 v[208:209], off
	s_waitcnt vmcnt(8)
	s_waitcnt lgkmcnt(0)
	s_barrier
	s_setprio 1
	v_mfma_f32_16x16x32_bf16 v[64:67], v[100:103], v[164:167], v[64:67]
	v_mfma_f32_16x16x32_bf16 v[60:63], v[108:111], v[164:167], v[60:63]
	v_mfma_f32_16x16x32_bf16 v[48:51], v[100:103], v[172:175], v[48:51]
	v_mfma_f32_16x16x32_bf16 v[44:47], v[108:111], v[172:175], v[44:47]
	v_mfma_f32_16x16x32_bf16 v[32:35], v[100:103], v[180:183], v[32:35]
	v_mfma_f32_16x16x32_bf16 v[28:31], v[108:111], v[180:183], v[28:31]
	v_mfma_f32_16x16x32_bf16 v[16:19], v[100:103], v[188:191], v[16:19]
	v_mfma_f32_16x16x32_bf16 v[12:15], v[108:111], v[188:191], v[12:15]
	v_mfma_f32_16x16x32_bf16 v[64:67], v[104:107], v[168:171], v[64:67]
	v_mfma_f32_16x16x32_bf16 v[60:63], v[112:115], v[168:171], v[60:63]
	v_mfma_f32_16x16x32_bf16 v[48:51], v[104:107], v[176:179], v[48:51]
	v_mfma_f32_16x16x32_bf16 v[44:47], v[112:115], v[176:179], v[44:47]
	v_mfma_f32_16x16x32_bf16 v[32:35], v[104:107], v[184:187], v[32:35]
	v_mfma_f32_16x16x32_bf16 v[28:31], v[112:115], v[184:187], v[28:31]
	v_mfma_f32_16x16x32_bf16 v[16:19], v[104:107], v[192:195], v[16:19]
	v_mfma_f32_16x16x32_bf16 v[12:15], v[112:115], v[192:195], v[12:15]
	s_setprio 0
	s_setprio 1
	v_mfma_f32_16x16x32_bf16 v[56:59], v[132:135], v[164:167], v[56:59]
	v_mfma_f32_16x16x32_bf16 v[52:55], v[140:143], v[164:167], v[52:55]
	v_mfma_f32_16x16x32_bf16 v[40:43], v[132:135], v[172:175], v[40:43]
	v_mfma_f32_16x16x32_bf16 v[36:39], v[140:143], v[172:175], v[36:39]
	v_mfma_f32_16x16x32_bf16 v[24:27], v[132:135], v[180:183], v[24:27]
	v_mfma_f32_16x16x32_bf16 v[20:23], v[140:143], v[180:183], v[20:23]
	v_mfma_f32_16x16x32_bf16 v[8:11], v[132:135], v[188:191], v[8:11]
	v_mfma_f32_16x16x32_bf16 v[4:7], v[140:143], v[188:191], v[4:7]
	v_mfma_f32_16x16x32_bf16 v[56:59], v[136:139], v[168:171], v[56:59]
	v_mfma_f32_16x16x32_bf16 v[52:55], v[144:147], v[168:171], v[52:55]
	v_mfma_f32_16x16x32_bf16 v[40:43], v[136:139], v[176:179], v[40:43]
	v_mfma_f32_16x16x32_bf16 v[36:39], v[144:147], v[176:179], v[36:39]
	v_mfma_f32_16x16x32_bf16 v[24:27], v[136:139], v[184:187], v[24:27]
	v_mfma_f32_16x16x32_bf16 v[20:23], v[144:147], v[184:187], v[20:23]
	v_mfma_f32_16x16x32_bf16 v[8:11], v[136:139], v[192:195], v[8:11]
	v_mfma_f32_16x16x32_bf16 v[4:7], v[144:147], v[192:195], v[4:7]
	s_barrier
	s_setprio 0
	s_add_u32 s26, s26, 0x100
	s_addc_u32 s27, s27, 0
	s_add_u32 s19, s19, 0x100
	s_addc_u32 s20, s20, 0
	s_cmp_ge_i32 s22, s78
	s_mov_b32 s21, s22
	s_cbranch_scc0 .LBB0_811

.LBB0_1302:
	s_andn2_b64 vcc, exec, s[42:43]
	s_cbranch_vccnz .LBB0_1305
	s_add_u32 s2, s30, 0x80
	s_addc_u32 s3, s31, 0
	s_add_u32 s19, s26, 0x100
	s_addc_u32 s20, s27, 0
	s_mov_b32 s21, 0
	s_add_i32 s22, s21, 2
	s_add_u32 s23, s2, 0x80
	s_addc_u32 s26, s3, 0
	s_add_i32 s30, 0, 0x10000
	s_cmp_eq_u32 s64, s21
	s_cselect_b32 s27, s47, s26
	s_cselect_b32 s26, s46, s23
	s_cselect_b32 s29, s49, s20
	s_cselect_b32 s28, s48, s19
	s_add_i32 s21, 0, 0x14000
	v_add_u32_e32 v144, s30, v220
	v_add_u32_e32 v160, s21, v220
	ds_read_b128 v[132:135], v144
	ds_read_b128 v[136:139], v144 offset:1024
	ds_read_b128 v[140:143], v144 offset:2048
	ds_read_b128 v[144:147], v144 offset:3072
	ds_read_b128 v[148:151], v160
	ds_read_b128 v[152:155], v160 offset:1024
	ds_read_b128 v[156:159], v160 offset:2048
	ds_read_b128 v[160:163], v160 offset:3072
	v_lshl_add_u64 v[210:211], s[2:3], 0, v[198:199]
	s_add_i32 m0, s56, 0xc000
	ds_read_b128 v[164:167], v221
	ds_read_b128 v[168:171], v221 offset:1024
	ds_read_b128 v[172:175], v221 offset:2048
	ds_read_b128 v[176:179], v221 offset:3072
	ds_read_b128 v[180:183], v221 offset:4096
	ds_read_b128 v[184:187], v221 offset:5120
	ds_read_b128 v[202:205], v221 offset:6144
	ds_read_b128 v[206:209], v221 offset:7168
	global_load_lds_dwordx4 v[210:211], off
	v_lshl_add_u64 v[210:211], s[2:3], 0, v[200:201]
	s_add_i32 m0, s56, 0xe000
	s_nop 0
	global_load_lds_dwordx4 v[210:211], off
	s_waitcnt vmcnt(8)
	s_waitcnt lgkmcnt(0)
	s_barrier
	s_setprio 1
	v_mfma_f32_16x16x32_bf16 v[124:127], v[132:135], v[164:167], 0
	v_mfma_f32_16x16x32_bf16 v[128:131], v[140:143], v[164:167], 0
	v_mfma_f32_16x16x32_bf16 v[112:115], v[132:135], v[172:175], 0
	v_mfma_f32_16x16x32_bf16 v[108:111], v[140:143], v[172:175], 0
	v_mfma_f32_16x16x32_bf16 v[96:99], v[132:135], v[180:183], 0
	v_mfma_f32_16x16x32_bf16 v[92:95], v[140:143], v[180:183], 0
	v_mfma_f32_16x16x32_bf16 v[80:83], v[132:135], v[202:205], 0
	v_mfma_f32_16x16x32_bf16 v[76:79], v[140:143], v[202:205], 0
	v_mfma_f32_16x16x32_bf16 v[124:127], v[136:139], v[168:171], v[124:127]
	v_mfma_f32_16x16x32_bf16 v[128:131], v[144:147], v[168:171], v[128:131]
	v_mfma_f32_16x16x32_bf16 v[112:115], v[136:139], v[176:179], v[112:115]
	v_mfma_f32_16x16x32_bf16 v[108:111], v[144:147], v[176:179], v[108:111]
	v_mfma_f32_16x16x32_bf16 v[96:99], v[136:139], v[184:187], v[96:99]
	v_mfma_f32_16x16x32_bf16 v[92:95], v[144:147], v[184:187], v[92:95]
	v_mfma_f32_16x16x32_bf16 v[80:83], v[136:139], v[206:209], v[80:83]
	v_mfma_f32_16x16x32_bf16 v[76:79], v[144:147], v[206:209], v[76:79]
	s_setprio 0
	s_setprio 1
	v_mfma_f32_16x16x32_bf16 v[120:123], v[148:151], v[164:167], 0
	v_mfma_f32_16x16x32_bf16 v[116:119], v[156:159], v[164:167], 0
	v_mfma_f32_16x16x32_bf16 v[104:107], v[148:151], v[172:175], 0
	v_mfma_f32_16x16x32_bf16 v[100:103], v[156:159], v[172:175], 0
	v_mfma_f32_16x16x32_bf16 v[88:91], v[148:151], v[180:183], 0
	v_mfma_f32_16x16x32_bf16 v[84:87], v[156:159], v[180:183], 0
	v_mfma_f32_16x16x32_bf16 v[72:75], v[148:151], v[202:205], 0
	v_mfma_f32_16x16x32_bf16 v[68:71], v[156:159], v[202:205], 0
	v_mfma_f32_16x16x32_bf16 v[120:123], v[152:155], v[168:171], v[120:123]
	v_mfma_f32_16x16x32_bf16 v[116:119], v[160:163], v[168:171], v[116:119]
	v_mfma_f32_16x16x32_bf16 v[104:107], v[152:155], v[176:179], v[104:107]
	v_mfma_f32_16x16x32_bf16 v[100:103], v[160:163], v[176:179], v[100:103]
	v_mfma_f32_16x16x32_bf16 v[88:91], v[152:155], v[184:187], v[88:91]
	v_mfma_f32_16x16x32_bf16 v[84:87], v[160:163], v[184:187], v[84:87]
	v_mfma_f32_16x16x32_bf16 v[72:75], v[152:155], v[206:209], v[72:75]
	v_mfma_f32_16x16x32_bf16 v[68:71], v[160:163], v[206:209], v[68:71]
	s_barrier
	s_setprio 0
	s_add_i32 s23, s30, s55
	v_lshl_add_u64 v[210:211], s[28:29], 0, v[2:3]
	s_mov_b32 m0, s23
	ds_read_b128 v[164:167], v221 offset:16384
	ds_read_b128 v[168:171], v221 offset:17408
	ds_read_b128 v[172:175], v221 offset:18432
	ds_read_b128 v[176:179], v221 offset:19456
	ds_read_b128 v[180:183], v221 offset:20480
	ds_read_b128 v[184:187], v221 offset:21504
	ds_read_b128 v[202:205], v221 offset:22528
	ds_read_b128 v[206:209], v221 offset:23552
	global_load_lds_dwordx4 v[210:211], off
	s_add_i32 m0, s23, 0x2000
	v_lshl_add_u64 v[212:213], s[28:29], 0, v[188:189]
	s_add_u32 s28, s28, s8
	s_addc_u32 s29, s29, s9
	s_add_i32 s21, s21, s55
	global_load_lds_dwordx4 v[212:213], off
	v_lshl_add_u64 v[214:215], s[28:29], 0, v[2:3]
	s_mov_b32 m0, s21
	v_lshl_add_u64 v[222:223], s[28:29], 0, v[188:189]
	global_load_lds_dwordx4 v[214:215], off
	s_add_i32 m0, s21, 0x2000
	v_lshl_add_u64 v[224:225], s[26:27], 0, v[192:193]
	global_load_lds_dwordx4 v[222:223], off
	s_mov_b32 m0, s56
	v_lshl_add_u64 v[226:227], s[26:27], 0, v[190:191]
	global_load_lds_dwordx4 v[224:225], off
	s_mov_b32 m0, s57
	s_nop 0
	global_load_lds_dwordx4 v[226:227], off
	s_waitcnt vmcnt(8)
	s_waitcnt lgkmcnt(0)
	s_barrier
	s_setprio 1
	v_mfma_f32_16x16x32_bf16 v[64:67], v[132:135], v[164:167], 0
	v_mfma_f32_16x16x32_bf16 v[60:63], v[140:143], v[164:167], 0
	v_mfma_f32_16x16x32_bf16 v[48:51], v[132:135], v[172:175], 0
	v_mfma_f32_16x16x32_bf16 v[44:47], v[140:143], v[172:175], 0
	v_mfma_f32_16x16x32_bf16 v[32:35], v[132:135], v[180:183], 0
	v_mfma_f32_16x16x32_bf16 v[28:31], v[140:143], v[180:183], 0
	v_mfma_f32_16x16x32_bf16 v[16:19], v[132:135], v[202:205], 0
	v_mfma_f32_16x16x32_bf16 v[12:15], v[140:143], v[202:205], 0
	v_mfma_f32_16x16x32_bf16 v[64:67], v[136:139], v[168:171], v[64:67]
	v_mfma_f32_16x16x32_bf16 v[60:63], v[144:147], v[168:171], v[60:63]
	v_mfma_f32_16x16x32_bf16 v[48:51], v[136:139], v[176:179], v[48:51]
	v_mfma_f32_16x16x32_bf16 v[44:47], v[144:147], v[176:179], v[44:47]
	v_mfma_f32_16x16x32_bf16 v[32:35], v[136:139], v[184:187], v[32:35]
	v_mfma_f32_16x16x32_bf16 v[28:31], v[144:147], v[184:187], v[28:31]
	v_mfma_f32_16x16x32_bf16 v[16:19], v[136:139], v[206:209], v[16:19]
	v_mfma_f32_16x16x32_bf16 v[12:15], v[144:147], v[206:209], v[12:15]
	s_setprio 0
	s_setprio 1
	v_mfma_f32_16x16x32_bf16 v[56:59], v[148:151], v[164:167], 0
	v_mfma_f32_16x16x32_bf16 v[52:55], v[156:159], v[164:167], 0
	v_mfma_f32_16x16x32_bf16 v[40:43], v[148:151], v[172:175], 0
	v_mfma_f32_16x16x32_bf16 v[36:39], v[156:159], v[172:175], 0
	v_mfma_f32_16x16x32_bf16 v[24:27], v[148:151], v[180:183], 0
	v_mfma_f32_16x16x32_bf16 v[20:23], v[156:159], v[180:183], 0
	v_mfma_f32_16x16x32_bf16 v[8:11], v[148:151], v[202:205], 0
	v_mfma_f32_16x16x32_bf16 v[4:7], v[156:159], v[202:205], 0
	v_mfma_f32_16x16x32_bf16 v[56:59], v[152:155], v[168:171], v[56:59]
	v_mfma_f32_16x16x32_bf16 v[52:55], v[160:163], v[168:171], v[52:55]
	v_mfma_f32_16x16x32_bf16 v[40:43], v[152:155], v[176:179], v[40:43]
	v_mfma_f32_16x16x32_bf16 v[36:39], v[160:163], v[176:179], v[36:39]
	v_mfma_f32_16x16x32_bf16 v[24:27], v[152:155], v[184:187], v[24:27]
	v_mfma_f32_16x16x32_bf16 v[20:23], v[160:163], v[184:187], v[20:23]
	v_mfma_f32_16x16x32_bf16 v[8:11], v[152:155], v[206:209], v[8:11]
	v_mfma_f32_16x16x32_bf16 v[4:7], v[160:163], v[206:209], v[4:7]
	s_barrier
	s_setprio 0
	s_add_i32 s21, 0, 0x18000
	s_add_i32 s23, 0, 0x1c000
	v_add_u32_e32 v144, s21, v220
	v_add_u32_e32 v160, s23, v220
	ds_read_b128 v[132:135], v144
	ds_read_b128 v[136:139], v144 offset:1024
	ds_read_b128 v[140:143], v144 offset:2048
	ds_read_b128 v[144:147], v144 offset:3072
	ds_read_b128 v[148:151], v160
	ds_read_b128 v[152:155], v160 offset:1024
	ds_read_b128 v[156:159], v160 offset:2048
	ds_read_b128 v[160:163], v160 offset:3072
	s_add_u32 s26, s26, s8
	s_addc_u32 s27, s27, s9
	s_mov_b32 m0, s58
	v_lshl_add_u64 v[228:229], s[26:27], 0, v[192:193]
	ds_read_b128 v[164:167], v221 offset:32768
	ds_read_b128 v[168:171], v221 offset:33792
	ds_read_b128 v[172:175], v221 offset:34816
	ds_read_b128 v[176:179], v221 offset:35840
	ds_read_b128 v[180:183], v221 offset:36864
	ds_read_b128 v[184:187], v221 offset:37888
	ds_read_b128 v[202:205], v221 offset:38912
	ds_read_b128 v[206:209], v221 offset:39936
	global_load_lds_dwordx4 v[228:229], off
	v_lshl_add_u64 v[228:229], s[26:27], 0, v[190:191]
	s_mov_b32 m0, s59
	s_nop 0
	global_load_lds_dwordx4 v[228:229], off
	s_waitcnt vmcnt(8)
	s_waitcnt lgkmcnt(0)
	s_barrier
	s_setprio 1
	v_mfma_f32_16x16x32_bf16 v[124:127], v[132:135], v[164:167], v[124:127]
	v_mfma_f32_16x16x32_bf16 v[128:131], v[140:143], v[164:167], v[128:131]
	v_mfma_f32_16x16x32_bf16 v[112:115], v[132:135], v[172:175], v[112:115]
	v_mfma_f32_16x16x32_bf16 v[108:111], v[140:143], v[172:175], v[108:111]
	v_mfma_f32_16x16x32_bf16 v[96:99], v[132:135], v[180:183], v[96:99]
	v_mfma_f32_16x16x32_bf16 v[92:95], v[140:143], v[180:183], v[92:95]
	v_mfma_f32_16x16x32_bf16 v[80:83], v[132:135], v[202:205], v[80:83]
	v_mfma_f32_16x16x32_bf16 v[76:79], v[140:143], v[202:205], v[76:79]
	v_mfma_f32_16x16x32_bf16 v[124:127], v[136:139], v[168:171], v[124:127]
	v_mfma_f32_16x16x32_bf16 v[128:131], v[144:147], v[168:171], v[128:131]
	v_mfma_f32_16x16x32_bf16 v[112:115], v[136:139], v[176:179], v[112:115]
	v_mfma_f32_16x16x32_bf16 v[108:111], v[144:147], v[176:179], v[108:111]
	v_mfma_f32_16x16x32_bf16 v[96:99], v[136:139], v[184:187], v[96:99]
	v_mfma_f32_16x16x32_bf16 v[92:95], v[144:147], v[184:187], v[92:95]
	v_mfma_f32_16x16x32_bf16 v[80:83], v[136:139], v[206:209], v[80:83]
	v_mfma_f32_16x16x32_bf16 v[76:79], v[144:147], v[206:209], v[76:79]
	s_setprio 0
	s_setprio 1
	v_mfma_f32_16x16x32_bf16 v[120:123], v[148:151], v[164:167], v[120:123]
	v_mfma_f32_16x16x32_bf16 v[116:119], v[156:159], v[164:167], v[116:119]
	v_mfma_f32_16x16x32_bf16 v[104:107], v[148:151], v[172:175], v[104:107]
	v_mfma_f32_16x16x32_bf16 v[100:103], v[156:159], v[172:175], v[100:103]
	v_mfma_f32_16x16x32_bf16 v[88:91], v[148:151], v[180:183], v[88:91]
	v_mfma_f32_16x16x32_bf16 v[84:87], v[156:159], v[180:183], v[84:87]
	v_mfma_f32_16x16x32_bf16 v[72:75], v[148:151], v[202:205], v[72:75]
	v_mfma_f32_16x16x32_bf16 v[68:71], v[156:159], v[202:205], v[68:71]
	v_mfma_f32_16x16x32_bf16 v[120:123], v[152:155], v[168:171], v[120:123]
	v_mfma_f32_16x16x32_bf16 v[116:119], v[160:163], v[168:171], v[116:119]
	v_mfma_f32_16x16x32_bf16 v[104:107], v[152:155], v[176:179], v[104:107]
	v_mfma_f32_16x16x32_bf16 v[100:103], v[160:163], v[176:179], v[100:103]
	v_mfma_f32_16x16x32_bf16 v[88:91], v[152:155], v[184:187], v[88:91]
	v_mfma_f32_16x16x32_bf16 v[84:87], v[160:163], v[184:187], v[84:87]
	v_mfma_f32_16x16x32_bf16 v[72:75], v[152:155], v[206:209], v[72:75]
	v_mfma_f32_16x16x32_bf16 v[68:71], v[160:163], v[206:209], v[68:71]
	s_barrier
	s_setprio 0
	s_add_i32 s21, s21, s55
	v_lshl_add_u64 v[210:211], v[210:211], 0, s[24:25]
	s_mov_b32 m0, s21
	ds_read_b128 v[164:167], v221 offset:49152
	ds_read_b128 v[168:171], v221 offset:50176
	ds_read_b128 v[172:175], v221 offset:51200
	ds_read_b128 v[176:179], v221 offset:52224
	ds_read_b128 v[180:183], v221 offset:53248
	ds_read_b128 v[184:187], v221 offset:54272
	ds_read_b128 v[202:205], v221 offset:55296
	ds_read_b128 v[206:209], v221 offset:56320
	global_load_lds_dwordx4 v[210:211], off
	v_lshl_add_u64 v[210:211], v[212:213], 0, s[24:25]
	s_add_i32 m0, s21, 0x2000
	s_add_i32 s21, s23, s55
	global_load_lds_dwordx4 v[210:211], off
	v_lshl_add_u64 v[210:211], v[214:215], 0, s[24:25]
	s_mov_b32 m0, s21
	s_nop 0
	global_load_lds_dwordx4 v[210:211], off
	v_lshl_add_u64 v[210:211], v[222:223], 0, s[24:25]
	s_add_i32 m0, s21, 0x2000
	s_nop 0
	global_load_lds_dwordx4 v[210:211], off
	v_lshl_add_u64 v[210:211], v[224:225], 0, s[24:25]
	s_mov_b32 m0, s60
	s_nop 0
	global_load_lds_dwordx4 v[210:211], off
	v_lshl_add_u64 v[210:211], v[226:227], 0, s[24:25]
	s_mov_b32 m0, s61
	s_nop 0
	global_load_lds_dwordx4 v[210:211], off
	s_waitcnt vmcnt(8)
	s_waitcnt lgkmcnt(0)
	s_barrier
	s_setprio 1
	v_mfma_f32_16x16x32_bf16 v[64:67], v[132:135], v[164:167], v[64:67]
	v_mfma_f32_16x16x32_bf16 v[60:63], v[140:143], v[164:167], v[60:63]
	v_mfma_f32_16x16x32_bf16 v[48:51], v[132:135], v[172:175], v[48:51]
	v_mfma_f32_16x16x32_bf16 v[44:47], v[140:143], v[172:175], v[44:47]
	v_mfma_f32_16x16x32_bf16 v[32:35], v[132:135], v[180:183], v[32:35]
	v_mfma_f32_16x16x32_bf16 v[28:31], v[140:143], v[180:183], v[28:31]
	v_mfma_f32_16x16x32_bf16 v[16:19], v[132:135], v[202:205], v[16:19]
	v_mfma_f32_16x16x32_bf16 v[12:15], v[140:143], v[202:205], v[12:15]
	v_mfma_f32_16x16x32_bf16 v[64:67], v[136:139], v[168:171], v[64:67]
	v_mfma_f32_16x16x32_bf16 v[60:63], v[144:147], v[168:171], v[60:63]
	v_mfma_f32_16x16x32_bf16 v[48:51], v[136:139], v[176:179], v[48:51]
	v_mfma_f32_16x16x32_bf16 v[44:47], v[144:147], v[176:179], v[44:47]
	v_mfma_f32_16x16x32_bf16 v[32:35], v[136:139], v[184:187], v[32:35]
	v_mfma_f32_16x16x32_bf16 v[28:31], v[144:147], v[184:187], v[28:31]
	v_mfma_f32_16x16x32_bf16 v[16:19], v[136:139], v[206:209], v[16:19]
	v_mfma_f32_16x16x32_bf16 v[12:15], v[144:147], v[206:209], v[12:15]
	s_setprio 0
	s_setprio 1
	v_mfma_f32_16x16x32_bf16 v[56:59], v[148:151], v[164:167], v[56:59]
	v_mfma_f32_16x16x32_bf16 v[52:55], v[156:159], v[164:167], v[52:55]
	v_mfma_f32_16x16x32_bf16 v[40:43], v[148:151], v[172:175], v[40:43]
	v_mfma_f32_16x16x32_bf16 v[36:39], v[156:159], v[172:175], v[36:39]
	v_mfma_f32_16x16x32_bf16 v[24:27], v[148:151], v[180:183], v[24:27]
	v_mfma_f32_16x16x32_bf16 v[20:23], v[156:159], v[180:183], v[20:23]
	v_mfma_f32_16x16x32_bf16 v[8:11], v[148:151], v[202:205], v[8:11]
	v_mfma_f32_16x16x32_bf16 v[4:7], v[156:159], v[202:205], v[4:7]
	v_mfma_f32_16x16x32_bf16 v[56:59], v[152:155], v[168:171], v[56:59]
	v_mfma_f32_16x16x32_bf16 v[52:55], v[160:163], v[168:171], v[52:55]
	v_mfma_f32_16x16x32_bf16 v[40:43], v[152:155], v[176:179], v[40:43]
	v_mfma_f32_16x16x32_bf16 v[36:39], v[160:163], v[176:179], v[36:39]
	v_mfma_f32_16x16x32_bf16 v[24:27], v[152:155], v[184:187], v[24:27]
	v_mfma_f32_16x16x32_bf16 v[20:23], v[160:163], v[184:187], v[20:23]
	v_mfma_f32_16x16x32_bf16 v[8:11], v[152:155], v[206:209], v[8:11]
	v_mfma_f32_16x16x32_bf16 v[4:7], v[160:163], v[206:209], v[4:7]
	s_barrier
	s_setprio 0
	s_add_u32 s2, s2, 0x100
	s_addc_u32 s3, s3, 0
	s_add_u32 s19, s19, 0x100
	s_addc_u32 s20, s20, 0
	s_cmp_ge_i32 s22, s62
	s_mov_b32 s21, s22
	s_cbranch_scc1 .LBB0_1305
.LBB0_1304:
	s_add_i32 s22, s21, 2
	s_add_u32 s23, s2, 0x80
	s_addc_u32 s26, s3, 0
	s_add_i32 s30, 0, 0x10000
	s_cmp_eq_u32 s64, s21
	s_cselect_b32 s27, s47, s26
	s_cselect_b32 s26, s46, s23
	s_cselect_b32 s29, s49, s20
	s_cselect_b32 s28, s48, s19
	s_add_i32 s21, 0, 0x14000
	v_add_u32_e32 v144, s30, v220
	v_add_u32_e32 v160, s21, v220
	ds_read_b128 v[132:135], v144
	ds_read_b128 v[136:139], v144 offset:1024
	ds_read_b128 v[140:143], v144 offset:2048
	ds_read_b128 v[144:147], v144 offset:3072
	ds_read_b128 v[148:151], v160
	ds_read_b128 v[152:155], v160 offset:1024
	ds_read_b128 v[156:159], v160 offset:2048
	ds_read_b128 v[160:163], v160 offset:3072
	v_lshl_add_u64 v[210:211], s[2:3], 0, v[198:199]
	s_add_i32 m0, s56, 0xc000
	ds_read_b128 v[164:167], v221
	ds_read_b128 v[168:171], v221 offset:1024
	ds_read_b128 v[172:175], v221 offset:2048
	ds_read_b128 v[176:179], v221 offset:3072
	ds_read_b128 v[180:183], v221 offset:4096
	ds_read_b128 v[184:187], v221 offset:5120
	ds_read_b128 v[202:205], v221 offset:6144
	ds_read_b128 v[206:209], v221 offset:7168
	global_load_lds_dwordx4 v[210:211], off
	v_lshl_add_u64 v[210:211], s[2:3], 0, v[200:201]
	s_add_i32 m0, s56, 0xe000
	s_nop 0
	global_load_lds_dwordx4 v[210:211], off
	s_waitcnt vmcnt(8)
	s_waitcnt lgkmcnt(0)
	s_barrier
	s_setprio 1
	v_mfma_f32_16x16x32_bf16 v[124:127], v[132:135], v[164:167], v[124:127]
	v_mfma_f32_16x16x32_bf16 v[128:131], v[140:143], v[164:167], v[128:131]
	v_mfma_f32_16x16x32_bf16 v[112:115], v[132:135], v[172:175], v[112:115]
	v_mfma_f32_16x16x32_bf16 v[108:111], v[140:143], v[172:175], v[108:111]
	v_mfma_f32_16x16x32_bf16 v[96:99], v[132:135], v[180:183], v[96:99]
	v_mfma_f32_16x16x32_bf16 v[92:95], v[140:143], v[180:183], v[92:95]
	v_mfma_f32_16x16x32_bf16 v[80:83], v[132:135], v[202:205], v[80:83]
	v_mfma_f32_16x16x32_bf16 v[76:79], v[140:143], v[202:205], v[76:79]
	v_mfma_f32_16x16x32_bf16 v[124:127], v[136:139], v[168:171], v[124:127]
	v_mfma_f32_16x16x32_bf16 v[128:131], v[144:147], v[168:171], v[128:131]
	v_mfma_f32_16x16x32_bf16 v[112:115], v[136:139], v[176:179], v[112:115]
	v_mfma_f32_16x16x32_bf16 v[108:111], v[144:147], v[176:179], v[108:111]
	v_mfma_f32_16x16x32_bf16 v[96:99], v[136:139], v[184:187], v[96:99]
	v_mfma_f32_16x16x32_bf16 v[92:95], v[144:147], v[184:187], v[92:95]
	v_mfma_f32_16x16x32_bf16 v[80:83], v[136:139], v[206:209], v[80:83]
	v_mfma_f32_16x16x32_bf16 v[76:79], v[144:147], v[206:209], v[76:79]
	s_setprio 0
	s_setprio 1
	v_mfma_f32_16x16x32_bf16 v[120:123], v[148:151], v[164:167], v[120:123]
	v_mfma_f32_16x16x32_bf16 v[116:119], v[156:159], v[164:167], v[116:119]
	v_mfma_f32_16x16x32_bf16 v[104:107], v[148:151], v[172:175], v[104:107]
	v_mfma_f32_16x16x32_bf16 v[100:103], v[156:159], v[172:175], v[100:103]
	v_mfma_f32_16x16x32_bf16 v[88:91], v[148:151], v[180:183], v[88:91]
	v_mfma_f32_16x16x32_bf16 v[84:87], v[156:159], v[180:183], v[84:87]
	v_mfma_f32_16x16x32_bf16 v[72:75], v[148:151], v[202:205], v[72:75]
	v_mfma_f32_16x16x32_bf16 v[68:71], v[156:159], v[202:205], v[68:71]
	v_mfma_f32_16x16x32_bf16 v[120:123], v[152:155], v[168:171], v[120:123]
	v_mfma_f32_16x16x32_bf16 v[116:119], v[160:163], v[168:171], v[116:119]
	v_mfma_f32_16x16x32_bf16 v[104:107], v[152:155], v[176:179], v[104:107]
	v_mfma_f32_16x16x32_bf16 v[100:103], v[160:163], v[176:179], v[100:103]
	v_mfma_f32_16x16x32_bf16 v[88:91], v[152:155], v[184:187], v[88:91]
	v_mfma_f32_16x16x32_bf16 v[84:87], v[160:163], v[184:187], v[84:87]
	v_mfma_f32_16x16x32_bf16 v[72:75], v[152:155], v[206:209], v[72:75]
	v_mfma_f32_16x16x32_bf16 v[68:71], v[160:163], v[206:209], v[68:71]
	s_barrier
	s_setprio 0
	s_add_i32 s23, s30, s55
	v_lshl_add_u64 v[210:211], s[28:29], 0, v[2:3]
	s_mov_b32 m0, s23
	ds_read_b128 v[164:167], v221 offset:16384
	ds_read_b128 v[168:171], v221 offset:17408
	ds_read_b128 v[172:175], v221 offset:18432
	ds_read_b128 v[176:179], v221 offset:19456
	ds_read_b128 v[180:183], v221 offset:20480
	ds_read_b128 v[184:187], v221 offset:21504
	ds_read_b128 v[202:205], v221 offset:22528
	ds_read_b128 v[206:209], v221 offset:23552
	global_load_lds_dwordx4 v[210:211], off
	s_add_i32 m0, s23, 0x2000
	v_lshl_add_u64 v[212:213], s[28:29], 0, v[188:189]
	s_add_u32 s28, s28, s8
	s_addc_u32 s29, s29, s9
	s_add_i32 s21, s21, s55
	global_load_lds_dwordx4 v[212:213], off
	v_lshl_add_u64 v[214:215], s[28:29], 0, v[2:3]
	s_mov_b32 m0, s21
	v_lshl_add_u64 v[222:223], s[28:29], 0, v[188:189]
	global_load_lds_dwordx4 v[214:215], off
	s_add_i32 m0, s21, 0x2000
	v_lshl_add_u64 v[224:225], s[26:27], 0, v[192:193]
	global_load_lds_dwordx4 v[222:223], off
	s_mov_b32 m0, s56
	v_lshl_add_u64 v[226:227], s[26:27], 0, v[190:191]
	global_load_lds_dwordx4 v[224:225], off
	s_mov_b32 m0, s57
	s_nop 0
	global_load_lds_dwordx4 v[226:227], off
	s_waitcnt vmcnt(8)
	s_waitcnt lgkmcnt(0)
	s_barrier
	s_setprio 1
	v_mfma_f32_16x16x32_bf16 v[64:67], v[132:135], v[164:167], v[64:67]
	v_mfma_f32_16x16x32_bf16 v[60:63], v[140:143], v[164:167], v[60:63]
	v_mfma_f32_16x16x32_bf16 v[48:51], v[132:135], v[172:175], v[48:51]
	v_mfma_f32_16x16x32_bf16 v[44:47], v[140:143], v[172:175], v[44:47]
	v_mfma_f32_16x16x32_bf16 v[32:35], v[132:135], v[180:183], v[32:35]
	v_mfma_f32_16x16x32_bf16 v[28:31], v[140:143], v[180:183], v[28:31]
	v_mfma_f32_16x16x32_bf16 v[16:19], v[132:135], v[202:205], v[16:19]
	v_mfma_f32_16x16x32_bf16 v[12:15], v[140:143], v[202:205], v[12:15]
	v_mfma_f32_16x16x32_bf16 v[64:67], v[136:139], v[168:171], v[64:67]
	v_mfma_f32_16x16x32_bf16 v[60:63], v[144:147], v[168:171], v[60:63]
	v_mfma_f32_16x16x32_bf16 v[48:51], v[136:139], v[176:179], v[48:51]
	v_mfma_f32_16x16x32_bf16 v[44:47], v[144:147], v[176:179], v[44:47]
	v_mfma_f32_16x16x32_bf16 v[32:35], v[136:139], v[184:187], v[32:35]
	v_mfma_f32_16x16x32_bf16 v[28:31], v[144:147], v[184:187], v[28:31]
	v_mfma_f32_16x16x32_bf16 v[16:19], v[136:139], v[206:209], v[16:19]
	v_mfma_f32_16x16x32_bf16 v[12:15], v[144:147], v[206:209], v[12:15]
	s_setprio 0
	s_setprio 1
	v_mfma_f32_16x16x32_bf16 v[56:59], v[148:151], v[164:167], v[56:59]
	v_mfma_f32_16x16x32_bf16 v[52:55], v[156:159], v[164:167], v[52:55]
	v_mfma_f32_16x16x32_bf16 v[40:43], v[148:151], v[172:175], v[40:43]
	v_mfma_f32_16x16x32_bf16 v[36:39], v[156:159], v[172:175], v[36:39]
	v_mfma_f32_16x16x32_bf16 v[24:27], v[148:151], v[180:183], v[24:27]
	v_mfma_f32_16x16x32_bf16 v[20:23], v[156:159], v[180:183], v[20:23]
	v_mfma_f32_16x16x32_bf16 v[8:11], v[148:151], v[202:205], v[8:11]
	v_mfma_f32_16x16x32_bf16 v[4:7], v[156:159], v[202:205], v[4:7]
	v_mfma_f32_16x16x32_bf16 v[56:59], v[152:155], v[168:171], v[56:59]
	v_mfma_f32_16x16x32_bf16 v[52:55], v[160:163], v[168:171], v[52:55]
	v_mfma_f32_16x16x32_bf16 v[40:43], v[152:155], v[176:179], v[40:43]
	v_mfma_f32_16x16x32_bf16 v[36:39], v[160:163], v[176:179], v[36:39]
	v_mfma_f32_16x16x32_bf16 v[24:27], v[152:155], v[184:187], v[24:27]
	v_mfma_f32_16x16x32_bf16 v[20:23], v[160:163], v[184:187], v[20:23]
	v_mfma_f32_16x16x32_bf16 v[8:11], v[152:155], v[206:209], v[8:11]
	v_mfma_f32_16x16x32_bf16 v[4:7], v[160:163], v[206:209], v[4:7]
	s_barrier
	s_setprio 0
	s_add_i32 s21, 0, 0x18000
	s_add_i32 s23, 0, 0x1c000
	v_add_u32_e32 v144, s21, v220
	v_add_u32_e32 v160, s23, v220
	ds_read_b128 v[132:135], v144
	ds_read_b128 v[136:139], v144 offset:1024
	ds_read_b128 v[140:143], v144 offset:2048
	ds_read_b128 v[144:147], v144 offset:3072
	ds_read_b128 v[148:151], v160
	ds_read_b128 v[152:155], v160 offset:1024
	ds_read_b128 v[156:159], v160 offset:2048
	ds_read_b128 v[160:163], v160 offset:3072
	s_add_u32 s26, s26, s8
	s_addc_u32 s27, s27, s9
	s_mov_b32 m0, s58
	v_lshl_add_u64 v[228:229], s[26:27], 0, v[192:193]
	ds_read_b128 v[164:167], v221 offset:32768
	ds_read_b128 v[168:171], v221 offset:33792
	ds_read_b128 v[172:175], v221 offset:34816
	ds_read_b128 v[176:179], v221 offset:35840
	ds_read_b128 v[180:183], v221 offset:36864
	ds_read_b128 v[184:187], v221 offset:37888
	ds_read_b128 v[202:205], v221 offset:38912
	ds_read_b128 v[206:209], v221 offset:39936
	global_load_lds_dwordx4 v[228:229], off
	v_lshl_add_u64 v[228:229], s[26:27], 0, v[190:191]
	s_mov_b32 m0, s59
	s_nop 0
	global_load_lds_dwordx4 v[228:229], off
	s_waitcnt vmcnt(8)
	s_waitcnt lgkmcnt(0)
	s_barrier
	s_setprio 1
	v_mfma_f32_16x16x32_bf16 v[124:127], v[132:135], v[164:167], v[124:127]
	v_mfma_f32_16x16x32_bf16 v[128:131], v[140:143], v[164:167], v[128:131]
	v_mfma_f32_16x16x32_bf16 v[112:115], v[132:135], v[172:175], v[112:115]
	v_mfma_f32_16x16x32_bf16 v[108:111], v[140:143], v[172:175], v[108:111]
	v_mfma_f32_16x16x32_bf16 v[96:99], v[132:135], v[180:183], v[96:99]
	v_mfma_f32_16x16x32_bf16 v[92:95], v[140:143], v[180:183], v[92:95]
	v_mfma_f32_16x16x32_bf16 v[80:83], v[132:135], v[202:205], v[80:83]
	v_mfma_f32_16x16x32_bf16 v[76:79], v[140:143], v[202:205], v[76:79]
	v_mfma_f32_16x16x32_bf16 v[124:127], v[136:139], v[168:171], v[124:127]
	v_mfma_f32_16x16x32_bf16 v[128:131], v[144:147], v[168:171], v[128:131]
	v_mfma_f32_16x16x32_bf16 v[112:115], v[136:139], v[176:179], v[112:115]
	v_mfma_f32_16x16x32_bf16 v[108:111], v[144:147], v[176:179], v[108:111]
	v_mfma_f32_16x16x32_bf16 v[96:99], v[136:139], v[184:187], v[96:99]
	v_mfma_f32_16x16x32_bf16 v[92:95], v[144:147], v[184:187], v[92:95]
	v_mfma_f32_16x16x32_bf16 v[80:83], v[136:139], v[206:209], v[80:83]
	v_mfma_f32_16x16x32_bf16 v[76:79], v[144:147], v[206:209], v[76:79]
	s_setprio 0
	s_setprio 1
	v_mfma_f32_16x16x32_bf16 v[120:123], v[148:151], v[164:167], v[120:123]
	v_mfma_f32_16x16x32_bf16 v[116:119], v[156:159], v[164:167], v[116:119]
	v_mfma_f32_16x16x32_bf16 v[104:107], v[148:151], v[172:175], v[104:107]
	v_mfma_f32_16x16x32_bf16 v[100:103], v[156:159], v[172:175], v[100:103]
	v_mfma_f32_16x16x32_bf16 v[88:91], v[148:151], v[180:183], v[88:91]
	v_mfma_f32_16x16x32_bf16 v[84:87], v[156:159], v[180:183], v[84:87]
	v_mfma_f32_16x16x32_bf16 v[72:75], v[148:151], v[202:205], v[72:75]
	v_mfma_f32_16x16x32_bf16 v[68:71], v[156:159], v[202:205], v[68:71]
	v_mfma_f32_16x16x32_bf16 v[120:123], v[152:155], v[168:171], v[120:123]
	v_mfma_f32_16x16x32_bf16 v[116:119], v[160:163], v[168:171], v[116:119]
	v_mfma_f32_16x16x32_bf16 v[104:107], v[152:155], v[176:179], v[104:107]
	v_mfma_f32_16x16x32_bf16 v[100:103], v[160:163], v[176:179], v[100:103]
	v_mfma_f32_16x16x32_bf16 v[88:91], v[152:155], v[184:187], v[88:91]
	v_mfma_f32_16x16x32_bf16 v[84:87], v[160:163], v[184:187], v[84:87]
	v_mfma_f32_16x16x32_bf16 v[72:75], v[152:155], v[206:209], v[72:75]
	v_mfma_f32_16x16x32_bf16 v[68:71], v[160:163], v[206:209], v[68:71]
	s_barrier
	s_setprio 0
	s_add_i32 s21, s21, s55
	v_lshl_add_u64 v[210:211], v[210:211], 0, s[24:25]
	s_mov_b32 m0, s21
	ds_read_b128 v[164:167], v221 offset:49152
	ds_read_b128 v[168:171], v221 offset:50176
	ds_read_b128 v[172:175], v221 offset:51200
	ds_read_b128 v[176:179], v221 offset:52224
	ds_read_b128 v[180:183], v221 offset:53248
	ds_read_b128 v[184:187], v221 offset:54272
	ds_read_b128 v[202:205], v221 offset:55296
	ds_read_b128 v[206:209], v221 offset:56320
	global_load_lds_dwordx4 v[210:211], off
	v_lshl_add_u64 v[210:211], v[212:213], 0, s[24:25]
	s_add_i32 m0, s21, 0x2000
	s_add_i32 s21, s23, s55
	global_load_lds_dwordx4 v[210:211], off
	v_lshl_add_u64 v[210:211], v[214:215], 0, s[24:25]
	s_mov_b32 m0, s21
	s_nop 0
	global_load_lds_dwordx4 v[210:211], off
	v_lshl_add_u64 v[210:211], v[222:223], 0, s[24:25]
	s_add_i32 m0, s21, 0x2000
	s_nop 0
	global_load_lds_dwordx4 v[210:211], off
	v_lshl_add_u64 v[210:211], v[224:225], 0, s[24:25]
	s_mov_b32 m0, s60
	s_nop 0
	global_load_lds_dwordx4 v[210:211], off
	v_lshl_add_u64 v[210:211], v[226:227], 0, s[24:25]
	s_mov_b32 m0, s61
	s_nop 0
	global_load_lds_dwordx4 v[210:211], off
	s_waitcnt vmcnt(8)
	s_waitcnt lgkmcnt(0)
	s_barrier
	s_setprio 1
	v_mfma_f32_16x16x32_bf16 v[64:67], v[132:135], v[164:167], v[64:67]
	v_mfma_f32_16x16x32_bf16 v[60:63], v[140:143], v[164:167], v[60:63]
	v_mfma_f32_16x16x32_bf16 v[48:51], v[132:135], v[172:175], v[48:51]
	v_mfma_f32_16x16x32_bf16 v[44:47], v[140:143], v[172:175], v[44:47]
	v_mfma_f32_16x16x32_bf16 v[32:35], v[132:135], v[180:183], v[32:35]
	v_mfma_f32_16x16x32_bf16 v[28:31], v[140:143], v[180:183], v[28:31]
	v_mfma_f32_16x16x32_bf16 v[16:19], v[132:135], v[202:205], v[16:19]
	v_mfma_f32_16x16x32_bf16 v[12:15], v[140:143], v[202:205], v[12:15]
	v_mfma_f32_16x16x32_bf16 v[64:67], v[136:139], v[168:171], v[64:67]
	v_mfma_f32_16x16x32_bf16 v[60:63], v[144:147], v[168:171], v[60:63]
	v_mfma_f32_16x16x32_bf16 v[48:51], v[136:139], v[176:179], v[48:51]
	v_mfma_f32_16x16x32_bf16 v[44:47], v[144:147], v[176:179], v[44:47]
	v_mfma_f32_16x16x32_bf16 v[32:35], v[136:139], v[184:187], v[32:35]
	v_mfma_f32_16x16x32_bf16 v[28:31], v[144:147], v[184:187], v[28:31]
	v_mfma_f32_16x16x32_bf16 v[16:19], v[136:139], v[206:209], v[16:19]
	v_mfma_f32_16x16x32_bf16 v[12:15], v[144:147], v[206:209], v[12:15]
	s_setprio 0
	s_setprio 1
	v_mfma_f32_16x16x32_bf16 v[56:59], v[148:151], v[164:167], v[56:59]
	v_mfma_f32_16x16x32_bf16 v[52:55], v[156:159], v[164:167], v[52:55]
	v_mfma_f32_16x16x32_bf16 v[40:43], v[148:151], v[172:175], v[40:43]
	v_mfma_f32_16x16x32_bf16 v[36:39], v[156:159], v[172:175], v[36:39]
	v_mfma_f32_16x16x32_bf16 v[24:27], v[148:151], v[180:183], v[24:27]
	v_mfma_f32_16x16x32_bf16 v[20:23], v[156:159], v[180:183], v[20:23]
	v_mfma_f32_16x16x32_bf16 v[8:11], v[148:151], v[202:205], v[8:11]
	v_mfma_f32_16x16x32_bf16 v[4:7], v[156:159], v[202:205], v[4:7]
	v_mfma_f32_16x16x32_bf16 v[56:59], v[152:155], v[168:171], v[56:59]
	v_mfma_f32_16x16x32_bf16 v[52:55], v[160:163], v[168:171], v[52:55]
	v_mfma_f32_16x16x32_bf16 v[40:43], v[152:155], v[176:179], v[40:43]
	v_mfma_f32_16x16x32_bf16 v[36:39], v[160:163], v[176:179], v[36:39]
	v_mfma_f32_16x16x32_bf16 v[24:27], v[152:155], v[184:187], v[24:27]
	v_mfma_f32_16x16x32_bf16 v[20:23], v[160:163], v[184:187], v[20:23]
	v_mfma_f32_16x16x32_bf16 v[8:11], v[152:155], v[206:209], v[8:11]
	v_mfma_f32_16x16x32_bf16 v[4:7], v[160:163], v[206:209], v[4:7]
	s_barrier
	s_setprio 0
	s_add_u32 s2, s2, 0x100
	s_addc_u32 s3, s3, 0
	s_add_u32 s19, s19, 0x100
	s_addc_u32 s20, s20, 0
	s_cmp_ge_i32 s22, s62
	s_mov_b32 s21, s22
	s_cbranch_scc0 .LBB0_1304

.LBB0_1327:
	s_andn2_b64 vcc, exec, s[16:17]
	s_waitcnt lgkmcnt(0)
	s_cbranch_vccnz .LBB0_1330
	s_add_u32 s2, s30, 0x80
	s_addc_u32 s3, s31, 0
	s_add_u32 s19, s26, 0x100
	s_addc_u32 s20, s27, 0
	s_mov_b32 s21, 0
	s_add_i32 s22, s21, 2
	s_add_u32 s23, s2, 0x80
	s_addc_u32 s26, s3, 0
	s_add_i32 s30, 0, 0x10000
	s_cmp_eq_u32 s63, s21
	s_cselect_b32 s27, s45, s26
	s_cselect_b32 s26, s44, s23
	s_cselect_b32 s29, s47, s20
	s_cselect_b32 s28, s46, s19
	s_add_i32 s21, 0, 0x14000
	v_add_u32_e32 v154, s30, v166
	v_add_u32_e32 v162, s21, v166
	ds_read_b128 v[132:135], v154
	ds_read_b128 v[136:139], v154 offset:1024
	ds_read_b128 v[140:143], v154 offset:2048
	ds_read_b128 v[154:157], v154 offset:3072
	ds_read_b128 v[158:161], v162
	ds_read_b128 v[170:173], v162 offset:1024
	ds_read_b128 v[174:177], v162 offset:2048
	ds_read_b128 v[178:181], v162 offset:3072
	v_lshl_add_u64 v[162:163], s[2:3], 0, v[150:151]
	s_add_i32 m0, s53, 0xc000
	ds_read_b128 v[182:185], v168
	ds_read_b128 v[186:189], v168 offset:1024
	ds_read_b128 v[190:193], v168 offset:2048
	ds_read_b128 v[194:197], v168 offset:3072
	ds_read_b128 v[198:201], v168 offset:4096
	ds_read_b128 v[202:205], v168 offset:5120
	ds_read_b128 v[206:209], v168 offset:6144
	ds_read_b128 v[218:221], v168 offset:7168
	global_load_lds_dwordx4 v[162:163], off
	v_lshl_add_u64 v[162:163], s[2:3], 0, v[152:153]
	s_add_i32 m0, s53, 0xe000
	s_nop 0
	global_load_lds_dwordx4 v[162:163], off
	s_waitcnt vmcnt(8)
	s_waitcnt lgkmcnt(0)
	s_barrier
	s_setprio 1
	v_mfma_f32_16x16x32_bf16 v[128:131], v[132:135], v[182:185], 0
	v_mfma_f32_16x16x32_bf16 v[124:127], v[140:143], v[182:185], 0
	v_mfma_f32_16x16x32_bf16 v[112:115], v[132:135], v[190:193], 0
	v_mfma_f32_16x16x32_bf16 v[108:111], v[140:143], v[190:193], 0
	v_mfma_f32_16x16x32_bf16 v[96:99], v[132:135], v[198:201], 0
	v_mfma_f32_16x16x32_bf16 v[92:95], v[140:143], v[198:201], 0
	v_mfma_f32_16x16x32_bf16 v[80:83], v[132:135], v[206:209], 0
	v_mfma_f32_16x16x32_bf16 v[76:79], v[140:143], v[206:209], 0
	v_mfma_f32_16x16x32_bf16 v[128:131], v[136:139], v[186:189], v[128:131]
	v_mfma_f32_16x16x32_bf16 v[124:127], v[154:157], v[186:189], v[124:127]
	v_mfma_f32_16x16x32_bf16 v[112:115], v[136:139], v[194:197], v[112:115]
	v_mfma_f32_16x16x32_bf16 v[108:111], v[154:157], v[194:197], v[108:111]
	v_mfma_f32_16x16x32_bf16 v[96:99], v[136:139], v[202:205], v[96:99]
	v_mfma_f32_16x16x32_bf16 v[92:95], v[154:157], v[202:205], v[92:95]
	v_mfma_f32_16x16x32_bf16 v[80:83], v[136:139], v[218:221], v[80:83]
	v_mfma_f32_16x16x32_bf16 v[76:79], v[154:157], v[218:221], v[76:79]
	s_setprio 0
	s_setprio 1
	v_mfma_f32_16x16x32_bf16 v[120:123], v[158:161], v[182:185], 0
	v_mfma_f32_16x16x32_bf16 v[116:119], v[174:177], v[182:185], 0
	v_mfma_f32_16x16x32_bf16 v[104:107], v[158:161], v[190:193], 0
	v_mfma_f32_16x16x32_bf16 v[100:103], v[174:177], v[190:193], 0
	v_mfma_f32_16x16x32_bf16 v[88:91], v[158:161], v[198:201], 0
	v_mfma_f32_16x16x32_bf16 v[84:87], v[174:177], v[198:201], 0
	v_mfma_f32_16x16x32_bf16 v[72:75], v[158:161], v[206:209], 0
	v_mfma_f32_16x16x32_bf16 v[68:71], v[174:177], v[206:209], 0
	v_mfma_f32_16x16x32_bf16 v[120:123], v[170:173], v[186:189], v[120:123]
	v_mfma_f32_16x16x32_bf16 v[116:119], v[178:181], v[186:189], v[116:119]
	v_mfma_f32_16x16x32_bf16 v[104:107], v[170:173], v[194:197], v[104:107]
	v_mfma_f32_16x16x32_bf16 v[100:103], v[178:181], v[194:197], v[100:103]
	v_mfma_f32_16x16x32_bf16 v[88:91], v[170:173], v[202:205], v[88:91]
	v_mfma_f32_16x16x32_bf16 v[84:87], v[178:181], v[202:205], v[84:87]
	v_mfma_f32_16x16x32_bf16 v[72:75], v[170:173], v[218:221], v[72:75]
	v_mfma_f32_16x16x32_bf16 v[68:71], v[178:181], v[218:221], v[68:71]
	s_barrier
	s_setprio 0
	s_add_i32 s23, s30, s52
	v_lshl_add_u64 v[162:163], s[28:29], 0, v[2:3]
	s_mov_b32 m0, s23
	ds_read_b128 v[182:185], v168 offset:16384
	ds_read_b128 v[186:189], v168 offset:17408
	ds_read_b128 v[190:193], v168 offset:18432
	ds_read_b128 v[194:197], v168 offset:19456
	ds_read_b128 v[198:201], v168 offset:20480
	ds_read_b128 v[202:205], v168 offset:21504
	ds_read_b128 v[206:209], v168 offset:22528
	ds_read_b128 v[218:221], v168 offset:23552
	global_load_lds_dwordx4 v[162:163], off
	s_add_i32 m0, s23, 0x2000
	v_lshl_add_u64 v[210:211], s[28:29], 0, v[144:145]
	s_add_u32 s28, s28, s8
	s_addc_u32 s29, s29, s9
	s_add_i32 s21, s21, s52
	global_load_lds_dwordx4 v[210:211], off
	v_lshl_add_u64 v[212:213], s[28:29], 0, v[2:3]
	s_mov_b32 m0, s21
	v_lshl_add_u64 v[214:215], s[28:29], 0, v[144:145]
	global_load_lds_dwordx4 v[212:213], off
	s_add_i32 m0, s21, 0x2000
	v_lshl_add_u64 v[222:223], s[26:27], 0, v[148:149]
	global_load_lds_dwordx4 v[214:215], off
	s_mov_b32 m0, s53
	v_lshl_add_u64 v[224:225], s[26:27], 0, v[146:147]
	global_load_lds_dwordx4 v[222:223], off
	s_mov_b32 m0, s54
	s_nop 0
	global_load_lds_dwordx4 v[224:225], off
	s_waitcnt vmcnt(8)
	s_waitcnt lgkmcnt(0)
	s_barrier
	s_setprio 1
	v_mfma_f32_16x16x32_bf16 v[64:67], v[132:135], v[182:185], 0
	v_mfma_f32_16x16x32_bf16 v[60:63], v[140:143], v[182:185], 0
	v_mfma_f32_16x16x32_bf16 v[48:51], v[132:135], v[190:193], 0
	v_mfma_f32_16x16x32_bf16 v[44:47], v[140:143], v[190:193], 0
	v_mfma_f32_16x16x32_bf16 v[32:35], v[132:135], v[198:201], 0
	v_mfma_f32_16x16x32_bf16 v[28:31], v[140:143], v[198:201], 0
	v_mfma_f32_16x16x32_bf16 v[16:19], v[132:135], v[206:209], 0
	v_mfma_f32_16x16x32_bf16 v[12:15], v[140:143], v[206:209], 0
	v_mfma_f32_16x16x32_bf16 v[64:67], v[136:139], v[186:189], v[64:67]
	v_mfma_f32_16x16x32_bf16 v[60:63], v[154:157], v[186:189], v[60:63]
	v_mfma_f32_16x16x32_bf16 v[48:51], v[136:139], v[194:197], v[48:51]
	v_mfma_f32_16x16x32_bf16 v[44:47], v[154:157], v[194:197], v[44:47]
	v_mfma_f32_16x16x32_bf16 v[32:35], v[136:139], v[202:205], v[32:35]
	v_mfma_f32_16x16x32_bf16 v[28:31], v[154:157], v[202:205], v[28:31]
	v_mfma_f32_16x16x32_bf16 v[16:19], v[136:139], v[218:221], v[16:19]
	v_mfma_f32_16x16x32_bf16 v[12:15], v[154:157], v[218:221], v[12:15]
	s_setprio 0
	s_setprio 1
	v_mfma_f32_16x16x32_bf16 v[56:59], v[158:161], v[182:185], 0
	v_mfma_f32_16x16x32_bf16 v[52:55], v[174:177], v[182:185], 0
	v_mfma_f32_16x16x32_bf16 v[40:43], v[158:161], v[190:193], 0
	v_mfma_f32_16x16x32_bf16 v[36:39], v[174:177], v[190:193], 0
	v_mfma_f32_16x16x32_bf16 v[24:27], v[158:161], v[198:201], 0
	v_mfma_f32_16x16x32_bf16 v[20:23], v[174:177], v[198:201], 0
	v_mfma_f32_16x16x32_bf16 v[8:11], v[158:161], v[206:209], 0
	v_mfma_f32_16x16x32_bf16 v[4:7], v[174:177], v[206:209], 0
	v_mfma_f32_16x16x32_bf16 v[56:59], v[170:173], v[186:189], v[56:59]
	v_mfma_f32_16x16x32_bf16 v[52:55], v[178:181], v[186:189], v[52:55]
	v_mfma_f32_16x16x32_bf16 v[40:43], v[170:173], v[194:197], v[40:43]
	v_mfma_f32_16x16x32_bf16 v[36:39], v[178:181], v[194:197], v[36:39]
	v_mfma_f32_16x16x32_bf16 v[24:27], v[170:173], v[202:205], v[24:27]
	v_mfma_f32_16x16x32_bf16 v[20:23], v[178:181], v[202:205], v[20:23]
	v_mfma_f32_16x16x32_bf16 v[8:11], v[170:173], v[218:221], v[8:11]
	v_mfma_f32_16x16x32_bf16 v[4:7], v[178:181], v[218:221], v[4:7]
	s_barrier
	s_setprio 0
	s_add_i32 s21, 0, 0x18000
	s_add_i32 s23, 0, 0x1c000
	v_add_u32_e32 v154, s21, v166
	v_add_u32_e32 v164, s23, v166
	ds_read_b128 v[132:135], v154
	ds_read_b128 v[136:139], v154 offset:1024
	ds_read_b128 v[140:143], v154 offset:2048
	ds_read_b128 v[154:157], v154 offset:3072
	ds_read_b128 v[158:161], v164
	ds_read_b128 v[170:173], v164 offset:1024
	ds_read_b128 v[174:177], v164 offset:2048
	ds_read_b128 v[178:181], v164 offset:3072
	s_add_u32 s26, s26, s8
	s_addc_u32 s27, s27, s9
	s_mov_b32 m0, s55
	v_lshl_add_u64 v[226:227], s[26:27], 0, v[148:149]
	ds_read_b128 v[182:185], v168 offset:32768
	ds_read_b128 v[186:189], v168 offset:33792
	ds_read_b128 v[190:193], v168 offset:34816
	ds_read_b128 v[194:197], v168 offset:35840
	ds_read_b128 v[198:201], v168 offset:36864
	ds_read_b128 v[202:205], v168 offset:37888
	ds_read_b128 v[206:209], v168 offset:38912
	ds_read_b128 v[218:221], v168 offset:39936
	global_load_lds_dwordx4 v[226:227], off
	v_lshl_add_u64 v[226:227], s[26:27], 0, v[146:147]
	s_mov_b32 m0, s56
	s_nop 0
	global_load_lds_dwordx4 v[226:227], off
	s_waitcnt vmcnt(8)
	s_waitcnt lgkmcnt(0)
	s_barrier
	s_setprio 1
	v_mfma_f32_16x16x32_bf16 v[128:131], v[132:135], v[182:185], v[128:131]
	v_mfma_f32_16x16x32_bf16 v[124:127], v[140:143], v[182:185], v[124:127]
	v_mfma_f32_16x16x32_bf16 v[112:115], v[132:135], v[190:193], v[112:115]
	v_mfma_f32_16x16x32_bf16 v[108:111], v[140:143], v[190:193], v[108:111]
	v_mfma_f32_16x16x32_bf16 v[96:99], v[132:135], v[198:201], v[96:99]
	v_mfma_f32_16x16x32_bf16 v[92:95], v[140:143], v[198:201], v[92:95]
	v_mfma_f32_16x16x32_bf16 v[80:83], v[132:135], v[206:209], v[80:83]
	v_mfma_f32_16x16x32_bf16 v[76:79], v[140:143], v[206:209], v[76:79]
	v_mfma_f32_16x16x32_bf16 v[128:131], v[136:139], v[186:189], v[128:131]
	v_mfma_f32_16x16x32_bf16 v[124:127], v[154:157], v[186:189], v[124:127]
	v_mfma_f32_16x16x32_bf16 v[112:115], v[136:139], v[194:197], v[112:115]
	v_mfma_f32_16x16x32_bf16 v[108:111], v[154:157], v[194:197], v[108:111]
	v_mfma_f32_16x16x32_bf16 v[96:99], v[136:139], v[202:205], v[96:99]
	v_mfma_f32_16x16x32_bf16 v[92:95], v[154:157], v[202:205], v[92:95]
	v_mfma_f32_16x16x32_bf16 v[80:83], v[136:139], v[218:221], v[80:83]
	v_mfma_f32_16x16x32_bf16 v[76:79], v[154:157], v[218:221], v[76:79]
	s_setprio 0
	s_setprio 1
	v_mfma_f32_16x16x32_bf16 v[120:123], v[158:161], v[182:185], v[120:123]
	v_mfma_f32_16x16x32_bf16 v[116:119], v[174:177], v[182:185], v[116:119]
	v_mfma_f32_16x16x32_bf16 v[104:107], v[158:161], v[190:193], v[104:107]
	v_mfma_f32_16x16x32_bf16 v[100:103], v[174:177], v[190:193], v[100:103]
	v_mfma_f32_16x16x32_bf16 v[88:91], v[158:161], v[198:201], v[88:91]
	v_mfma_f32_16x16x32_bf16 v[84:87], v[174:177], v[198:201], v[84:87]
	v_mfma_f32_16x16x32_bf16 v[72:75], v[158:161], v[206:209], v[72:75]
	v_mfma_f32_16x16x32_bf16 v[68:71], v[174:177], v[206:209], v[68:71]
	v_mfma_f32_16x16x32_bf16 v[120:123], v[170:173], v[186:189], v[120:123]
	v_mfma_f32_16x16x32_bf16 v[116:119], v[178:181], v[186:189], v[116:119]
	v_mfma_f32_16x16x32_bf16 v[104:107], v[170:173], v[194:197], v[104:107]
	v_mfma_f32_16x16x32_bf16 v[100:103], v[178:181], v[194:197], v[100:103]
	v_mfma_f32_16x16x32_bf16 v[88:91], v[170:173], v[202:205], v[88:91]
	v_mfma_f32_16x16x32_bf16 v[84:87], v[178:181], v[202:205], v[84:87]
	v_mfma_f32_16x16x32_bf16 v[72:75], v[170:173], v[218:221], v[72:75]
	v_mfma_f32_16x16x32_bf16 v[68:71], v[178:181], v[218:221], v[68:71]
	s_barrier
	s_setprio 0
	s_add_i32 s21, s21, s52
	v_lshl_add_u64 v[162:163], v[162:163], 0, s[24:25]
	s_mov_b32 m0, s21
	ds_read_b128 v[182:185], v168 offset:49152
	ds_read_b128 v[186:189], v168 offset:50176
	ds_read_b128 v[190:193], v168 offset:51200
	ds_read_b128 v[194:197], v168 offset:52224
	ds_read_b128 v[198:201], v168 offset:53248
	ds_read_b128 v[202:205], v168 offset:54272
	ds_read_b128 v[206:209], v168 offset:55296
	ds_read_b128 v[218:221], v168 offset:56320
	global_load_lds_dwordx4 v[162:163], off
	v_lshl_add_u64 v[162:163], v[210:211], 0, s[24:25]
	s_add_i32 m0, s21, 0x2000
	s_add_i32 s21, s23, s52
	global_load_lds_dwordx4 v[162:163], off
	v_lshl_add_u64 v[162:163], v[212:213], 0, s[24:25]
	s_mov_b32 m0, s21
	s_nop 0
	global_load_lds_dwordx4 v[162:163], off
	v_lshl_add_u64 v[162:163], v[214:215], 0, s[24:25]
	s_add_i32 m0, s21, 0x2000
	s_nop 0
	global_load_lds_dwordx4 v[162:163], off
	v_lshl_add_u64 v[162:163], v[222:223], 0, s[24:25]
	s_mov_b32 m0, s61
	s_nop 0
	global_load_lds_dwordx4 v[162:163], off
	v_lshl_add_u64 v[162:163], v[224:225], 0, s[24:25]
	s_mov_b32 m0, s62
	s_nop 0
	global_load_lds_dwordx4 v[162:163], off
	s_waitcnt vmcnt(8)
	s_waitcnt lgkmcnt(0)
	s_barrier
	s_setprio 1
	v_mfma_f32_16x16x32_bf16 v[64:67], v[132:135], v[182:185], v[64:67]
	v_mfma_f32_16x16x32_bf16 v[60:63], v[140:143], v[182:185], v[60:63]
	v_mfma_f32_16x16x32_bf16 v[48:51], v[132:135], v[190:193], v[48:51]
	v_mfma_f32_16x16x32_bf16 v[44:47], v[140:143], v[190:193], v[44:47]
	v_mfma_f32_16x16x32_bf16 v[32:35], v[132:135], v[198:201], v[32:35]
	v_mfma_f32_16x16x32_bf16 v[28:31], v[140:143], v[198:201], v[28:31]
	v_mfma_f32_16x16x32_bf16 v[16:19], v[132:135], v[206:209], v[16:19]
	v_mfma_f32_16x16x32_bf16 v[12:15], v[140:143], v[206:209], v[12:15]
	v_mfma_f32_16x16x32_bf16 v[64:67], v[136:139], v[186:189], v[64:67]
	v_mfma_f32_16x16x32_bf16 v[60:63], v[154:157], v[186:189], v[60:63]
	v_mfma_f32_16x16x32_bf16 v[48:51], v[136:139], v[194:197], v[48:51]
	v_mfma_f32_16x16x32_bf16 v[44:47], v[154:157], v[194:197], v[44:47]
	v_mfma_f32_16x16x32_bf16 v[32:35], v[136:139], v[202:205], v[32:35]
	v_mfma_f32_16x16x32_bf16 v[28:31], v[154:157], v[202:205], v[28:31]
	v_mfma_f32_16x16x32_bf16 v[16:19], v[136:139], v[218:221], v[16:19]
	v_mfma_f32_16x16x32_bf16 v[12:15], v[154:157], v[218:221], v[12:15]
	s_setprio 0
	s_setprio 1
	v_mfma_f32_16x16x32_bf16 v[56:59], v[158:161], v[182:185], v[56:59]
	v_mfma_f32_16x16x32_bf16 v[52:55], v[174:177], v[182:185], v[52:55]
	v_mfma_f32_16x16x32_bf16 v[40:43], v[158:161], v[190:193], v[40:43]
	v_mfma_f32_16x16x32_bf16 v[36:39], v[174:177], v[190:193], v[36:39]
	v_mfma_f32_16x16x32_bf16 v[24:27], v[158:161], v[198:201], v[24:27]
	v_mfma_f32_16x16x32_bf16 v[20:23], v[174:177], v[198:201], v[20:23]
	v_mfma_f32_16x16x32_bf16 v[8:11], v[158:161], v[206:209], v[8:11]
	v_mfma_f32_16x16x32_bf16 v[4:7], v[174:177], v[206:209], v[4:7]
	v_mfma_f32_16x16x32_bf16 v[56:59], v[170:173], v[186:189], v[56:59]
	v_mfma_f32_16x16x32_bf16 v[52:55], v[178:181], v[186:189], v[52:55]
	v_mfma_f32_16x16x32_bf16 v[40:43], v[170:173], v[194:197], v[40:43]
	v_mfma_f32_16x16x32_bf16 v[36:39], v[178:181], v[194:197], v[36:39]
	v_mfma_f32_16x16x32_bf16 v[24:27], v[170:173], v[202:205], v[24:27]
	v_mfma_f32_16x16x32_bf16 v[20:23], v[178:181], v[202:205], v[20:23]
	v_mfma_f32_16x16x32_bf16 v[8:11], v[170:173], v[218:221], v[8:11]
	v_mfma_f32_16x16x32_bf16 v[4:7], v[178:181], v[218:221], v[4:7]
	s_barrier
	s_setprio 0
	s_add_u32 s2, s2, 0x100
	s_addc_u32 s3, s3, 0
	s_add_u32 s19, s19, 0x100
	s_addc_u32 s20, s20, 0
	s_cmp_ge_i32 s22, s59
	s_mov_b32 s21, s22
	s_cbranch_scc1 .LBB0_1330
.LBB0_1329:
	s_add_i32 s22, s21, 2
	s_add_u32 s23, s2, 0x80
	s_addc_u32 s26, s3, 0
	s_add_i32 s30, 0, 0x10000
	s_cmp_eq_u32 s63, s21
	s_cselect_b32 s27, s45, s26
	s_cselect_b32 s26, s44, s23
	s_cselect_b32 s29, s47, s20
	s_cselect_b32 s28, s46, s19
	s_add_i32 s21, 0, 0x14000
	v_add_u32_e32 v154, s30, v166
	v_add_u32_e32 v162, s21, v166
	ds_read_b128 v[132:135], v154
	ds_read_b128 v[136:139], v154 offset:1024
	ds_read_b128 v[140:143], v154 offset:2048
	ds_read_b128 v[154:157], v154 offset:3072
	ds_read_b128 v[158:161], v162
	ds_read_b128 v[170:173], v162 offset:1024
	ds_read_b128 v[174:177], v162 offset:2048
	ds_read_b128 v[178:181], v162 offset:3072
	v_lshl_add_u64 v[162:163], s[2:3], 0, v[150:151]
	s_add_i32 m0, s53, 0xc000
	ds_read_b128 v[182:185], v168
	ds_read_b128 v[186:189], v168 offset:1024
	ds_read_b128 v[190:193], v168 offset:2048
	ds_read_b128 v[194:197], v168 offset:3072
	ds_read_b128 v[198:201], v168 offset:4096
	ds_read_b128 v[202:205], v168 offset:5120
	ds_read_b128 v[206:209], v168 offset:6144
	ds_read_b128 v[218:221], v168 offset:7168
	global_load_lds_dwordx4 v[162:163], off
	v_lshl_add_u64 v[162:163], s[2:3], 0, v[152:153]
	s_add_i32 m0, s53, 0xe000
	s_nop 0
	global_load_lds_dwordx4 v[162:163], off
	s_waitcnt vmcnt(8)
	s_waitcnt lgkmcnt(0)
	s_barrier
	s_setprio 1
	v_mfma_f32_16x16x32_bf16 v[128:131], v[132:135], v[182:185], v[128:131]
	v_mfma_f32_16x16x32_bf16 v[124:127], v[140:143], v[182:185], v[124:127]
	v_mfma_f32_16x16x32_bf16 v[112:115], v[132:135], v[190:193], v[112:115]
	v_mfma_f32_16x16x32_bf16 v[108:111], v[140:143], v[190:193], v[108:111]
	v_mfma_f32_16x16x32_bf16 v[96:99], v[132:135], v[198:201], v[96:99]
	v_mfma_f32_16x16x32_bf16 v[92:95], v[140:143], v[198:201], v[92:95]
	v_mfma_f32_16x16x32_bf16 v[80:83], v[132:135], v[206:209], v[80:83]
	v_mfma_f32_16x16x32_bf16 v[76:79], v[140:143], v[206:209], v[76:79]
	v_mfma_f32_16x16x32_bf16 v[128:131], v[136:139], v[186:189], v[128:131]
	v_mfma_f32_16x16x32_bf16 v[124:127], v[154:157], v[186:189], v[124:127]
	v_mfma_f32_16x16x32_bf16 v[112:115], v[136:139], v[194:197], v[112:115]
	v_mfma_f32_16x16x32_bf16 v[108:111], v[154:157], v[194:197], v[108:111]
	v_mfma_f32_16x16x32_bf16 v[96:99], v[136:139], v[202:205], v[96:99]
	v_mfma_f32_16x16x32_bf16 v[92:95], v[154:157], v[202:205], v[92:95]
	v_mfma_f32_16x16x32_bf16 v[80:83], v[136:139], v[218:221], v[80:83]
	v_mfma_f32_16x16x32_bf16 v[76:79], v[154:157], v[218:221], v[76:79]
	s_setprio 0
	s_setprio 1
	v_mfma_f32_16x16x32_bf16 v[120:123], v[158:161], v[182:185], v[120:123]
	v_mfma_f32_16x16x32_bf16 v[116:119], v[174:177], v[182:185], v[116:119]
	v_mfma_f32_16x16x32_bf16 v[104:107], v[158:161], v[190:193], v[104:107]
	v_mfma_f32_16x16x32_bf16 v[100:103], v[174:177], v[190:193], v[100:103]
	v_mfma_f32_16x16x32_bf16 v[88:91], v[158:161], v[198:201], v[88:91]
	v_mfma_f32_16x16x32_bf16 v[84:87], v[174:177], v[198:201], v[84:87]
	v_mfma_f32_16x16x32_bf16 v[72:75], v[158:161], v[206:209], v[72:75]
	v_mfma_f32_16x16x32_bf16 v[68:71], v[174:177], v[206:209], v[68:71]
	v_mfma_f32_16x16x32_bf16 v[120:123], v[170:173], v[186:189], v[120:123]
	v_mfma_f32_16x16x32_bf16 v[116:119], v[178:181], v[186:189], v[116:119]
	v_mfma_f32_16x16x32_bf16 v[104:107], v[170:173], v[194:197], v[104:107]
	v_mfma_f32_16x16x32_bf16 v[100:103], v[178:181], v[194:197], v[100:103]
	v_mfma_f32_16x16x32_bf16 v[88:91], v[170:173], v[202:205], v[88:91]
	v_mfma_f32_16x16x32_bf16 v[84:87], v[178:181], v[202:205], v[84:87]
	v_mfma_f32_16x16x32_bf16 v[72:75], v[170:173], v[218:221], v[72:75]
	v_mfma_f32_16x16x32_bf16 v[68:71], v[178:181], v[218:221], v[68:71]
	s_barrier
	s_setprio 0
	s_add_i32 s23, s30, s52
	v_lshl_add_u64 v[162:163], s[28:29], 0, v[2:3]
	s_mov_b32 m0, s23
	ds_read_b128 v[182:185], v168 offset:16384
	ds_read_b128 v[186:189], v168 offset:17408
	ds_read_b128 v[190:193], v168 offset:18432
	ds_read_b128 v[194:197], v168 offset:19456
	ds_read_b128 v[198:201], v168 offset:20480
	ds_read_b128 v[202:205], v168 offset:21504
	ds_read_b128 v[206:209], v168 offset:22528
	ds_read_b128 v[218:221], v168 offset:23552
	global_load_lds_dwordx4 v[162:163], off
	s_add_i32 m0, s23, 0x2000
	v_lshl_add_u64 v[210:211], s[28:29], 0, v[144:145]
	s_add_u32 s28, s28, s8
	s_addc_u32 s29, s29, s9
	s_add_i32 s21, s21, s52
	global_load_lds_dwordx4 v[210:211], off
	v_lshl_add_u64 v[212:213], s[28:29], 0, v[2:3]
	s_mov_b32 m0, s21
	v_lshl_add_u64 v[214:215], s[28:29], 0, v[144:145]
	global_load_lds_dwordx4 v[212:213], off
	s_add_i32 m0, s21, 0x2000
	v_lshl_add_u64 v[222:223], s[26:27], 0, v[148:149]
	global_load_lds_dwordx4 v[214:215], off
	s_mov_b32 m0, s53
	v_lshl_add_u64 v[224:225], s[26:27], 0, v[146:147]
	global_load_lds_dwordx4 v[222:223], off
	s_mov_b32 m0, s54
	s_nop 0
	global_load_lds_dwordx4 v[224:225], off
	s_waitcnt vmcnt(8)
	s_waitcnt lgkmcnt(0)
	s_barrier
	s_setprio 1
	v_mfma_f32_16x16x32_bf16 v[64:67], v[132:135], v[182:185], v[64:67]
	v_mfma_f32_16x16x32_bf16 v[60:63], v[140:143], v[182:185], v[60:63]
	v_mfma_f32_16x16x32_bf16 v[48:51], v[132:135], v[190:193], v[48:51]
	v_mfma_f32_16x16x32_bf16 v[44:47], v[140:143], v[190:193], v[44:47]
	v_mfma_f32_16x16x32_bf16 v[32:35], v[132:135], v[198:201], v[32:35]
	v_mfma_f32_16x16x32_bf16 v[28:31], v[140:143], v[198:201], v[28:31]
	v_mfma_f32_16x16x32_bf16 v[16:19], v[132:135], v[206:209], v[16:19]
	v_mfma_f32_16x16x32_bf16 v[12:15], v[140:143], v[206:209], v[12:15]
	v_mfma_f32_16x16x32_bf16 v[64:67], v[136:139], v[186:189], v[64:67]
	v_mfma_f32_16x16x32_bf16 v[60:63], v[154:157], v[186:189], v[60:63]
	v_mfma_f32_16x16x32_bf16 v[48:51], v[136:139], v[194:197], v[48:51]
	v_mfma_f32_16x16x32_bf16 v[44:47], v[154:157], v[194:197], v[44:47]
	v_mfma_f32_16x16x32_bf16 v[32:35], v[136:139], v[202:205], v[32:35]
	v_mfma_f32_16x16x32_bf16 v[28:31], v[154:157], v[202:205], v[28:31]
	v_mfma_f32_16x16x32_bf16 v[16:19], v[136:139], v[218:221], v[16:19]
	v_mfma_f32_16x16x32_bf16 v[12:15], v[154:157], v[218:221], v[12:15]
	s_setprio 0
	s_setprio 1
	v_mfma_f32_16x16x32_bf16 v[56:59], v[158:161], v[182:185], v[56:59]
	v_mfma_f32_16x16x32_bf16 v[52:55], v[174:177], v[182:185], v[52:55]
	v_mfma_f32_16x16x32_bf16 v[40:43], v[158:161], v[190:193], v[40:43]
	v_mfma_f32_16x16x32_bf16 v[36:39], v[174:177], v[190:193], v[36:39]
	v_mfma_f32_16x16x32_bf16 v[24:27], v[158:161], v[198:201], v[24:27]
	v_mfma_f32_16x16x32_bf16 v[20:23], v[174:177], v[198:201], v[20:23]
	v_mfma_f32_16x16x32_bf16 v[8:11], v[158:161], v[206:209], v[8:11]
	v_mfma_f32_16x16x32_bf16 v[4:7], v[174:177], v[206:209], v[4:7]
	v_mfma_f32_16x16x32_bf16 v[56:59], v[170:173], v[186:189], v[56:59]
	v_mfma_f32_16x16x32_bf16 v[52:55], v[178:181], v[186:189], v[52:55]
	v_mfma_f32_16x16x32_bf16 v[40:43], v[170:173], v[194:197], v[40:43]
	v_mfma_f32_16x16x32_bf16 v[36:39], v[178:181], v[194:197], v[36:39]
	v_mfma_f32_16x16x32_bf16 v[24:27], v[170:173], v[202:205], v[24:27]
	v_mfma_f32_16x16x32_bf16 v[20:23], v[178:181], v[202:205], v[20:23]
	v_mfma_f32_16x16x32_bf16 v[8:11], v[170:173], v[218:221], v[8:11]
	v_mfma_f32_16x16x32_bf16 v[4:7], v[178:181], v[218:221], v[4:7]
	s_barrier
	s_setprio 0
	s_add_i32 s21, 0, 0x18000
	s_add_i32 s23, 0, 0x1c000
	v_add_u32_e32 v154, s21, v166
	v_add_u32_e32 v164, s23, v166
	ds_read_b128 v[132:135], v154
	ds_read_b128 v[136:139], v154 offset:1024
	ds_read_b128 v[140:143], v154 offset:2048
	ds_read_b128 v[154:157], v154 offset:3072
	ds_read_b128 v[158:161], v164
	ds_read_b128 v[170:173], v164 offset:1024
	ds_read_b128 v[174:177], v164 offset:2048
	ds_read_b128 v[178:181], v164 offset:3072
	s_add_u32 s26, s26, s8
	s_addc_u32 s27, s27, s9
	s_mov_b32 m0, s55
	v_lshl_add_u64 v[226:227], s[26:27], 0, v[148:149]
	ds_read_b128 v[182:185], v168 offset:32768
	ds_read_b128 v[186:189], v168 offset:33792
	ds_read_b128 v[190:193], v168 offset:34816
	ds_read_b128 v[194:197], v168 offset:35840
	ds_read_b128 v[198:201], v168 offset:36864
	ds_read_b128 v[202:205], v168 offset:37888
	ds_read_b128 v[206:209], v168 offset:38912
	ds_read_b128 v[218:221], v168 offset:39936
	global_load_lds_dwordx4 v[226:227], off
	v_lshl_add_u64 v[226:227], s[26:27], 0, v[146:147]
	s_mov_b32 m0, s56
	s_nop 0
	global_load_lds_dwordx4 v[226:227], off
	s_waitcnt vmcnt(8)
	s_waitcnt lgkmcnt(0)
	s_barrier
	s_setprio 1
	v_mfma_f32_16x16x32_bf16 v[128:131], v[132:135], v[182:185], v[128:131]
	v_mfma_f32_16x16x32_bf16 v[124:127], v[140:143], v[182:185], v[124:127]
	v_mfma_f32_16x16x32_bf16 v[112:115], v[132:135], v[190:193], v[112:115]
	v_mfma_f32_16x16x32_bf16 v[108:111], v[140:143], v[190:193], v[108:111]
	v_mfma_f32_16x16x32_bf16 v[96:99], v[132:135], v[198:201], v[96:99]
	v_mfma_f32_16x16x32_bf16 v[92:95], v[140:143], v[198:201], v[92:95]
	v_mfma_f32_16x16x32_bf16 v[80:83], v[132:135], v[206:209], v[80:83]
	v_mfma_f32_16x16x32_bf16 v[76:79], v[140:143], v[206:209], v[76:79]
	v_mfma_f32_16x16x32_bf16 v[128:131], v[136:139], v[186:189], v[128:131]
	v_mfma_f32_16x16x32_bf16 v[124:127], v[154:157], v[186:189], v[124:127]
	v_mfma_f32_16x16x32_bf16 v[112:115], v[136:139], v[194:197], v[112:115]
	v_mfma_f32_16x16x32_bf16 v[108:111], v[154:157], v[194:197], v[108:111]
	v_mfma_f32_16x16x32_bf16 v[96:99], v[136:139], v[202:205], v[96:99]
	v_mfma_f32_16x16x32_bf16 v[92:95], v[154:157], v[202:205], v[92:95]
	v_mfma_f32_16x16x32_bf16 v[80:83], v[136:139], v[218:221], v[80:83]
	v_mfma_f32_16x16x32_bf16 v[76:79], v[154:157], v[218:221], v[76:79]
	s_setprio 0
	s_setprio 1
	v_mfma_f32_16x16x32_bf16 v[120:123], v[158:161], v[182:185], v[120:123]
	v_mfma_f32_16x16x32_bf16 v[116:119], v[174:177], v[182:185], v[116:119]
	v_mfma_f32_16x16x32_bf16 v[104:107], v[158:161], v[190:193], v[104:107]
	v_mfma_f32_16x16x32_bf16 v[100:103], v[174:177], v[190:193], v[100:103]
	v_mfma_f32_16x16x32_bf16 v[88:91], v[158:161], v[198:201], v[88:91]
	v_mfma_f32_16x16x32_bf16 v[84:87], v[174:177], v[198:201], v[84:87]
	v_mfma_f32_16x16x32_bf16 v[72:75], v[158:161], v[206:209], v[72:75]
	v_mfma_f32_16x16x32_bf16 v[68:71], v[174:177], v[206:209], v[68:71]
	v_mfma_f32_16x16x32_bf16 v[120:123], v[170:173], v[186:189], v[120:123]
	v_mfma_f32_16x16x32_bf16 v[116:119], v[178:181], v[186:189], v[116:119]
	v_mfma_f32_16x16x32_bf16 v[104:107], v[170:173], v[194:197], v[104:107]
	v_mfma_f32_16x16x32_bf16 v[100:103], v[178:181], v[194:197], v[100:103]
	v_mfma_f32_16x16x32_bf16 v[88:91], v[170:173], v[202:205], v[88:91]
	v_mfma_f32_16x16x32_bf16 v[84:87], v[178:181], v[202:205], v[84:87]
	v_mfma_f32_16x16x32_bf16 v[72:75], v[170:173], v[218:221], v[72:75]
	v_mfma_f32_16x16x32_bf16 v[68:71], v[178:181], v[218:221], v[68:71]
	s_barrier
	s_setprio 0
	s_add_i32 s21, s21, s52
	v_lshl_add_u64 v[162:163], v[162:163], 0, s[24:25]
	s_mov_b32 m0, s21
	ds_read_b128 v[182:185], v168 offset:49152
	ds_read_b128 v[186:189], v168 offset:50176
	ds_read_b128 v[190:193], v168 offset:51200
	ds_read_b128 v[194:197], v168 offset:52224
	ds_read_b128 v[198:201], v168 offset:53248
	ds_read_b128 v[202:205], v168 offset:54272
	ds_read_b128 v[206:209], v168 offset:55296
	ds_read_b128 v[218:221], v168 offset:56320
	global_load_lds_dwordx4 v[162:163], off
	v_lshl_add_u64 v[162:163], v[210:211], 0, s[24:25]
	s_add_i32 m0, s21, 0x2000
	s_add_i32 s21, s23, s52
	global_load_lds_dwordx4 v[162:163], off
	v_lshl_add_u64 v[162:163], v[212:213], 0, s[24:25]
	s_mov_b32 m0, s21
	s_nop 0
	global_load_lds_dwordx4 v[162:163], off
	v_lshl_add_u64 v[162:163], v[214:215], 0, s[24:25]
	s_add_i32 m0, s21, 0x2000
	s_nop 0
	global_load_lds_dwordx4 v[162:163], off
	v_lshl_add_u64 v[162:163], v[222:223], 0, s[24:25]
	s_mov_b32 m0, s61
	s_nop 0
	global_load_lds_dwordx4 v[162:163], off
	v_lshl_add_u64 v[162:163], v[224:225], 0, s[24:25]
	s_mov_b32 m0, s62
	s_nop 0
	global_load_lds_dwordx4 v[162:163], off
	s_waitcnt vmcnt(8)
	s_waitcnt lgkmcnt(0)
	s_barrier
	s_setprio 1
	v_mfma_f32_16x16x32_bf16 v[64:67], v[132:135], v[182:185], v[64:67]
	v_mfma_f32_16x16x32_bf16 v[60:63], v[140:143], v[182:185], v[60:63]
	v_mfma_f32_16x16x32_bf16 v[48:51], v[132:135], v[190:193], v[48:51]
	v_mfma_f32_16x16x32_bf16 v[44:47], v[140:143], v[190:193], v[44:47]
	v_mfma_f32_16x16x32_bf16 v[32:35], v[132:135], v[198:201], v[32:35]
	v_mfma_f32_16x16x32_bf16 v[28:31], v[140:143], v[198:201], v[28:31]
	v_mfma_f32_16x16x32_bf16 v[16:19], v[132:135], v[206:209], v[16:19]
	v_mfma_f32_16x16x32_bf16 v[12:15], v[140:143], v[206:209], v[12:15]
	v_mfma_f32_16x16x32_bf16 v[64:67], v[136:139], v[186:189], v[64:67]
	v_mfma_f32_16x16x32_bf16 v[60:63], v[154:157], v[186:189], v[60:63]
	v_mfma_f32_16x16x32_bf16 v[48:51], v[136:139], v[194:197], v[48:51]
	v_mfma_f32_16x16x32_bf16 v[44:47], v[154:157], v[194:197], v[44:47]
	v_mfma_f32_16x16x32_bf16 v[32:35], v[136:139], v[202:205], v[32:35]
	v_mfma_f32_16x16x32_bf16 v[28:31], v[154:157], v[202:205], v[28:31]
	v_mfma_f32_16x16x32_bf16 v[16:19], v[136:139], v[218:221], v[16:19]
	v_mfma_f32_16x16x32_bf16 v[12:15], v[154:157], v[218:221], v[12:15]
	s_setprio 0
	s_setprio 1
	v_mfma_f32_16x16x32_bf16 v[56:59], v[158:161], v[182:185], v[56:59]
	v_mfma_f32_16x16x32_bf16 v[52:55], v[174:177], v[182:185], v[52:55]
	v_mfma_f32_16x16x32_bf16 v[40:43], v[158:161], v[190:193], v[40:43]
	v_mfma_f32_16x16x32_bf16 v[36:39], v[174:177], v[190:193], v[36:39]
	v_mfma_f32_16x16x32_bf16 v[24:27], v[158:161], v[198:201], v[24:27]
	v_mfma_f32_16x16x32_bf16 v[20:23], v[174:177], v[198:201], v[20:23]
	v_mfma_f32_16x16x32_bf16 v[8:11], v[158:161], v[206:209], v[8:11]
	v_mfma_f32_16x16x32_bf16 v[4:7], v[174:177], v[206:209], v[4:7]
	v_mfma_f32_16x16x32_bf16 v[56:59], v[170:173], v[186:189], v[56:59]
	v_mfma_f32_16x16x32_bf16 v[52:55], v[178:181], v[186:189], v[52:55]
	v_mfma_f32_16x16x32_bf16 v[40:43], v[170:173], v[194:197], v[40:43]
	v_mfma_f32_16x16x32_bf16 v[36:39], v[178:181], v[194:197], v[36:39]
	v_mfma_f32_16x16x32_bf16 v[24:27], v[170:173], v[202:205], v[24:27]
	v_mfma_f32_16x16x32_bf16 v[20:23], v[178:181], v[202:205], v[20:23]
	v_mfma_f32_16x16x32_bf16 v[8:11], v[170:173], v[218:221], v[8:11]
	v_mfma_f32_16x16x32_bf16 v[4:7], v[178:181], v[218:221], v[4:7]
	s_barrier
	s_setprio 0
	s_add_u32 s2, s2, 0x100
	s_addc_u32 s3, s3, 0
	s_add_u32 s19, s19, 0x100
	s_addc_u32 s20, s20, 0
	s_cmp_ge_i32 s22, s59
	s_mov_b32 s21, s22
	s_cbranch_scc0 .LBB0_1329

.LBB0_1865:
	s_add_i32 s29, s26, 2
	s_add_u32 s34, s30, 0x80
	s_addc_u32 s27, s31, 0
	s_add_i32 s37, 0, 0x10000
	s_cmp_eq_u32 s17, s26
	s_cselect_b32 s27, s3, s27
	s_cselect_b32 s26, s2, s34
	v_add_u32_e32 v2, s37, v207
	s_cselect_b32 s43, s45, s28
	s_cselect_b32 s42, s44, s23
	s_add_i32 s34, 0, 0x14000
	ds_read_b128 v[54:57], v2
	ds_read_b128 v[58:61], v2 offset:1024
	ds_read_b128 v[62:65], v2 offset:2048
	ds_read_b128 v[66:69], v2 offset:3072
	v_add_u32_e32 v2, s34, v207
	ds_read_b128 v[150:153], v2
	ds_read_b128 v[154:157], v2 offset:1024
	ds_read_b128 v[158:161], v2 offset:2048
	ds_read_b128 v[162:165], v2 offset:3072
	v_lshl_add_u64 v[4:5], s[30:31], 0, v[188:189]
	s_add_i32 m0, s55, 0xc000
	ds_read_b128 v[166:169], v209
	ds_read_b128 v[170:173], v209 offset:1024
	ds_read_b128 v[174:177], v209 offset:2048
	ds_read_b128 v[192:195], v209 offset:3072
	ds_read_b128 v[196:199], v209 offset:4096
	ds_read_b128 v[200:203], v209 offset:5120
	ds_read_b128 v[218:221], v209 offset:6144
	ds_read_b128 v[222:225], v209 offset:7168
	global_load_lds_dwordx4 v[4:5], off
	v_lshl_add_u64 v[4:5], s[30:31], 0, v[190:191]
	s_add_i32 m0, s55, 0xe000
	s_nop 0
	global_load_lds_dwordx4 v[4:5], off
	s_waitcnt vmcnt(8)
	s_waitcnt lgkmcnt(0)
	s_barrier
	s_setprio 1
	v_mfma_f32_16x16x32_bf16 v[90:93], v[54:57], v[166:169], v[90:93]
	v_mfma_f32_16x16x32_bf16 v[86:89], v[62:65], v[166:169], v[86:89]
	v_mfma_f32_16x16x32_bf16 v[106:109], v[54:57], v[174:177], v[106:109]
	v_mfma_f32_16x16x32_bf16 v[102:105], v[62:65], v[174:177], v[102:105]
	v_mfma_f32_16x16x32_bf16 v[138:141], v[54:57], v[196:199], v[138:141]
	v_mfma_f32_16x16x32_bf16 v[134:137], v[62:65], v[196:199], v[134:137]
	v_mfma_f32_16x16x32_bf16 v[130:133], v[54:57], v[218:221], v[130:133]
	v_mfma_f32_16x16x32_bf16 v[126:129], v[62:65], v[218:221], v[126:129]
	v_mfma_f32_16x16x32_bf16 v[90:93], v[58:61], v[170:173], v[90:93]
	v_mfma_f32_16x16x32_bf16 v[86:89], v[66:69], v[170:173], v[86:89]
	v_mfma_f32_16x16x32_bf16 v[106:109], v[58:61], v[192:195], v[106:109]
	v_mfma_f32_16x16x32_bf16 v[102:105], v[66:69], v[192:195], v[102:105]
	v_mfma_f32_16x16x32_bf16 v[138:141], v[58:61], v[200:203], v[138:141]
	v_mfma_f32_16x16x32_bf16 v[134:137], v[66:69], v[200:203], v[134:137]
	v_mfma_f32_16x16x32_bf16 v[130:133], v[58:61], v[222:225], v[130:133]
	v_mfma_f32_16x16x32_bf16 v[126:129], v[66:69], v[222:225], v[126:129]
	s_setprio 0
	s_setprio 1
	v_mfma_f32_16x16x32_bf16 v[98:101], v[150:153], v[166:169], v[98:101]
	v_mfma_f32_16x16x32_bf16 v[94:97], v[158:161], v[166:169], v[94:97]
	v_mfma_f32_16x16x32_bf16 v[122:125], v[150:153], v[174:177], v[122:125]
	v_mfma_f32_16x16x32_bf16 v[110:113], v[158:161], v[174:177], v[110:113]
	v_mfma_f32_16x16x32_bf16 v[146:149], v[150:153], v[196:199], v[146:149]
	v_mfma_f32_16x16x32_bf16 v[142:145], v[158:161], v[196:199], v[142:145]
	v_mfma_f32_16x16x32_bf16 v[118:121], v[150:153], v[218:221], v[118:121]
	v_mfma_f32_16x16x32_bf16 v[114:117], v[158:161], v[218:221], v[114:117]
	v_mfma_f32_16x16x32_bf16 v[98:101], v[154:157], v[170:173], v[98:101]
	v_mfma_f32_16x16x32_bf16 v[94:97], v[162:165], v[170:173], v[94:97]
	v_mfma_f32_16x16x32_bf16 v[122:125], v[154:157], v[192:195], v[122:125]
	v_mfma_f32_16x16x32_bf16 v[110:113], v[162:165], v[192:195], v[110:113]
	v_mfma_f32_16x16x32_bf16 v[146:149], v[154:157], v[200:203], v[146:149]
	v_mfma_f32_16x16x32_bf16 v[142:145], v[162:165], v[200:203], v[142:145]
	v_mfma_f32_16x16x32_bf16 v[118:121], v[154:157], v[222:225], v[118:121]
	v_mfma_f32_16x16x32_bf16 v[114:117], v[162:165], v[222:225], v[114:117]
	s_barrier
	s_setprio 0
	s_add_i32 s37, s37, s54
	v_lshl_add_u64 v[204:205], s[42:43], 0, v[182:183]
	s_mov_b32 m0, s37
	ds_read_b128 v[166:169], v209 offset:16384
	ds_read_b128 v[170:173], v209 offset:17408
	ds_read_b128 v[174:177], v209 offset:18432
	ds_read_b128 v[192:195], v209 offset:19456
	ds_read_b128 v[196:199], v209 offset:20480
	ds_read_b128 v[200:203], v209 offset:21504
	ds_read_b128 v[218:221], v209 offset:22528
	ds_read_b128 v[222:225], v209 offset:23552
	global_load_lds_dwordx4 v[204:205], off
	s_add_i32 m0, s37, 0x2000
	v_lshl_add_u64 v[210:211], s[42:43], 0, v[178:179]
	s_add_u32 s42, s42, s6
	s_addc_u32 s43, s43, s7
	s_add_i32 s34, s34, s54
	global_load_lds_dwordx4 v[210:211], off
	v_lshl_add_u64 v[212:213], s[42:43], 0, v[182:183]
	s_mov_b32 m0, s34
	v_lshl_add_u64 v[214:215], s[42:43], 0, v[178:179]
	global_load_lds_dwordx4 v[212:213], off
	s_add_i32 m0, s34, 0x2000
	v_lshl_add_u64 v[226:227], s[26:27], 0, v[184:185]
	global_load_lds_dwordx4 v[214:215], off
	s_mov_b32 m0, s55
	v_lshl_add_u64 v[228:229], s[26:27], 0, v[180:181]
	global_load_lds_dwordx4 v[226:227], off
	s_mov_b32 m0, s56
	s_nop 0
	global_load_lds_dwordx4 v[228:229], off
	s_waitcnt vmcnt(8)
	s_waitcnt lgkmcnt(0)
	s_barrier
	s_setprio 1
	v_mfma_f32_16x16x32_bf16 v[82:85], v[54:57], v[166:169], v[82:85]
	v_mfma_f32_16x16x32_bf16 v[78:81], v[62:65], v[166:169], v[78:81]
	v_mfma_f32_16x16x32_bf16 v[50:53], v[54:57], v[174:177], v[50:53]
	v_mfma_f32_16x16x32_bf16 v[46:49], v[62:65], v[174:177], v[46:49]
	v_mfma_f32_16x16x32_bf16 v[34:37], v[54:57], v[196:199], v[34:37]
	v_mfma_f32_16x16x32_bf16 v[30:33], v[62:65], v[196:199], v[30:33]
	v_mfma_f32_16x16x32_bf16 v[18:21], v[54:57], v[218:221], v[18:21]
	v_mfma_f32_16x16x32_bf16 v[14:17], v[62:65], v[218:221], v[14:17]
	v_mfma_f32_16x16x32_bf16 v[82:85], v[58:61], v[170:173], v[82:85]
	v_mfma_f32_16x16x32_bf16 v[78:81], v[66:69], v[170:173], v[78:81]
	v_mfma_f32_16x16x32_bf16 v[50:53], v[58:61], v[192:195], v[50:53]
	v_mfma_f32_16x16x32_bf16 v[46:49], v[66:69], v[192:195], v[46:49]
	v_mfma_f32_16x16x32_bf16 v[34:37], v[58:61], v[200:203], v[34:37]
	v_mfma_f32_16x16x32_bf16 v[30:33], v[66:69], v[200:203], v[30:33]
	v_mfma_f32_16x16x32_bf16 v[18:21], v[58:61], v[222:225], v[18:21]
	v_mfma_f32_16x16x32_bf16 v[14:17], v[66:69], v[222:225], v[14:17]
	s_setprio 0
	s_setprio 1
	v_mfma_f32_16x16x32_bf16 v[42:45], v[150:153], v[174:177], v[42:45]
	v_mfma_f32_16x16x32_bf16 v[38:41], v[158:161], v[174:177], v[38:41]
	v_mfma_f32_16x16x32_bf16 v[26:29], v[150:153], v[196:199], v[26:29]
	v_mfma_f32_16x16x32_bf16 v[22:25], v[158:161], v[196:199], v[22:25]
	v_mfma_f32_16x16x32_bf16 v[10:13], v[150:153], v[218:221], v[10:13]
	v_mfma_f32_16x16x32_bf16 v[4:7], v[158:161], v[218:221], v[6:9]
	v_mfma_f32_16x16x32_bf16 v[54:57], v[150:153], v[166:169], v[74:77]
	v_mfma_f32_16x16x32_bf16 v[58:61], v[158:161], v[166:169], v[70:73]
	v_mfma_f32_16x16x32_bf16 v[42:45], v[154:157], v[192:195], v[42:45]
	v_mfma_f32_16x16x32_bf16 v[38:41], v[162:165], v[192:195], v[38:41]
	v_mfma_f32_16x16x32_bf16 v[26:29], v[154:157], v[200:203], v[26:29]
	v_mfma_f32_16x16x32_bf16 v[22:25], v[162:165], v[200:203], v[22:25]
	v_mfma_f32_16x16x32_bf16 v[10:13], v[154:157], v[222:225], v[10:13]
	v_mfma_f32_16x16x32_bf16 v[4:7], v[162:165], v[222:225], v[4:7]
	v_mfma_f32_16x16x32_bf16 v[54:57], v[154:157], v[170:173], v[54:57]
	v_mfma_f32_16x16x32_bf16 v[58:61], v[162:165], v[170:173], v[58:61]
	s_barrier
	s_setprio 0
	s_add_i32 s34, 0, 0x18000
	v_add_u32_e32 v2, s34, v207
	s_add_i32 s37, 0, 0x1c000
	ds_read_b128 v[62:65], v2
	ds_read_b128 v[66:69], v2 offset:1024
	ds_read_b128 v[70:73], v2 offset:2048
	ds_read_b128 v[74:77], v2 offset:3072
	v_add_u32_e32 v2, s37, v207
	ds_read_b128 v[150:153], v2
	ds_read_b128 v[154:157], v2 offset:1024
	ds_read_b128 v[158:161], v2 offset:2048
	ds_read_b128 v[162:165], v2 offset:3072
	s_add_u32 s26, s26, s6
	s_addc_u32 s27, s27, s7
	s_mov_b32 m0, s57
	v_lshl_add_u64 v[8:9], s[26:27], 0, v[184:185]
	ds_read_b128 v[166:169], v209 offset:32768
	ds_read_b128 v[170:173], v209 offset:33792
	ds_read_b128 v[174:177], v209 offset:34816
	ds_read_b128 v[192:195], v209 offset:35840
	ds_read_b128 v[196:199], v209 offset:36864
	ds_read_b128 v[200:203], v209 offset:37888
	ds_read_b128 v[218:221], v209 offset:38912
	ds_read_b128 v[222:225], v209 offset:39936
	global_load_lds_dwordx4 v[8:9], off
	v_lshl_add_u64 v[8:9], s[26:27], 0, v[180:181]
	s_mov_b32 m0, s58
	s_nop 0
	global_load_lds_dwordx4 v[8:9], off
	s_waitcnt vmcnt(8)
	s_waitcnt lgkmcnt(0)
	s_barrier
	s_setprio 1
	v_mfma_f32_16x16x32_bf16 v[90:93], v[62:65], v[166:169], v[90:93]
	v_mfma_f32_16x16x32_bf16 v[86:89], v[70:73], v[166:169], v[86:89]
	v_mfma_f32_16x16x32_bf16 v[106:109], v[62:65], v[174:177], v[106:109]
	v_mfma_f32_16x16x32_bf16 v[102:105], v[70:73], v[174:177], v[102:105]
	v_mfma_f32_16x16x32_bf16 v[138:141], v[62:65], v[196:199], v[138:141]
	v_mfma_f32_16x16x32_bf16 v[134:137], v[70:73], v[196:199], v[134:137]
	v_mfma_f32_16x16x32_bf16 v[130:133], v[62:65], v[218:221], v[130:133]
	v_mfma_f32_16x16x32_bf16 v[126:129], v[70:73], v[218:221], v[126:129]
	v_mfma_f32_16x16x32_bf16 v[90:93], v[66:69], v[170:173], v[90:93]
	v_mfma_f32_16x16x32_bf16 v[86:89], v[74:77], v[170:173], v[86:89]
	v_mfma_f32_16x16x32_bf16 v[106:109], v[66:69], v[192:195], v[106:109]
	v_mfma_f32_16x16x32_bf16 v[102:105], v[74:77], v[192:195], v[102:105]
	v_mfma_f32_16x16x32_bf16 v[138:141], v[66:69], v[200:203], v[138:141]
	v_mfma_f32_16x16x32_bf16 v[134:137], v[74:77], v[200:203], v[134:137]
	v_mfma_f32_16x16x32_bf16 v[130:133], v[66:69], v[222:225], v[130:133]
	v_mfma_f32_16x16x32_bf16 v[126:129], v[74:77], v[222:225], v[126:129]
	s_setprio 0
	s_setprio 1
	v_mfma_f32_16x16x32_bf16 v[98:101], v[150:153], v[166:169], v[98:101]
	v_mfma_f32_16x16x32_bf16 v[94:97], v[158:161], v[166:169], v[94:97]
	v_mfma_f32_16x16x32_bf16 v[122:125], v[150:153], v[174:177], v[122:125]
	v_mfma_f32_16x16x32_bf16 v[110:113], v[158:161], v[174:177], v[110:113]
	v_mfma_f32_16x16x32_bf16 v[146:149], v[150:153], v[196:199], v[146:149]
	v_mfma_f32_16x16x32_bf16 v[142:145], v[158:161], v[196:199], v[142:145]
	v_mfma_f32_16x16x32_bf16 v[118:121], v[150:153], v[218:221], v[118:121]
	v_mfma_f32_16x16x32_bf16 v[114:117], v[158:161], v[218:221], v[114:117]
	v_mfma_f32_16x16x32_bf16 v[98:101], v[154:157], v[170:173], v[98:101]
	v_mfma_f32_16x16x32_bf16 v[94:97], v[162:165], v[170:173], v[94:97]
	v_mfma_f32_16x16x32_bf16 v[122:125], v[154:157], v[192:195], v[122:125]
	v_mfma_f32_16x16x32_bf16 v[110:113], v[162:165], v[192:195], v[110:113]
	v_mfma_f32_16x16x32_bf16 v[146:149], v[154:157], v[200:203], v[146:149]
	v_mfma_f32_16x16x32_bf16 v[142:145], v[162:165], v[200:203], v[142:145]
	v_mfma_f32_16x16x32_bf16 v[118:121], v[154:157], v[222:225], v[118:121]
	v_mfma_f32_16x16x32_bf16 v[114:117], v[162:165], v[222:225], v[114:117]
	s_barrier
	s_setprio 0
	s_add_i32 s26, s34, s54
	v_lshl_add_u64 v[8:9], v[204:205], 0, s[24:25]
	s_mov_b32 m0, s26
	ds_read_b128 v[166:169], v209 offset:49152
	ds_read_b128 v[170:173], v209 offset:50176
	ds_read_b128 v[174:177], v209 offset:51200
	ds_read_b128 v[192:195], v209 offset:52224
	ds_read_b128 v[196:199], v209 offset:53248
	ds_read_b128 v[200:203], v209 offset:54272
	ds_read_b128 v[218:221], v209 offset:55296
	ds_read_b128 v[222:225], v209 offset:56320
	global_load_lds_dwordx4 v[8:9], off
	v_lshl_add_u64 v[8:9], v[210:211], 0, s[24:25]
	s_add_i32 m0, s26, 0x2000
	s_add_i32 s26, s37, s54
	global_load_lds_dwordx4 v[8:9], off
	v_lshl_add_u64 v[8:9], v[212:213], 0, s[24:25]
	s_mov_b32 m0, s26
	s_nop 0
	global_load_lds_dwordx4 v[8:9], off
	v_lshl_add_u64 v[8:9], v[214:215], 0, s[24:25]
	s_add_i32 m0, s26, 0x2000
	s_nop 0
	global_load_lds_dwordx4 v[8:9], off
	v_lshl_add_u64 v[8:9], v[226:227], 0, s[24:25]
	s_mov_b32 m0, s59
	s_nop 0
	global_load_lds_dwordx4 v[8:9], off
	v_lshl_add_u64 v[8:9], v[228:229], 0, s[24:25]
	s_mov_b32 m0, s60
	s_nop 0
	global_load_lds_dwordx4 v[8:9], off
	s_waitcnt vmcnt(8)
	s_waitcnt lgkmcnt(0)
	s_barrier
	s_setprio 1
	v_mfma_f32_16x16x32_bf16 v[82:85], v[62:65], v[166:169], v[82:85]
	v_mfma_f32_16x16x32_bf16 v[78:81], v[70:73], v[166:169], v[78:81]
	v_mfma_f32_16x16x32_bf16 v[50:53], v[62:65], v[174:177], v[50:53]
	v_mfma_f32_16x16x32_bf16 v[46:49], v[70:73], v[174:177], v[46:49]
	v_mfma_f32_16x16x32_bf16 v[34:37], v[62:65], v[196:199], v[34:37]
	v_mfma_f32_16x16x32_bf16 v[30:33], v[70:73], v[196:199], v[30:33]
	v_mfma_f32_16x16x32_bf16 v[18:21], v[62:65], v[218:221], v[18:21]
	v_mfma_f32_16x16x32_bf16 v[14:17], v[70:73], v[218:221], v[14:17]
	v_mfma_f32_16x16x32_bf16 v[82:85], v[66:69], v[170:173], v[82:85]
	v_mfma_f32_16x16x32_bf16 v[78:81], v[74:77], v[170:173], v[78:81]
	v_mfma_f32_16x16x32_bf16 v[50:53], v[66:69], v[192:195], v[50:53]
	v_mfma_f32_16x16x32_bf16 v[46:49], v[74:77], v[192:195], v[46:49]
	v_mfma_f32_16x16x32_bf16 v[34:37], v[66:69], v[200:203], v[34:37]
	v_mfma_f32_16x16x32_bf16 v[30:33], v[74:77], v[200:203], v[30:33]
	v_mfma_f32_16x16x32_bf16 v[18:21], v[66:69], v[222:225], v[18:21]
	v_mfma_f32_16x16x32_bf16 v[14:17], v[74:77], v[222:225], v[14:17]
	s_setprio 0
	s_setprio 1
	v_mfma_f32_16x16x32_bf16 v[54:57], v[150:153], v[166:169], v[54:57]
	v_mfma_f32_16x16x32_bf16 v[74:77], v[154:157], v[170:173], v[54:57]
	v_mfma_f32_16x16x32_bf16 v[54:57], v[158:161], v[166:169], v[58:61]
	v_mfma_f32_16x16x32_bf16 v[42:45], v[150:153], v[174:177], v[42:45]
	v_mfma_f32_16x16x32_bf16 v[38:41], v[158:161], v[174:177], v[38:41]
	v_mfma_f32_16x16x32_bf16 v[26:29], v[150:153], v[196:199], v[26:29]
	v_mfma_f32_16x16x32_bf16 v[22:25], v[158:161], v[196:199], v[22:25]
	v_mfma_f32_16x16x32_bf16 v[8:11], v[150:153], v[218:221], v[10:13]
	v_mfma_f32_16x16x32_bf16 v[4:7], v[158:161], v[218:221], v[4:7]
	v_mfma_f32_16x16x32_bf16 v[70:73], v[162:165], v[170:173], v[54:57]
	v_mfma_f32_16x16x32_bf16 v[42:45], v[154:157], v[192:195], v[42:45]
	v_mfma_f32_16x16x32_bf16 v[38:41], v[162:165], v[192:195], v[38:41]
	v_mfma_f32_16x16x32_bf16 v[26:29], v[154:157], v[200:203], v[26:29]
	v_mfma_f32_16x16x32_bf16 v[22:25], v[162:165], v[200:203], v[22:25]
	v_mfma_f32_16x16x32_bf16 v[10:13], v[154:157], v[222:225], v[8:11]
	v_mfma_f32_16x16x32_bf16 v[6:9], v[162:165], v[222:225], v[4:7]
	s_barrier
	s_setprio 0
	s_add_u32 s30, s30, 0x100
	s_addc_u32 s31, s31, 0
	s_add_u32 s23, s23, 0x100
	s_addc_u32 s28, s28, 0
	s_cmp_ge_u32 s29, s19
	s_mov_b32 s26, s29
	s_cbranch_scc0 .LBB0_1865
	s_and_b64 vcc, exec, s[14:15]
	s_cbranch_vccz .LBB0_1868
	s_barrier

.LBB0_2143:
	s_add_i32 s22, s21, 2
	s_add_u32 s23, s26, 0x80
	s_addc_u32 s28, s27, 0
	s_add_i32 s70, 0, 0x10000
	s_cmp_eq_u32 s65, s21
	s_cselect_b32 s31, s3, s28
	s_cselect_b32 s30, s2, s23
	s_cselect_b32 s29, s51, s20
	s_cselect_b32 s28, s50, s19
	s_add_i32 s21, 0, 0x14000
	v_add_u32_e32 v144, s70, v240
	v_add_u32_e32 v160, s21, v240
	ds_read_b128 v[132:135], v144
	ds_read_b128 v[136:139], v144 offset:1024
	ds_read_b128 v[140:143], v144 offset:2048
	ds_read_b128 v[144:147], v144 offset:3072
	ds_read_b128 v[148:151], v160
	ds_read_b128 v[152:155], v160 offset:1024
	ds_read_b128 v[156:159], v160 offset:2048
	ds_read_b128 v[160:163], v160 offset:3072
	v_lshl_add_u64 v[206:207], s[26:27], 0, v[202:203]
	s_add_i32 m0, s58, 0xc000
	ds_read_b128 v[164:167], v242
	ds_read_b128 v[168:171], v242 offset:1024
	ds_read_b128 v[172:175], v242 offset:2048
	ds_read_b128 v[176:179], v242 offset:3072
	ds_read_b128 v[180:183], v242 offset:4096
	ds_read_b128 v[184:187], v242 offset:5120
	ds_read_b128 v[188:191], v242 offset:6144
	ds_read_b128 v[192:195], v242 offset:7168
	global_load_lds_dwordx4 v[206:207], off
	v_lshl_add_u64 v[206:207], s[26:27], 0, v[204:205]
	s_add_i32 m0, s58, 0xe000
	s_nop 0
	global_load_lds_dwordx4 v[206:207], off
	s_waitcnt vmcnt(8)
	s_waitcnt lgkmcnt(0)
	s_barrier
	s_setprio 1
	v_mfma_f32_16x16x32_bf16 v[128:131], v[132:135], v[164:167], v[128:131]
	v_mfma_f32_16x16x32_bf16 v[124:127], v[140:143], v[164:167], v[124:127]
	v_mfma_f32_16x16x32_bf16 v[112:115], v[132:135], v[172:175], v[112:115]
	v_mfma_f32_16x16x32_bf16 v[108:111], v[140:143], v[172:175], v[108:111]
	v_mfma_f32_16x16x32_bf16 v[96:99], v[132:135], v[180:183], v[96:99]
	v_mfma_f32_16x16x32_bf16 v[92:95], v[140:143], v[180:183], v[92:95]
	v_mfma_f32_16x16x32_bf16 v[80:83], v[132:135], v[188:191], v[80:83]
	v_mfma_f32_16x16x32_bf16 v[76:79], v[140:143], v[188:191], v[76:79]
	v_mfma_f32_16x16x32_bf16 v[128:131], v[136:139], v[168:171], v[128:131]
	v_mfma_f32_16x16x32_bf16 v[124:127], v[144:147], v[168:171], v[124:127]
	v_mfma_f32_16x16x32_bf16 v[112:115], v[136:139], v[176:179], v[112:115]
	v_mfma_f32_16x16x32_bf16 v[108:111], v[144:147], v[176:179], v[108:111]
	v_mfma_f32_16x16x32_bf16 v[96:99], v[136:139], v[184:187], v[96:99]
	v_mfma_f32_16x16x32_bf16 v[92:95], v[144:147], v[184:187], v[92:95]
	v_mfma_f32_16x16x32_bf16 v[80:83], v[136:139], v[192:195], v[80:83]
	v_mfma_f32_16x16x32_bf16 v[76:79], v[144:147], v[192:195], v[76:79]
	s_setprio 0
	s_setprio 1
	v_mfma_f32_16x16x32_bf16 v[120:123], v[148:151], v[164:167], v[120:123]
	v_mfma_f32_16x16x32_bf16 v[116:119], v[156:159], v[164:167], v[116:119]
	v_mfma_f32_16x16x32_bf16 v[104:107], v[148:151], v[172:175], v[104:107]
	v_mfma_f32_16x16x32_bf16 v[100:103], v[156:159], v[172:175], v[100:103]
	v_mfma_f32_16x16x32_bf16 v[88:91], v[148:151], v[180:183], v[88:91]
	v_mfma_f32_16x16x32_bf16 v[84:87], v[156:159], v[180:183], v[84:87]
	v_mfma_f32_16x16x32_bf16 v[72:75], v[148:151], v[188:191], v[72:75]
	v_mfma_f32_16x16x32_bf16 v[68:71], v[156:159], v[188:191], v[68:71]
	v_mfma_f32_16x16x32_bf16 v[120:123], v[152:155], v[168:171], v[120:123]
	v_mfma_f32_16x16x32_bf16 v[116:119], v[160:163], v[168:171], v[116:119]
	v_mfma_f32_16x16x32_bf16 v[104:107], v[152:155], v[176:179], v[104:107]
	v_mfma_f32_16x16x32_bf16 v[100:103], v[160:163], v[176:179], v[100:103]
	v_mfma_f32_16x16x32_bf16 v[88:91], v[152:155], v[184:187], v[88:91]
	v_mfma_f32_16x16x32_bf16 v[84:87], v[160:163], v[184:187], v[84:87]
	v_mfma_f32_16x16x32_bf16 v[72:75], v[152:155], v[192:195], v[72:75]
	v_mfma_f32_16x16x32_bf16 v[68:71], v[160:163], v[192:195], v[68:71]
	s_barrier
	s_setprio 0
	s_add_i32 s23, s70, s57
	v_lshl_add_u64 v[206:207], s[28:29], 0, v[2:3]
	s_mov_b32 m0, s23
	ds_read_b128 v[164:167], v242 offset:16384
	ds_read_b128 v[168:171], v242 offset:17408
	ds_read_b128 v[172:175], v242 offset:18432
	ds_read_b128 v[176:179], v242 offset:19456
	ds_read_b128 v[180:183], v242 offset:20480
	ds_read_b128 v[184:187], v242 offset:21504
	ds_read_b128 v[188:191], v242 offset:22528
	ds_read_b128 v[192:195], v242 offset:23552
	global_load_lds_dwordx4 v[206:207], off
	s_add_i32 m0, s23, 0x2000
	v_lshl_add_u64 v[208:209], s[28:29], 0, v[196:197]
	s_add_u32 s28, s28, s14
	s_addc_u32 s29, s29, s15
	s_add_i32 s21, s21, s57
	global_load_lds_dwordx4 v[208:209], off
	v_lshl_add_u64 v[210:211], s[28:29], 0, v[2:3]
	s_mov_b32 m0, s21
	v_lshl_add_u64 v[212:213], s[28:29], 0, v[196:197]
	global_load_lds_dwordx4 v[210:211], off
	s_add_i32 m0, s21, 0x2000
	v_lshl_add_u64 v[214:215], s[30:31], 0, v[200:201]
	global_load_lds_dwordx4 v[212:213], off
	s_mov_b32 m0, s58
	v_lshl_add_u64 v[218:219], s[30:31], 0, v[198:199]
	global_load_lds_dwordx4 v[214:215], off
	s_mov_b32 m0, s59
	s_nop 0
	global_load_lds_dwordx4 v[218:219], off
	s_waitcnt vmcnt(8)
	s_waitcnt lgkmcnt(0)
	s_barrier
	s_setprio 1
	v_mfma_f32_16x16x32_bf16 v[64:67], v[132:135], v[164:167], v[64:67]
	v_mfma_f32_16x16x32_bf16 v[60:63], v[140:143], v[164:167], v[60:63]
	v_mfma_f32_16x16x32_bf16 v[48:51], v[132:135], v[172:175], v[48:51]
	v_mfma_f32_16x16x32_bf16 v[44:47], v[140:143], v[172:175], v[44:47]
	v_mfma_f32_16x16x32_bf16 v[32:35], v[132:135], v[180:183], v[32:35]
	v_mfma_f32_16x16x32_bf16 v[28:31], v[140:143], v[180:183], v[28:31]
	v_mfma_f32_16x16x32_bf16 v[16:19], v[132:135], v[188:191], v[16:19]
	v_mfma_f32_16x16x32_bf16 v[12:15], v[140:143], v[188:191], v[12:15]
	v_mfma_f32_16x16x32_bf16 v[64:67], v[136:139], v[168:171], v[64:67]
	v_mfma_f32_16x16x32_bf16 v[60:63], v[144:147], v[168:171], v[60:63]
	v_mfma_f32_16x16x32_bf16 v[48:51], v[136:139], v[176:179], v[48:51]
	v_mfma_f32_16x16x32_bf16 v[44:47], v[144:147], v[176:179], v[44:47]
	v_mfma_f32_16x16x32_bf16 v[32:35], v[136:139], v[184:187], v[32:35]
	v_mfma_f32_16x16x32_bf16 v[28:31], v[144:147], v[184:187], v[28:31]
	v_mfma_f32_16x16x32_bf16 v[16:19], v[136:139], v[192:195], v[16:19]
	v_mfma_f32_16x16x32_bf16 v[12:15], v[144:147], v[192:195], v[12:15]
	s_setprio 0
	s_setprio 1
	v_mfma_f32_16x16x32_bf16 v[56:59], v[148:151], v[164:167], v[56:59]
	v_mfma_f32_16x16x32_bf16 v[52:55], v[156:159], v[164:167], v[52:55]
	v_mfma_f32_16x16x32_bf16 v[40:43], v[148:151], v[172:175], v[40:43]
	v_mfma_f32_16x16x32_bf16 v[36:39], v[156:159], v[172:175], v[36:39]
	v_mfma_f32_16x16x32_bf16 v[24:27], v[148:151], v[180:183], v[24:27]
	v_mfma_f32_16x16x32_bf16 v[20:23], v[156:159], v[180:183], v[20:23]
	v_mfma_f32_16x16x32_bf16 v[8:11], v[148:151], v[188:191], v[8:11]
	v_mfma_f32_16x16x32_bf16 v[4:7], v[156:159], v[188:191], v[4:7]
	v_mfma_f32_16x16x32_bf16 v[56:59], v[152:155], v[168:171], v[56:59]
	v_mfma_f32_16x16x32_bf16 v[52:55], v[160:163], v[168:171], v[52:55]
	v_mfma_f32_16x16x32_bf16 v[40:43], v[152:155], v[176:179], v[40:43]
	v_mfma_f32_16x16x32_bf16 v[36:39], v[160:163], v[176:179], v[36:39]
	v_mfma_f32_16x16x32_bf16 v[24:27], v[152:155], v[184:187], v[24:27]
	v_mfma_f32_16x16x32_bf16 v[20:23], v[160:163], v[184:187], v[20:23]
	v_mfma_f32_16x16x32_bf16 v[8:11], v[152:155], v[192:195], v[8:11]
	v_mfma_f32_16x16x32_bf16 v[4:7], v[160:163], v[192:195], v[4:7]
	s_barrier
	s_setprio 0
	s_add_i32 s21, 0, 0x18000
	s_add_i32 s23, 0, 0x1c000
	v_add_u32_e32 v144, s21, v240
	v_add_u32_e32 v160, s23, v240
	ds_read_b128 v[132:135], v144
	ds_read_b128 v[136:139], v144 offset:1024
	ds_read_b128 v[140:143], v144 offset:2048
	ds_read_b128 v[144:147], v144 offset:3072
	ds_read_b128 v[148:151], v160
	ds_read_b128 v[152:155], v160 offset:1024
	ds_read_b128 v[156:159], v160 offset:2048
	ds_read_b128 v[160:163], v160 offset:3072
	s_add_u32 s28, s30, s14
	s_addc_u32 s29, s31, s15
	s_mov_b32 m0, s60
	v_lshl_add_u64 v[220:221], s[28:29], 0, v[200:201]
	ds_read_b128 v[164:167], v242 offset:32768
	ds_read_b128 v[168:171], v242 offset:33792
	ds_read_b128 v[172:175], v242 offset:34816
	ds_read_b128 v[176:179], v242 offset:35840
	ds_read_b128 v[180:183], v242 offset:36864
	ds_read_b128 v[184:187], v242 offset:37888
	ds_read_b128 v[188:191], v242 offset:38912
	ds_read_b128 v[192:195], v242 offset:39936
	global_load_lds_dwordx4 v[220:221], off
	v_lshl_add_u64 v[220:221], s[28:29], 0, v[198:199]
	s_mov_b32 m0, s61
	s_nop 0
	global_load_lds_dwordx4 v[220:221], off
	s_waitcnt vmcnt(8)
	s_waitcnt lgkmcnt(0)
	s_barrier
	s_setprio 1
	v_mfma_f32_16x16x32_bf16 v[128:131], v[132:135], v[164:167], v[128:131]
	v_mfma_f32_16x16x32_bf16 v[124:127], v[140:143], v[164:167], v[124:127]
	v_mfma_f32_16x16x32_bf16 v[112:115], v[132:135], v[172:175], v[112:115]
	v_mfma_f32_16x16x32_bf16 v[108:111], v[140:143], v[172:175], v[108:111]
	v_mfma_f32_16x16x32_bf16 v[96:99], v[132:135], v[180:183], v[96:99]
	v_mfma_f32_16x16x32_bf16 v[92:95], v[140:143], v[180:183], v[92:95]
	v_mfma_f32_16x16x32_bf16 v[80:83], v[132:135], v[188:191], v[80:83]
	v_mfma_f32_16x16x32_bf16 v[76:79], v[140:143], v[188:191], v[76:79]
	v_mfma_f32_16x16x32_bf16 v[128:131], v[136:139], v[168:171], v[128:131]
	v_mfma_f32_16x16x32_bf16 v[124:127], v[144:147], v[168:171], v[124:127]
	v_mfma_f32_16x16x32_bf16 v[112:115], v[136:139], v[176:179], v[112:115]
	v_mfma_f32_16x16x32_bf16 v[108:111], v[144:147], v[176:179], v[108:111]
	v_mfma_f32_16x16x32_bf16 v[96:99], v[136:139], v[184:187], v[96:99]
	v_mfma_f32_16x16x32_bf16 v[92:95], v[144:147], v[184:187], v[92:95]
	v_mfma_f32_16x16x32_bf16 v[80:83], v[136:139], v[192:195], v[80:83]
	v_mfma_f32_16x16x32_bf16 v[76:79], v[144:147], v[192:195], v[76:79]
	s_setprio 0
	s_setprio 1
	v_mfma_f32_16x16x32_bf16 v[120:123], v[148:151], v[164:167], v[120:123]
	v_mfma_f32_16x16x32_bf16 v[116:119], v[156:159], v[164:167], v[116:119]
	v_mfma_f32_16x16x32_bf16 v[104:107], v[148:151], v[172:175], v[104:107]
	v_mfma_f32_16x16x32_bf16 v[100:103], v[156:159], v[172:175], v[100:103]
	v_mfma_f32_16x16x32_bf16 v[88:91], v[148:151], v[180:183], v[88:91]
	v_mfma_f32_16x16x32_bf16 v[84:87], v[156:159], v[180:183], v[84:87]
	v_mfma_f32_16x16x32_bf16 v[72:75], v[148:151], v[188:191], v[72:75]
	v_mfma_f32_16x16x32_bf16 v[68:71], v[156:159], v[188:191], v[68:71]
	v_mfma_f32_16x16x32_bf16 v[120:123], v[152:155], v[168:171], v[120:123]
	v_mfma_f32_16x16x32_bf16 v[116:119], v[160:163], v[168:171], v[116:119]
	v_mfma_f32_16x16x32_bf16 v[104:107], v[152:155], v[176:179], v[104:107]
	v_mfma_f32_16x16x32_bf16 v[100:103], v[160:163], v[176:179], v[100:103]
	v_mfma_f32_16x16x32_bf16 v[88:91], v[152:155], v[184:187], v[88:91]
	v_mfma_f32_16x16x32_bf16 v[84:87], v[160:163], v[184:187], v[84:87]
	v_mfma_f32_16x16x32_bf16 v[72:75], v[152:155], v[192:195], v[72:75]
	v_mfma_f32_16x16x32_bf16 v[68:71], v[160:163], v[192:195], v[68:71]
	s_barrier
	s_setprio 0
	s_add_i32 s21, s21, s57
	v_lshl_add_u64 v[206:207], v[206:207], 0, s[24:25]
	s_mov_b32 m0, s21
	ds_read_b128 v[164:167], v242 offset:49152
	ds_read_b128 v[168:171], v242 offset:50176
	ds_read_b128 v[172:175], v242 offset:51200
	ds_read_b128 v[176:179], v242 offset:52224
	ds_read_b128 v[180:183], v242 offset:53248
	ds_read_b128 v[184:187], v242 offset:54272
	ds_read_b128 v[188:191], v242 offset:55296
	ds_read_b128 v[192:195], v242 offset:56320
	global_load_lds_dwordx4 v[206:207], off
	v_lshl_add_u64 v[206:207], v[208:209], 0, s[24:25]
	s_add_i32 m0, s21, 0x2000
	s_add_i32 s21, s23, s57
	global_load_lds_dwordx4 v[206:207], off
	v_lshl_add_u64 v[206:207], v[210:211], 0, s[24:25]
	s_mov_b32 m0, s21
	s_nop 0
	global_load_lds_dwordx4 v[206:207], off
	v_lshl_add_u64 v[206:207], v[212:213], 0, s[24:25]
	s_add_i32 m0, s21, 0x2000
	s_nop 0
	global_load_lds_dwordx4 v[206:207], off
	v_lshl_add_u64 v[206:207], v[214:215], 0, s[24:25]
	s_mov_b32 m0, s63
	s_nop 0
	global_load_lds_dwordx4 v[206:207], off
	v_lshl_add_u64 v[206:207], v[218:219], 0, s[24:25]
	s_mov_b32 m0, s64
	s_nop 0
	global_load_lds_dwordx4 v[206:207], off
	s_waitcnt vmcnt(8)
	s_waitcnt lgkmcnt(0)
	s_barrier
	s_setprio 1
	v_mfma_f32_16x16x32_bf16 v[64:67], v[132:135], v[164:167], v[64:67]
	v_mfma_f32_16x16x32_bf16 v[60:63], v[140:143], v[164:167], v[60:63]
	v_mfma_f32_16x16x32_bf16 v[48:51], v[132:135], v[172:175], v[48:51]
	v_mfma_f32_16x16x32_bf16 v[44:47], v[140:143], v[172:175], v[44:47]
	v_mfma_f32_16x16x32_bf16 v[32:35], v[132:135], v[180:183], v[32:35]
	v_mfma_f32_16x16x32_bf16 v[28:31], v[140:143], v[180:183], v[28:31]
	v_mfma_f32_16x16x32_bf16 v[16:19], v[132:135], v[188:191], v[16:19]
	v_mfma_f32_16x16x32_bf16 v[12:15], v[140:143], v[188:191], v[12:15]
	v_mfma_f32_16x16x32_bf16 v[64:67], v[136:139], v[168:171], v[64:67]
	v_mfma_f32_16x16x32_bf16 v[60:63], v[144:147], v[168:171], v[60:63]
	v_mfma_f32_16x16x32_bf16 v[48:51], v[136:139], v[176:179], v[48:51]
	v_mfma_f32_16x16x32_bf16 v[44:47], v[144:147], v[176:179], v[44:47]
	v_mfma_f32_16x16x32_bf16 v[32:35], v[136:139], v[184:187], v[32:35]
	v_mfma_f32_16x16x32_bf16 v[28:31], v[144:147], v[184:187], v[28:31]
	v_mfma_f32_16x16x32_bf16 v[16:19], v[136:139], v[192:195], v[16:19]
	v_mfma_f32_16x16x32_bf16 v[12:15], v[144:147], v[192:195], v[12:15]
	s_setprio 0
	s_setprio 1
	v_mfma_f32_16x16x32_bf16 v[56:59], v[148:151], v[164:167], v[56:59]
	v_mfma_f32_16x16x32_bf16 v[52:55], v[156:159], v[164:167], v[52:55]
	v_mfma_f32_16x16x32_bf16 v[40:43], v[148:151], v[172:175], v[40:43]
	v_mfma_f32_16x16x32_bf16 v[36:39], v[156:159], v[172:175], v[36:39]
	v_mfma_f32_16x16x32_bf16 v[24:27], v[148:151], v[180:183], v[24:27]
	v_mfma_f32_16x16x32_bf16 v[20:23], v[156:159], v[180:183], v[20:23]
	v_mfma_f32_16x16x32_bf16 v[8:11], v[148:151], v[188:191], v[8:11]
	v_mfma_f32_16x16x32_bf16 v[4:7], v[156:159], v[188:191], v[4:7]
	v_mfma_f32_16x16x32_bf16 v[56:59], v[152:155], v[168:171], v[56:59]
	v_mfma_f32_16x16x32_bf16 v[52:55], v[160:163], v[168:171], v[52:55]
	v_mfma_f32_16x16x32_bf16 v[40:43], v[152:155], v[176:179], v[40:43]
	v_mfma_f32_16x16x32_bf16 v[36:39], v[160:163], v[176:179], v[36:39]
	v_mfma_f32_16x16x32_bf16 v[24:27], v[152:155], v[184:187], v[24:27]
	v_mfma_f32_16x16x32_bf16 v[20:23], v[160:163], v[184:187], v[20:23]
	v_mfma_f32_16x16x32_bf16 v[8:11], v[152:155], v[192:195], v[8:11]
	v_mfma_f32_16x16x32_bf16 v[4:7], v[160:163], v[192:195], v[4:7]
	s_barrier
	s_setprio 0
	s_add_u32 s26, s26, 0x100
	s_addc_u32 s27, s27, 0
	s_add_u32 s19, s19, 0x100
	s_addc_u32 s20, s20, 0
	s_cmp_ge_i32 s22, s62
	s_mov_b32 s21, s22
	s_cbranch_scc0 .LBB0_2143

.LBB0_2304:
	s_add_i32 s72, s50, 2
	s_add_u32 s73, s48, 0x80
	s_addc_u32 s51, s49, 0
	s_add_i32 s76, 0, 0x10000
	s_cmp_eq_u32 s64, s50
	s_cselect_b32 s51, s3, s51
	s_cselect_b32 s50, s2, s73
	v_add_u32_e32 v2, s76, v145
	s_cselect_b32 s75, s47, s71
	s_cselect_b32 s74, s46, s70
	s_add_i32 s73, 0, 0x14000
	ds_read_b128 v[148:151], v2
	ds_read_b128 v[152:155], v2 offset:1024
	ds_read_b128 v[156:159], v2 offset:2048
	ds_read_b128 v[160:163], v2 offset:3072
	v_add_u32_e32 v2, s73, v145
	ds_read_b128 v[164:167], v2
	ds_read_b128 v[168:171], v2 offset:1024
	ds_read_b128 v[172:175], v2 offset:2048
	ds_read_b128 v[176:179], v2 offset:3072
	v_lshl_add_u64 v[212:213], s[48:49], 0, v[140:141]
	s_add_i32 m0, s21, 0xc000
	ds_read_b128 v[180:183], v146
	ds_read_b128 v[184:187], v146 offset:1024
	ds_read_b128 v[188:191], v146 offset:2048
	ds_read_b128 v[192:195], v146 offset:3072
	ds_read_b128 v[196:199], v146 offset:4096
	ds_read_b128 v[200:203], v146 offset:5120
	ds_read_b128 v[204:207], v146 offset:6144
	ds_read_b128 v[208:211], v146 offset:7168
	global_load_lds_dwordx4 v[212:213], off
	v_lshl_add_u64 v[212:213], s[48:49], 0, v[142:143]
	s_add_i32 m0, s21, 0xe000
	s_nop 0
	global_load_lds_dwordx4 v[212:213], off
	s_waitcnt vmcnt(8)
	s_waitcnt lgkmcnt(0)
	s_barrier
	s_setprio 1
	v_mfma_f32_16x16x32_bf16 v[4:7], v[148:151], v[180:183], v[4:7]
	v_mfma_f32_16x16x32_bf16 v[76:79], v[156:159], v[180:183], v[76:79]
	v_mfma_f32_16x16x32_bf16 v[44:47], v[148:151], v[188:191], v[44:47]
	v_mfma_f32_16x16x32_bf16 v[48:51], v[156:159], v[188:191], v[48:51]
	v_mfma_f32_16x16x32_bf16 v[28:31], v[148:151], v[196:199], v[28:31]
	v_mfma_f32_16x16x32_bf16 v[32:35], v[156:159], v[196:199], v[32:35]
	v_mfma_f32_16x16x32_bf16 v[12:15], v[148:151], v[204:207], v[12:15]
	v_mfma_f32_16x16x32_bf16 v[16:19], v[156:159], v[204:207], v[16:19]
	v_mfma_f32_16x16x32_bf16 v[4:7], v[152:155], v[184:187], v[4:7]
	v_mfma_f32_16x16x32_bf16 v[76:79], v[160:163], v[184:187], v[76:79]
	v_mfma_f32_16x16x32_bf16 v[44:47], v[152:155], v[192:195], v[44:47]
	v_mfma_f32_16x16x32_bf16 v[48:51], v[160:163], v[192:195], v[48:51]
	v_mfma_f32_16x16x32_bf16 v[28:31], v[152:155], v[200:203], v[28:31]
	v_mfma_f32_16x16x32_bf16 v[32:35], v[160:163], v[200:203], v[32:35]
	v_mfma_f32_16x16x32_bf16 v[12:15], v[152:155], v[208:211], v[12:15]
	v_mfma_f32_16x16x32_bf16 v[16:19], v[160:163], v[208:211], v[16:19]
	s_setprio 0
	s_setprio 1
	v_mfma_f32_16x16x32_bf16 v[72:75], v[164:167], v[180:183], v[72:75]
	v_mfma_f32_16x16x32_bf16 v[68:71], v[172:175], v[180:183], v[68:71]
	v_mfma_f32_16x16x32_bf16 v[36:39], v[164:167], v[188:191], v[36:39]
	v_mfma_f32_16x16x32_bf16 v[40:43], v[172:175], v[188:191], v[40:43]
	v_mfma_f32_16x16x32_bf16 v[20:23], v[164:167], v[196:199], v[20:23]
	v_mfma_f32_16x16x32_bf16 v[24:27], v[172:175], v[196:199], v[24:27]
	v_mfma_f32_16x16x32_bf16 v[132:135], v[164:167], v[204:207], v[132:135]
	v_mfma_f32_16x16x32_bf16 v[8:11], v[172:175], v[204:207], v[8:11]
	v_mfma_f32_16x16x32_bf16 v[72:75], v[168:171], v[184:187], v[72:75]
	v_mfma_f32_16x16x32_bf16 v[68:71], v[176:179], v[184:187], v[68:71]
	v_mfma_f32_16x16x32_bf16 v[36:39], v[168:171], v[192:195], v[36:39]
	v_mfma_f32_16x16x32_bf16 v[40:43], v[176:179], v[192:195], v[40:43]
	v_mfma_f32_16x16x32_bf16 v[20:23], v[168:171], v[200:203], v[20:23]
	v_mfma_f32_16x16x32_bf16 v[24:27], v[176:179], v[200:203], v[24:27]
	v_mfma_f32_16x16x32_bf16 v[132:135], v[168:171], v[208:211], v[132:135]
	v_mfma_f32_16x16x32_bf16 v[8:11], v[176:179], v[208:211], v[8:11]
	s_barrier
	s_setprio 0
	s_add_i32 s76, s76, s20
	v_lshl_add_u64 v[212:213], s[74:75], 0, v[136:137]
	s_mov_b32 m0, s76
	ds_read_b128 v[180:183], v146 offset:16384
	ds_read_b128 v[184:187], v146 offset:17408
	ds_read_b128 v[188:191], v146 offset:18432
	ds_read_b128 v[192:195], v146 offset:19456
	ds_read_b128 v[196:199], v146 offset:20480
	ds_read_b128 v[200:203], v146 offset:21504
	ds_read_b128 v[204:207], v146 offset:22528
	ds_read_b128 v[208:211], v146 offset:23552
	global_load_lds_dwordx4 v[212:213], off
	s_add_i32 m0, s76, 0x2000
	v_lshl_add_u64 v[214:215], s[74:75], 0, v[88:89]
	s_add_u32 s74, s74, s14
	s_addc_u32 s75, s75, s15
	s_add_i32 s73, s73, s20
	global_load_lds_dwordx4 v[214:215], off
	v_lshl_add_u64 v[218:219], s[74:75], 0, v[136:137]
	s_mov_b32 m0, s73
	v_lshl_add_u64 v[220:221], s[74:75], 0, v[88:89]
	global_load_lds_dwordx4 v[218:219], off
	s_add_i32 m0, s73, 0x2000
	v_lshl_add_u64 v[222:223], s[50:51], 0, v[138:139]
	global_load_lds_dwordx4 v[220:221], off
	s_mov_b32 m0, s21
	v_lshl_add_u64 v[224:225], s[50:51], 0, v[90:91]
	global_load_lds_dwordx4 v[222:223], off
	s_mov_b32 m0, s22
	s_nop 0
	global_load_lds_dwordx4 v[224:225], off
	s_waitcnt vmcnt(8)
	s_waitcnt lgkmcnt(0)
	s_barrier
	s_setprio 1
	v_mfma_f32_16x16x32_bf16 v[124:127], v[148:151], v[180:183], v[124:127]
	v_mfma_f32_16x16x32_bf16 v[128:131], v[156:159], v[180:183], v[128:131]
	v_mfma_f32_16x16x32_bf16 v[108:111], v[148:151], v[188:191], v[108:111]
	v_mfma_f32_16x16x32_bf16 v[112:115], v[156:159], v[188:191], v[112:115]
	v_mfma_f32_16x16x32_bf16 v[92:95], v[148:151], v[196:199], v[92:95]
	v_mfma_f32_16x16x32_bf16 v[96:99], v[156:159], v[196:199], v[96:99]
	v_mfma_f32_16x16x32_bf16 v[60:63], v[148:151], v[204:207], v[60:63]
	v_mfma_f32_16x16x32_bf16 v[64:67], v[156:159], v[204:207], v[64:67]
	v_mfma_f32_16x16x32_bf16 v[124:127], v[152:155], v[184:187], v[124:127]
	v_mfma_f32_16x16x32_bf16 v[128:131], v[160:163], v[184:187], v[128:131]
	v_mfma_f32_16x16x32_bf16 v[108:111], v[152:155], v[192:195], v[108:111]
	v_mfma_f32_16x16x32_bf16 v[112:115], v[160:163], v[192:195], v[112:115]
	v_mfma_f32_16x16x32_bf16 v[92:95], v[152:155], v[200:203], v[92:95]
	v_mfma_f32_16x16x32_bf16 v[96:99], v[160:163], v[200:203], v[96:99]
	v_mfma_f32_16x16x32_bf16 v[60:63], v[152:155], v[208:211], v[60:63]
	v_mfma_f32_16x16x32_bf16 v[64:67], v[160:163], v[208:211], v[64:67]
	s_setprio 0
	s_setprio 1
	v_mfma_f32_16x16x32_bf16 v[116:119], v[164:167], v[180:183], v[116:119]
	v_mfma_f32_16x16x32_bf16 v[120:123], v[172:175], v[180:183], v[120:123]
	v_mfma_f32_16x16x32_bf16 v[100:103], v[164:167], v[188:191], v[100:103]
	v_mfma_f32_16x16x32_bf16 v[104:107], v[172:175], v[188:191], v[104:107]
	v_mfma_f32_16x16x32_bf16 v[80:83], v[164:167], v[196:199], v[80:83]
	v_mfma_f32_16x16x32_bf16 v[84:87], v[172:175], v[196:199], v[84:87]
	v_mfma_f32_16x16x32_bf16 v[52:55], v[164:167], v[204:207], v[52:55]
	v_mfma_f32_16x16x32_bf16 v[56:59], v[172:175], v[204:207], v[56:59]
	v_mfma_f32_16x16x32_bf16 v[116:119], v[168:171], v[184:187], v[116:119]
	v_mfma_f32_16x16x32_bf16 v[120:123], v[176:179], v[184:187], v[120:123]
	v_mfma_f32_16x16x32_bf16 v[100:103], v[168:171], v[192:195], v[100:103]
	v_mfma_f32_16x16x32_bf16 v[104:107], v[176:179], v[192:195], v[104:107]
	v_mfma_f32_16x16x32_bf16 v[80:83], v[168:171], v[200:203], v[80:83]
	v_mfma_f32_16x16x32_bf16 v[84:87], v[176:179], v[200:203], v[84:87]
	v_mfma_f32_16x16x32_bf16 v[52:55], v[168:171], v[208:211], v[52:55]
	v_mfma_f32_16x16x32_bf16 v[56:59], v[176:179], v[208:211], v[56:59]
	s_barrier
	s_setprio 0
	s_add_i32 s73, 0, 0x18000
	v_add_u32_e32 v2, s73, v145
	s_add_i32 s74, 0, 0x1c000
	ds_read_b128 v[148:151], v2
	ds_read_b128 v[152:155], v2 offset:1024
	ds_read_b128 v[156:159], v2 offset:2048
	ds_read_b128 v[160:163], v2 offset:3072
	v_add_u32_e32 v2, s74, v145
	ds_read_b128 v[164:167], v2
	ds_read_b128 v[168:171], v2 offset:1024
	ds_read_b128 v[172:175], v2 offset:2048
	ds_read_b128 v[176:179], v2 offset:3072
	s_add_u32 s50, s50, s14
	s_addc_u32 s51, s51, s15
	s_mov_b32 m0, s23
	v_lshl_add_u64 v[226:227], s[50:51], 0, v[138:139]
	ds_read_b128 v[180:183], v146 offset:32768
	ds_read_b128 v[184:187], v146 offset:33792
	ds_read_b128 v[188:191], v146 offset:34816
	ds_read_b128 v[192:195], v146 offset:35840
	ds_read_b128 v[196:199], v146 offset:36864
	ds_read_b128 v[200:203], v146 offset:37888
	ds_read_b128 v[204:207], v146 offset:38912
	ds_read_b128 v[208:211], v146 offset:39936
	global_load_lds_dwordx4 v[226:227], off
	v_lshl_add_u64 v[226:227], s[50:51], 0, v[90:91]
	s_mov_b32 m0, s28
	s_nop 0
	global_load_lds_dwordx4 v[226:227], off
	s_waitcnt vmcnt(8)
	s_waitcnt lgkmcnt(0)
	s_barrier
	s_setprio 1
	v_mfma_f32_16x16x32_bf16 v[4:7], v[148:151], v[180:183], v[4:7]
	v_mfma_f32_16x16x32_bf16 v[76:79], v[156:159], v[180:183], v[76:79]
	v_mfma_f32_16x16x32_bf16 v[44:47], v[148:151], v[188:191], v[44:47]
	v_mfma_f32_16x16x32_bf16 v[48:51], v[156:159], v[188:191], v[48:51]
	v_mfma_f32_16x16x32_bf16 v[28:31], v[148:151], v[196:199], v[28:31]
	v_mfma_f32_16x16x32_bf16 v[32:35], v[156:159], v[196:199], v[32:35]
	v_mfma_f32_16x16x32_bf16 v[12:15], v[148:151], v[204:207], v[12:15]
	v_mfma_f32_16x16x32_bf16 v[16:19], v[156:159], v[204:207], v[16:19]
	v_mfma_f32_16x16x32_bf16 v[4:7], v[152:155], v[184:187], v[4:7]
	v_mfma_f32_16x16x32_bf16 v[76:79], v[160:163], v[184:187], v[76:79]
	v_mfma_f32_16x16x32_bf16 v[44:47], v[152:155], v[192:195], v[44:47]
	v_mfma_f32_16x16x32_bf16 v[48:51], v[160:163], v[192:195], v[48:51]
	v_mfma_f32_16x16x32_bf16 v[28:31], v[152:155], v[200:203], v[28:31]
	v_mfma_f32_16x16x32_bf16 v[32:35], v[160:163], v[200:203], v[32:35]
	v_mfma_f32_16x16x32_bf16 v[12:15], v[152:155], v[208:211], v[12:15]
	v_mfma_f32_16x16x32_bf16 v[16:19], v[160:163], v[208:211], v[16:19]
	s_setprio 0
	s_setprio 1
	v_mfma_f32_16x16x32_bf16 v[72:75], v[164:167], v[180:183], v[72:75]
	v_mfma_f32_16x16x32_bf16 v[68:71], v[172:175], v[180:183], v[68:71]
	v_mfma_f32_16x16x32_bf16 v[36:39], v[164:167], v[188:191], v[36:39]
	v_mfma_f32_16x16x32_bf16 v[40:43], v[172:175], v[188:191], v[40:43]
	v_mfma_f32_16x16x32_bf16 v[20:23], v[164:167], v[196:199], v[20:23]
	v_mfma_f32_16x16x32_bf16 v[24:27], v[172:175], v[196:199], v[24:27]
	v_mfma_f32_16x16x32_bf16 v[132:135], v[164:167], v[204:207], v[132:135]
	v_mfma_f32_16x16x32_bf16 v[8:11], v[172:175], v[204:207], v[8:11]
	v_mfma_f32_16x16x32_bf16 v[72:75], v[168:171], v[184:187], v[72:75]
	v_mfma_f32_16x16x32_bf16 v[68:71], v[176:179], v[184:187], v[68:71]
	v_mfma_f32_16x16x32_bf16 v[36:39], v[168:171], v[192:195], v[36:39]
	v_mfma_f32_16x16x32_bf16 v[40:43], v[176:179], v[192:195], v[40:43]
	v_mfma_f32_16x16x32_bf16 v[20:23], v[168:171], v[200:203], v[20:23]
	v_mfma_f32_16x16x32_bf16 v[24:27], v[176:179], v[200:203], v[24:27]
	v_mfma_f32_16x16x32_bf16 v[132:135], v[168:171], v[208:211], v[132:135]
	v_mfma_f32_16x16x32_bf16 v[8:11], v[176:179], v[208:211], v[8:11]
	s_barrier
	s_setprio 0
	s_add_i32 s50, s73, s20
	v_lshl_add_u64 v[212:213], v[212:213], 0, s[24:25]
	s_mov_b32 m0, s50
	ds_read_b128 v[180:183], v146 offset:49152
	ds_read_b128 v[184:187], v146 offset:50176
	ds_read_b128 v[188:191], v146 offset:51200
	ds_read_b128 v[192:195], v146 offset:52224
	ds_read_b128 v[196:199], v146 offset:53248
	ds_read_b128 v[200:203], v146 offset:54272
	ds_read_b128 v[204:207], v146 offset:55296
	ds_read_b128 v[208:211], v146 offset:56320
	global_load_lds_dwordx4 v[212:213], off
	v_lshl_add_u64 v[212:213], v[214:215], 0, s[24:25]
	s_add_i32 m0, s50, 0x2000
	s_add_i32 s50, s74, s20
	global_load_lds_dwordx4 v[212:213], off
	v_lshl_add_u64 v[212:213], v[218:219], 0, s[24:25]
	s_mov_b32 m0, s50
	s_nop 0
	global_load_lds_dwordx4 v[212:213], off
	v_lshl_add_u64 v[212:213], v[220:221], 0, s[24:25]
	s_add_i32 m0, s50, 0x2000
	s_nop 0
	global_load_lds_dwordx4 v[212:213], off
	v_lshl_add_u64 v[212:213], v[222:223], 0, s[24:25]
	s_mov_b32 m0, s29
	s_nop 0
	global_load_lds_dwordx4 v[212:213], off
	v_lshl_add_u64 v[212:213], v[224:225], 0, s[24:25]
	s_mov_b32 m0, s62
	s_nop 0
	global_load_lds_dwordx4 v[212:213], off
	s_waitcnt vmcnt(8)
	s_waitcnt lgkmcnt(0)
	s_barrier
	s_setprio 1
	v_mfma_f32_16x16x32_bf16 v[124:127], v[148:151], v[180:183], v[124:127]
	v_mfma_f32_16x16x32_bf16 v[128:131], v[156:159], v[180:183], v[128:131]
	v_mfma_f32_16x16x32_bf16 v[108:111], v[148:151], v[188:191], v[108:111]
	v_mfma_f32_16x16x32_bf16 v[112:115], v[156:159], v[188:191], v[112:115]
	v_mfma_f32_16x16x32_bf16 v[92:95], v[148:151], v[196:199], v[92:95]
	v_mfma_f32_16x16x32_bf16 v[96:99], v[156:159], v[196:199], v[96:99]
	v_mfma_f32_16x16x32_bf16 v[60:63], v[148:151], v[204:207], v[60:63]
	v_mfma_f32_16x16x32_bf16 v[64:67], v[156:159], v[204:207], v[64:67]
	v_mfma_f32_16x16x32_bf16 v[124:127], v[152:155], v[184:187], v[124:127]
	v_mfma_f32_16x16x32_bf16 v[128:131], v[160:163], v[184:187], v[128:131]
	v_mfma_f32_16x16x32_bf16 v[108:111], v[152:155], v[192:195], v[108:111]
	v_mfma_f32_16x16x32_bf16 v[112:115], v[160:163], v[192:195], v[112:115]
	v_mfma_f32_16x16x32_bf16 v[92:95], v[152:155], v[200:203], v[92:95]
	v_mfma_f32_16x16x32_bf16 v[96:99], v[160:163], v[200:203], v[96:99]
	v_mfma_f32_16x16x32_bf16 v[60:63], v[152:155], v[208:211], v[60:63]
	v_mfma_f32_16x16x32_bf16 v[64:67], v[160:163], v[208:211], v[64:67]
	s_setprio 0
	s_setprio 1
	v_mfma_f32_16x16x32_bf16 v[116:119], v[164:167], v[180:183], v[116:119]
	v_mfma_f32_16x16x32_bf16 v[120:123], v[172:175], v[180:183], v[120:123]
	v_mfma_f32_16x16x32_bf16 v[100:103], v[164:167], v[188:191], v[100:103]
	v_mfma_f32_16x16x32_bf16 v[104:107], v[172:175], v[188:191], v[104:107]
	v_mfma_f32_16x16x32_bf16 v[80:83], v[164:167], v[196:199], v[80:83]
	v_mfma_f32_16x16x32_bf16 v[84:87], v[172:175], v[196:199], v[84:87]
	v_mfma_f32_16x16x32_bf16 v[52:55], v[164:167], v[204:207], v[52:55]
	v_mfma_f32_16x16x32_bf16 v[56:59], v[172:175], v[204:207], v[56:59]
	v_mfma_f32_16x16x32_bf16 v[116:119], v[168:171], v[184:187], v[116:119]
	v_mfma_f32_16x16x32_bf16 v[120:123], v[176:179], v[184:187], v[120:123]
	v_mfma_f32_16x16x32_bf16 v[100:103], v[168:171], v[192:195], v[100:103]
	v_mfma_f32_16x16x32_bf16 v[104:107], v[176:179], v[192:195], v[104:107]
	v_mfma_f32_16x16x32_bf16 v[80:83], v[168:171], v[200:203], v[80:83]
	v_mfma_f32_16x16x32_bf16 v[84:87], v[176:179], v[200:203], v[84:87]
	v_mfma_f32_16x16x32_bf16 v[52:55], v[168:171], v[208:211], v[52:55]
	v_mfma_f32_16x16x32_bf16 v[56:59], v[176:179], v[208:211], v[56:59]
	s_barrier
	s_setprio 0
	s_add_u32 s48, s48, 0x100
	s_addc_u32 s49, s49, 0
	s_add_u32 s70, s70, 0x100
	s_addc_u32 s71, s71, 0
	s_cmp_ge_i32 s72, s63
	s_mov_b32 s50, s72
	s_cbranch_scc0 .LBB0_2304
	s_mov_b64 s[72:73], 0x2000
	s_mov_b64 s[74:75], 0x40000
	s_and_b64 vcc, exec, s[44:45]
	s_cbranch_vccnz .LBB0_2310

.LBB0_3265:
	s_andn2_b64 vcc, exec, s[14:15]
	s_cbranch_vccnz .LBB0_3268
	v_mov_b32_e32 v141, v3
	v_mov_b32_e32 v145, v3
	s_add_u32 s19, s26, 0x100
	s_addc_u32 s20, s27, 0
	v_lshl_add_u64 v[148:149], s[36:37], 0, v[140:141]
	v_lshl_add_u64 v[150:151], s[36:37], 0, v[144:145]
	s_mov_b32 s21, 0
	s_mov_b64 s[26:27], 0
	s_cmp_eq_u32 s56, s21
	s_cselect_b64 vcc, -1, 0
	s_add_i32 s21, s21, 2
	s_add_u32 s30, s26, 0x100
	s_addc_u32 s31, s27, 0
	s_and_b64 s[22:23], vcc, exec
	s_cselect_b32 s23, 0, s30
	s_cselect_b32 s22, 0, s31
	s_add_u32 s40, s2, s23
	s_addc_u32 s41, s3, s22
	s_add_u32 s28, s19, s26
	s_addc_u32 s29, s20, s27
	s_add_i32 s65, 0, 0x10000
	s_and_b64 s[22:23], vcc, exec
	v_add_u32_e32 v141, s65, v147
	s_cselect_b32 s23, s43, s29
	s_cselect_b32 s22, s42, s28
	s_add_i32 s28, 0, 0x14000
	ds_read_b128 v[158:161], v141
	ds_read_b128 v[162:165], v141 offset:1024
	ds_read_b128 v[166:169], v141 offset:2048
	ds_read_b128 v[170:173], v141 offset:3072
	v_add_u32_e32 v141, s28, v147
	ds_read_b128 v[174:177], v141
	ds_read_b128 v[178:181], v141 offset:1024
	ds_read_b128 v[182:185], v141 offset:2048
	ds_read_b128 v[186:189], v141 offset:3072
	v_cndmask_b32_e32 v2, v142, v157, vcc
	v_cndmask_b32_e32 v141, v140, v156, vcc
	v_cndmask_b32_e32 v210, v146, v154, vcc
	v_cndmask_b32_e32 v145, v144, v155, vcc
	v_lshl_add_u64 v[212:213], v[148:149], 0, s[26:27]
	s_add_i32 m0, s49, 0xc000
	ds_read_b128 v[190:193], v153
	ds_read_b128 v[194:197], v153 offset:1024
	ds_read_b128 v[198:201], v153 offset:2048
	ds_read_b128 v[202:205], v153 offset:3072
	ds_read_b128 v[206:209], v153 offset:4096
	ds_read_b128 v[218:221], v153 offset:5120
	ds_read_b128 v[222:225], v153 offset:6144
	ds_read_b128 v[226:229], v153 offset:7168
	global_load_lds_dwordx4 v[212:213], off
	v_lshl_add_u64 v[212:213], v[150:151], 0, s[26:27]
	s_add_i32 m0, s49, 0xe000
	s_nop 0
	global_load_lds_dwordx4 v[212:213], off
	s_waitcnt vmcnt(8)
	s_waitcnt lgkmcnt(0)
	s_barrier
	s_setprio 1
	v_mfma_f32_16x16x32_bf16 v[124:127], v[158:161], v[190:193], 0
	v_mfma_f32_16x16x32_bf16 v[120:123], v[166:169], v[190:193], 0
	v_mfma_f32_16x16x32_bf16 v[112:115], v[158:161], v[198:201], 0
	v_mfma_f32_16x16x32_bf16 v[104:107], v[166:169], v[198:201], 0
	v_mfma_f32_16x16x32_bf16 v[96:99], v[158:161], v[206:209], 0
	v_mfma_f32_16x16x32_bf16 v[88:91], v[166:169], v[206:209], 0
	v_mfma_f32_16x16x32_bf16 v[80:83], v[158:161], v[222:225], 0
	v_mfma_f32_16x16x32_bf16 v[72:75], v[166:169], v[222:225], 0
	v_mfma_f32_16x16x32_bf16 v[124:127], v[162:165], v[194:197], v[124:127]
	v_mfma_f32_16x16x32_bf16 v[120:123], v[170:173], v[194:197], v[120:123]
	v_mfma_f32_16x16x32_bf16 v[112:115], v[162:165], v[202:205], v[112:115]
	v_mfma_f32_16x16x32_bf16 v[104:107], v[170:173], v[202:205], v[104:107]
	v_mfma_f32_16x16x32_bf16 v[96:99], v[162:165], v[218:221], v[96:99]
	v_mfma_f32_16x16x32_bf16 v[88:91], v[170:173], v[218:221], v[88:91]
	v_mfma_f32_16x16x32_bf16 v[80:83], v[162:165], v[226:229], v[80:83]
	v_mfma_f32_16x16x32_bf16 v[72:75], v[170:173], v[226:229], v[72:75]
	s_setprio 0
	s_setprio 1
	v_mfma_f32_16x16x32_bf16 v[128:131], v[174:177], v[190:193], 0
	v_mfma_f32_16x16x32_bf16 v[116:119], v[182:185], v[190:193], 0
	v_mfma_f32_16x16x32_bf16 v[108:111], v[174:177], v[198:201], 0
	v_mfma_f32_16x16x32_bf16 v[100:103], v[182:185], v[198:201], 0
	v_mfma_f32_16x16x32_bf16 v[92:95], v[174:177], v[206:209], 0
	v_mfma_f32_16x16x32_bf16 v[84:87], v[182:185], v[206:209], 0
	v_mfma_f32_16x16x32_bf16 v[76:79], v[174:177], v[222:225], 0
	v_mfma_f32_16x16x32_bf16 v[68:71], v[182:185], v[222:225], 0
	v_mfma_f32_16x16x32_bf16 v[128:131], v[178:181], v[194:197], v[128:131]
	v_mfma_f32_16x16x32_bf16 v[116:119], v[186:189], v[194:197], v[116:119]
	v_mfma_f32_16x16x32_bf16 v[108:111], v[178:181], v[202:205], v[108:111]
	v_mfma_f32_16x16x32_bf16 v[100:103], v[186:189], v[202:205], v[100:103]
	v_mfma_f32_16x16x32_bf16 v[92:95], v[178:181], v[218:221], v[92:95]
	v_mfma_f32_16x16x32_bf16 v[84:87], v[186:189], v[218:221], v[84:87]
	v_mfma_f32_16x16x32_bf16 v[76:79], v[178:181], v[226:229], v[76:79]
	v_mfma_f32_16x16x32_bf16 v[68:71], v[186:189], v[226:229], v[68:71]
	s_barrier
	s_setprio 0
	s_add_i32 s26, s65, s47
	v_lshl_add_u64 v[212:213], s[22:23], 0, v[138:139]
	s_mov_b32 m0, s26
	ds_read_b128 v[190:193], v153 offset:16384
	ds_read_b128 v[194:197], v153 offset:17408
	ds_read_b128 v[198:201], v153 offset:18432
	ds_read_b128 v[202:205], v153 offset:19456
	ds_read_b128 v[206:209], v153 offset:20480
	ds_read_b128 v[218:221], v153 offset:21504
	ds_read_b128 v[222:225], v153 offset:22528
	ds_read_b128 v[226:229], v153 offset:23552
	global_load_lds_dwordx4 v[212:213], off
	s_add_i32 m0, s26, 0x2000
	v_lshl_add_u64 v[214:215], s[22:23], 0, v[136:137]
	s_add_u32 s22, s22, s6
	s_addc_u32 s23, s23, s7
	s_add_i32 s26, s28, s47
	global_load_lds_dwordx4 v[214:215], off
	v_lshl_add_u64 v[230:231], s[22:23], 0, v[138:139]
	s_mov_b32 m0, s26
	v_lshl_add_u64 v[240:241], s[22:23], 0, v[136:137]
	global_load_lds_dwordx4 v[230:231], off
	s_add_i32 m0, s26, 0x2000
	v_mov_b32_e32 v211, v3
	global_load_lds_dwordx4 v[240:241], off
	s_mov_b32 m0, s49
	v_lshl_add_u64 v[242:243], s[40:41], 0, v[2:3]
	global_load_lds_dwordx4 v2, s[40:41]
	s_mov_b32 m0, s50
	s_nop 0
	global_load_lds_dwordx4 v210, s[40:41]
	s_waitcnt vmcnt(8)
	s_waitcnt lgkmcnt(0)
	v_lshl_add_u64 v[210:211], s[40:41], 0, v[210:211]
	s_barrier
	s_setprio 1
	s_waitcnt lgkmcnt(0)
	v_mfma_f32_16x16x32_bf16 v[64:67], v[158:161], v[190:193], 0
	v_mfma_f32_16x16x32_bf16 v[56:59], v[166:169], v[190:193], 0
	v_mfma_f32_16x16x32_bf16 v[48:51], v[158:161], v[198:201], 0
	v_mfma_f32_16x16x32_bf16 v[40:43], v[166:169], v[198:201], 0
	v_mfma_f32_16x16x32_bf16 v[32:35], v[158:161], v[206:209], 0
	v_mfma_f32_16x16x32_bf16 v[24:27], v[166:169], v[206:209], 0
	v_mfma_f32_16x16x32_bf16 v[16:19], v[158:161], v[222:225], 0
	v_mfma_f32_16x16x32_bf16 v[8:11], v[166:169], v[222:225], 0
	v_mfma_f32_16x16x32_bf16 v[64:67], v[162:165], v[194:197], v[64:67]
	v_mfma_f32_16x16x32_bf16 v[56:59], v[170:173], v[194:197], v[56:59]
	v_mfma_f32_16x16x32_bf16 v[48:51], v[162:165], v[202:205], v[48:51]
	v_mfma_f32_16x16x32_bf16 v[40:43], v[170:173], v[202:205], v[40:43]
	v_mfma_f32_16x16x32_bf16 v[32:35], v[162:165], v[218:221], v[32:35]
	v_mfma_f32_16x16x32_bf16 v[24:27], v[170:173], v[218:221], v[24:27]
	v_mfma_f32_16x16x32_bf16 v[16:19], v[162:165], v[226:229], v[16:19]
	v_mfma_f32_16x16x32_bf16 v[8:11], v[170:173], v[226:229], v[8:11]
	s_setprio 0
	s_setprio 1
	v_mfma_f32_16x16x32_bf16 v[60:63], v[174:177], v[190:193], 0
	v_mfma_f32_16x16x32_bf16 v[52:55], v[182:185], v[190:193], 0
	v_mfma_f32_16x16x32_bf16 v[44:47], v[174:177], v[198:201], 0
	v_mfma_f32_16x16x32_bf16 v[36:39], v[182:185], v[198:201], 0
	v_mfma_f32_16x16x32_bf16 v[28:31], v[174:177], v[206:209], 0
	v_mfma_f32_16x16x32_bf16 v[20:23], v[182:185], v[206:209], 0
	v_mfma_f32_16x16x32_bf16 v[12:15], v[174:177], v[222:225], 0
	v_mfma_f32_16x16x32_bf16 v[4:7], v[182:185], v[222:225], 0
	v_mfma_f32_16x16x32_bf16 v[60:63], v[178:181], v[194:197], v[60:63]
	v_mfma_f32_16x16x32_bf16 v[52:55], v[186:189], v[194:197], v[52:55]
	v_mfma_f32_16x16x32_bf16 v[44:47], v[178:181], v[202:205], v[44:47]
	v_mfma_f32_16x16x32_bf16 v[36:39], v[186:189], v[202:205], v[36:39]
	v_mfma_f32_16x16x32_bf16 v[28:31], v[178:181], v[218:221], v[28:31]
	v_mfma_f32_16x16x32_bf16 v[20:23], v[186:189], v[218:221], v[20:23]
	v_mfma_f32_16x16x32_bf16 v[12:15], v[178:181], v[226:229], v[12:15]
	v_mfma_f32_16x16x32_bf16 v[4:7], v[186:189], v[226:229], v[4:7]
	s_barrier
	s_setprio 0
	s_add_i32 s22, 0, 0x18000
	v_add_u32_e32 v2, s22, v147
	s_add_i32 s23, 0, 0x1c000
	ds_read_b128 v[158:161], v2
	ds_read_b128 v[162:165], v2 offset:1024
	ds_read_b128 v[166:169], v2 offset:2048
	ds_read_b128 v[170:173], v2 offset:3072
	v_add_u32_e32 v2, s23, v147
	ds_read_b128 v[174:177], v2
	ds_read_b128 v[178:181], v2 offset:1024
	ds_read_b128 v[182:185], v2 offset:2048
	ds_read_b128 v[186:189], v2 offset:3072
	s_mov_b32 m0, s51
	ds_read_b128 v[190:193], v153 offset:32768
	ds_read_b128 v[194:197], v153 offset:33792
	ds_read_b128 v[198:201], v153 offset:34816
	ds_read_b128 v[202:205], v153 offset:35840
	ds_read_b128 v[206:209], v153 offset:36864
	ds_read_b128 v[218:221], v153 offset:37888
	ds_read_b128 v[222:225], v153 offset:38912
	ds_read_b128 v[226:229], v153 offset:39936
	global_load_lds_dwordx4 v141, s[40:41]
	s_mov_b32 m0, s52
	s_nop 0
	global_load_lds_dwordx4 v145, s[40:41]
	s_waitcnt vmcnt(8)
	s_waitcnt lgkmcnt(0)
	s_barrier
	s_setprio 1
	v_mfma_f32_16x16x32_bf16 v[124:127], v[158:161], v[190:193], v[124:127]
	v_mfma_f32_16x16x32_bf16 v[120:123], v[166:169], v[190:193], v[120:123]
	v_mfma_f32_16x16x32_bf16 v[112:115], v[158:161], v[198:201], v[112:115]
	v_mfma_f32_16x16x32_bf16 v[104:107], v[166:169], v[198:201], v[104:107]
	v_mfma_f32_16x16x32_bf16 v[96:99], v[158:161], v[206:209], v[96:99]
	v_mfma_f32_16x16x32_bf16 v[88:91], v[166:169], v[206:209], v[88:91]
	v_mfma_f32_16x16x32_bf16 v[80:83], v[158:161], v[222:225], v[80:83]
	v_mfma_f32_16x16x32_bf16 v[72:75], v[166:169], v[222:225], v[72:75]
	v_mfma_f32_16x16x32_bf16 v[124:127], v[162:165], v[194:197], v[124:127]
	v_mfma_f32_16x16x32_bf16 v[120:123], v[170:173], v[194:197], v[120:123]
	v_mfma_f32_16x16x32_bf16 v[112:115], v[162:165], v[202:205], v[112:115]
	v_mfma_f32_16x16x32_bf16 v[104:107], v[170:173], v[202:205], v[104:107]
	v_mfma_f32_16x16x32_bf16 v[96:99], v[162:165], v[218:221], v[96:99]
	v_mfma_f32_16x16x32_bf16 v[88:91], v[170:173], v[218:221], v[88:91]
	v_mfma_f32_16x16x32_bf16 v[80:83], v[162:165], v[226:229], v[80:83]
	v_mfma_f32_16x16x32_bf16 v[72:75], v[170:173], v[226:229], v[72:75]
	s_setprio 0
	s_setprio 1
	v_mfma_f32_16x16x32_bf16 v[128:131], v[174:177], v[190:193], v[128:131]
	v_mfma_f32_16x16x32_bf16 v[116:119], v[182:185], v[190:193], v[116:119]
	v_mfma_f32_16x16x32_bf16 v[108:111], v[174:177], v[198:201], v[108:111]
	v_mfma_f32_16x16x32_bf16 v[100:103], v[182:185], v[198:201], v[100:103]
	v_mfma_f32_16x16x32_bf16 v[92:95], v[174:177], v[206:209], v[92:95]
	v_mfma_f32_16x16x32_bf16 v[84:87], v[182:185], v[206:209], v[84:87]
	v_mfma_f32_16x16x32_bf16 v[76:79], v[174:177], v[222:225], v[76:79]
	v_mfma_f32_16x16x32_bf16 v[68:71], v[182:185], v[222:225], v[68:71]
	v_mfma_f32_16x16x32_bf16 v[128:131], v[178:181], v[194:197], v[128:131]
	v_mfma_f32_16x16x32_bf16 v[116:119], v[186:189], v[194:197], v[116:119]
	v_mfma_f32_16x16x32_bf16 v[108:111], v[178:181], v[202:205], v[108:111]
	v_mfma_f32_16x16x32_bf16 v[100:103], v[186:189], v[202:205], v[100:103]
	v_mfma_f32_16x16x32_bf16 v[92:95], v[178:181], v[218:221], v[92:95]
	v_mfma_f32_16x16x32_bf16 v[84:87], v[186:189], v[218:221], v[84:87]
	v_mfma_f32_16x16x32_bf16 v[76:79], v[178:181], v[226:229], v[76:79]
	v_mfma_f32_16x16x32_bf16 v[68:71], v[186:189], v[226:229], v[68:71]
	s_barrier
	s_setprio 0
	s_add_i32 s22, s22, s47
	v_lshl_add_u64 v[212:213], v[212:213], 0, s[24:25]
	s_mov_b32 m0, s22
	ds_read_b128 v[190:193], v153 offset:49152
	ds_read_b128 v[194:197], v153 offset:50176
	ds_read_b128 v[198:201], v153 offset:51200
	ds_read_b128 v[202:205], v153 offset:52224
	ds_read_b128 v[206:209], v153 offset:53248
	ds_read_b128 v[218:221], v153 offset:54272
	ds_read_b128 v[222:225], v153 offset:55296
	ds_read_b128 v[226:229], v153 offset:56320
	global_load_lds_dwordx4 v[212:213], off
	v_lshl_add_u64 v[212:213], v[214:215], 0, s[24:25]
	s_add_i32 m0, s22, 0x2000
	s_add_i32 s22, s23, s47
	global_load_lds_dwordx4 v[212:213], off
	v_lshl_add_u64 v[212:213], v[230:231], 0, s[24:25]
	s_mov_b32 m0, s22
	v_lshl_add_u64 v[210:211], v[210:211], 0, s[24:25]
	global_load_lds_dwordx4 v[212:213], off
	v_lshl_add_u64 v[212:213], v[240:241], 0, s[24:25]
	s_add_i32 m0, s22, 0x2000
	s_nop 0
	global_load_lds_dwordx4 v[212:213], off
	v_lshl_add_u64 v[212:213], v[242:243], 0, s[24:25]
	s_mov_b32 m0, s53
	s_nop 0
	global_load_lds_dwordx4 v[212:213], off
	s_mov_b32 m0, s54
	s_nop 0
	global_load_lds_dwordx4 v[210:211], off
	s_waitcnt vmcnt(8)
	s_waitcnt lgkmcnt(0)
	s_barrier
	s_setprio 1
	v_mfma_f32_16x16x32_bf16 v[64:67], v[158:161], v[190:193], v[64:67]
	v_mfma_f32_16x16x32_bf16 v[56:59], v[166:169], v[190:193], v[56:59]
	v_mfma_f32_16x16x32_bf16 v[48:51], v[158:161], v[198:201], v[48:51]
	v_mfma_f32_16x16x32_bf16 v[40:43], v[166:169], v[198:201], v[40:43]
	v_mfma_f32_16x16x32_bf16 v[32:35], v[158:161], v[206:209], v[32:35]
	v_mfma_f32_16x16x32_bf16 v[24:27], v[166:169], v[206:209], v[24:27]
	v_mfma_f32_16x16x32_bf16 v[16:19], v[158:161], v[222:225], v[16:19]
	v_mfma_f32_16x16x32_bf16 v[8:11], v[166:169], v[222:225], v[8:11]
	v_mfma_f32_16x16x32_bf16 v[64:67], v[162:165], v[194:197], v[64:67]
	v_mfma_f32_16x16x32_bf16 v[56:59], v[170:173], v[194:197], v[56:59]
	v_mfma_f32_16x16x32_bf16 v[48:51], v[162:165], v[202:205], v[48:51]
	v_mfma_f32_16x16x32_bf16 v[40:43], v[170:173], v[202:205], v[40:43]
	v_mfma_f32_16x16x32_bf16 v[32:35], v[162:165], v[218:221], v[32:35]
	v_mfma_f32_16x16x32_bf16 v[24:27], v[170:173], v[218:221], v[24:27]
	v_mfma_f32_16x16x32_bf16 v[16:19], v[162:165], v[226:229], v[16:19]
	v_mfma_f32_16x16x32_bf16 v[8:11], v[170:173], v[226:229], v[8:11]
	s_setprio 0
	s_setprio 1
	v_mfma_f32_16x16x32_bf16 v[60:63], v[174:177], v[190:193], v[60:63]
	v_mfma_f32_16x16x32_bf16 v[52:55], v[182:185], v[190:193], v[52:55]
	v_mfma_f32_16x16x32_bf16 v[44:47], v[174:177], v[198:201], v[44:47]
	v_mfma_f32_16x16x32_bf16 v[36:39], v[182:185], v[198:201], v[36:39]
	v_mfma_f32_16x16x32_bf16 v[28:31], v[174:177], v[206:209], v[28:31]
	v_mfma_f32_16x16x32_bf16 v[20:23], v[182:185], v[206:209], v[20:23]
	v_mfma_f32_16x16x32_bf16 v[12:15], v[174:177], v[222:225], v[12:15]
	v_mfma_f32_16x16x32_bf16 v[4:7], v[182:185], v[222:225], v[4:7]
	v_mfma_f32_16x16x32_bf16 v[60:63], v[178:181], v[194:197], v[60:63]
	v_mfma_f32_16x16x32_bf16 v[52:55], v[186:189], v[194:197], v[52:55]
	v_mfma_f32_16x16x32_bf16 v[44:47], v[178:181], v[202:205], v[44:47]
	v_mfma_f32_16x16x32_bf16 v[36:39], v[186:189], v[202:205], v[36:39]
	v_mfma_f32_16x16x32_bf16 v[28:31], v[178:181], v[218:221], v[28:31]
	v_mfma_f32_16x16x32_bf16 v[20:23], v[186:189], v[218:221], v[20:23]
	v_mfma_f32_16x16x32_bf16 v[12:15], v[178:181], v[226:229], v[12:15]
	v_mfma_f32_16x16x32_bf16 v[4:7], v[186:189], v[226:229], v[4:7]
	s_barrier
	s_setprio 0
	s_cmp_ge_i32 s21, s55
	s_mov_b64 s[26:27], s[30:31]
	s_cbranch_scc1 .LBB0_3268
.LBB0_3267:
	s_cmp_eq_u32 s56, s21
	s_cselect_b64 vcc, -1, 0
	s_add_i32 s21, s21, 2
	s_add_u32 s30, s26, 0x100
	s_addc_u32 s31, s27, 0
	s_and_b64 s[22:23], vcc, exec
	s_cselect_b32 s23, 0, s30
	s_cselect_b32 s22, 0, s31
	s_add_u32 s40, s2, s23
	s_addc_u32 s41, s3, s22
	s_add_u32 s28, s19, s26
	s_addc_u32 s29, s20, s27
	s_add_i32 s65, 0, 0x10000
	s_and_b64 s[22:23], vcc, exec
	v_add_u32_e32 v141, s65, v147
	s_cselect_b32 s23, s43, s29
	s_cselect_b32 s22, s42, s28
	s_add_i32 s28, 0, 0x14000
	ds_read_b128 v[158:161], v141
	ds_read_b128 v[162:165], v141 offset:1024
	ds_read_b128 v[166:169], v141 offset:2048
	ds_read_b128 v[170:173], v141 offset:3072
	v_add_u32_e32 v141, s28, v147
	ds_read_b128 v[174:177], v141
	ds_read_b128 v[178:181], v141 offset:1024
	ds_read_b128 v[182:185], v141 offset:2048
	ds_read_b128 v[186:189], v141 offset:3072
	v_cndmask_b32_e32 v2, v142, v157, vcc
	v_cndmask_b32_e32 v141, v140, v156, vcc
	v_cndmask_b32_e32 v210, v146, v154, vcc
	v_cndmask_b32_e32 v145, v144, v155, vcc
	v_lshl_add_u64 v[212:213], v[148:149], 0, s[26:27]
	s_add_i32 m0, s49, 0xc000
	ds_read_b128 v[190:193], v153
	ds_read_b128 v[194:197], v153 offset:1024
	ds_read_b128 v[198:201], v153 offset:2048
	ds_read_b128 v[202:205], v153 offset:3072
	ds_read_b128 v[206:209], v153 offset:4096
	ds_read_b128 v[218:221], v153 offset:5120
	ds_read_b128 v[222:225], v153 offset:6144
	ds_read_b128 v[226:229], v153 offset:7168
	global_load_lds_dwordx4 v[212:213], off
	v_lshl_add_u64 v[212:213], v[150:151], 0, s[26:27]
	s_add_i32 m0, s49, 0xe000
	s_nop 0
	global_load_lds_dwordx4 v[212:213], off
	s_waitcnt vmcnt(8)
	s_waitcnt lgkmcnt(0)
	s_barrier
	s_setprio 1
	v_mfma_f32_16x16x32_bf16 v[124:127], v[158:161], v[190:193], v[124:127]
	v_mfma_f32_16x16x32_bf16 v[120:123], v[166:169], v[190:193], v[120:123]
	v_mfma_f32_16x16x32_bf16 v[112:115], v[158:161], v[198:201], v[112:115]
	v_mfma_f32_16x16x32_bf16 v[104:107], v[166:169], v[198:201], v[104:107]
	v_mfma_f32_16x16x32_bf16 v[96:99], v[158:161], v[206:209], v[96:99]
	v_mfma_f32_16x16x32_bf16 v[88:91], v[166:169], v[206:209], v[88:91]
	v_mfma_f32_16x16x32_bf16 v[80:83], v[158:161], v[222:225], v[80:83]
	v_mfma_f32_16x16x32_bf16 v[72:75], v[166:169], v[222:225], v[72:75]
	v_mfma_f32_16x16x32_bf16 v[124:127], v[162:165], v[194:197], v[124:127]
	v_mfma_f32_16x16x32_bf16 v[120:123], v[170:173], v[194:197], v[120:123]
	v_mfma_f32_16x16x32_bf16 v[112:115], v[162:165], v[202:205], v[112:115]
	v_mfma_f32_16x16x32_bf16 v[104:107], v[170:173], v[202:205], v[104:107]
	v_mfma_f32_16x16x32_bf16 v[96:99], v[162:165], v[218:221], v[96:99]
	v_mfma_f32_16x16x32_bf16 v[88:91], v[170:173], v[218:221], v[88:91]
	v_mfma_f32_16x16x32_bf16 v[80:83], v[162:165], v[226:229], v[80:83]
	v_mfma_f32_16x16x32_bf16 v[72:75], v[170:173], v[226:229], v[72:75]
	s_setprio 0
	s_setprio 1
	v_mfma_f32_16x16x32_bf16 v[128:131], v[174:177], v[190:193], v[128:131]
	v_mfma_f32_16x16x32_bf16 v[116:119], v[182:185], v[190:193], v[116:119]
	v_mfma_f32_16x16x32_bf16 v[108:111], v[174:177], v[198:201], v[108:111]
	v_mfma_f32_16x16x32_bf16 v[100:103], v[182:185], v[198:201], v[100:103]
	v_mfma_f32_16x16x32_bf16 v[92:95], v[174:177], v[206:209], v[92:95]
	v_mfma_f32_16x16x32_bf16 v[84:87], v[182:185], v[206:209], v[84:87]
	v_mfma_f32_16x16x32_bf16 v[76:79], v[174:177], v[222:225], v[76:79]
	v_mfma_f32_16x16x32_bf16 v[68:71], v[182:185], v[222:225], v[68:71]
	v_mfma_f32_16x16x32_bf16 v[128:131], v[178:181], v[194:197], v[128:131]
	v_mfma_f32_16x16x32_bf16 v[116:119], v[186:189], v[194:197], v[116:119]
	v_mfma_f32_16x16x32_bf16 v[108:111], v[178:181], v[202:205], v[108:111]
	v_mfma_f32_16x16x32_bf16 v[100:103], v[186:189], v[202:205], v[100:103]
	v_mfma_f32_16x16x32_bf16 v[92:95], v[178:181], v[218:221], v[92:95]
	v_mfma_f32_16x16x32_bf16 v[84:87], v[186:189], v[218:221], v[84:87]
	v_mfma_f32_16x16x32_bf16 v[76:79], v[178:181], v[226:229], v[76:79]
	v_mfma_f32_16x16x32_bf16 v[68:71], v[186:189], v[226:229], v[68:71]
	s_barrier
	s_setprio 0
	s_add_i32 s26, s65, s47
	v_lshl_add_u64 v[212:213], s[22:23], 0, v[138:139]
	s_mov_b32 m0, s26
	ds_read_b128 v[190:193], v153 offset:16384
	ds_read_b128 v[194:197], v153 offset:17408
	ds_read_b128 v[198:201], v153 offset:18432
	ds_read_b128 v[202:205], v153 offset:19456
	ds_read_b128 v[206:209], v153 offset:20480
	ds_read_b128 v[218:221], v153 offset:21504
	ds_read_b128 v[222:225], v153 offset:22528
	ds_read_b128 v[226:229], v153 offset:23552
	global_load_lds_dwordx4 v[212:213], off
	s_add_i32 m0, s26, 0x2000
	v_lshl_add_u64 v[214:215], s[22:23], 0, v[136:137]
	s_add_u32 s22, s22, s6
	s_addc_u32 s23, s23, s7
	s_add_i32 s26, s28, s47
	global_load_lds_dwordx4 v[214:215], off
	v_lshl_add_u64 v[230:231], s[22:23], 0, v[138:139]
	s_mov_b32 m0, s26
	v_lshl_add_u64 v[240:241], s[22:23], 0, v[136:137]
	global_load_lds_dwordx4 v[230:231], off
	s_add_i32 m0, s26, 0x2000
	v_mov_b32_e32 v211, v3
	global_load_lds_dwordx4 v[240:241], off
	s_mov_b32 m0, s49
	v_lshl_add_u64 v[242:243], s[40:41], 0, v[2:3]
	global_load_lds_dwordx4 v2, s[40:41]
	s_mov_b32 m0, s50
	s_nop 0
	global_load_lds_dwordx4 v210, s[40:41]
	s_waitcnt vmcnt(8)
	s_waitcnt lgkmcnt(0)
	v_lshl_add_u64 v[210:211], s[40:41], 0, v[210:211]
	s_barrier
	s_setprio 1
	s_waitcnt lgkmcnt(0)
	v_mfma_f32_16x16x32_bf16 v[64:67], v[158:161], v[190:193], v[64:67]
	v_mfma_f32_16x16x32_bf16 v[56:59], v[166:169], v[190:193], v[56:59]
	v_mfma_f32_16x16x32_bf16 v[48:51], v[158:161], v[198:201], v[48:51]
	v_mfma_f32_16x16x32_bf16 v[40:43], v[166:169], v[198:201], v[40:43]
	v_mfma_f32_16x16x32_bf16 v[32:35], v[158:161], v[206:209], v[32:35]
	v_mfma_f32_16x16x32_bf16 v[24:27], v[166:169], v[206:209], v[24:27]
	v_mfma_f32_16x16x32_bf16 v[16:19], v[158:161], v[222:225], v[16:19]
	v_mfma_f32_16x16x32_bf16 v[8:11], v[166:169], v[222:225], v[8:11]
	v_mfma_f32_16x16x32_bf16 v[64:67], v[162:165], v[194:197], v[64:67]
	v_mfma_f32_16x16x32_bf16 v[56:59], v[170:173], v[194:197], v[56:59]
	v_mfma_f32_16x16x32_bf16 v[48:51], v[162:165], v[202:205], v[48:51]
	v_mfma_f32_16x16x32_bf16 v[40:43], v[170:173], v[202:205], v[40:43]
	v_mfma_f32_16x16x32_bf16 v[32:35], v[162:165], v[218:221], v[32:35]
	v_mfma_f32_16x16x32_bf16 v[24:27], v[170:173], v[218:221], v[24:27]
	v_mfma_f32_16x16x32_bf16 v[16:19], v[162:165], v[226:229], v[16:19]
	v_mfma_f32_16x16x32_bf16 v[8:11], v[170:173], v[226:229], v[8:11]
	s_setprio 0
	s_setprio 1
	v_mfma_f32_16x16x32_bf16 v[60:63], v[174:177], v[190:193], v[60:63]
	v_mfma_f32_16x16x32_bf16 v[52:55], v[182:185], v[190:193], v[52:55]
	v_mfma_f32_16x16x32_bf16 v[44:47], v[174:177], v[198:201], v[44:47]
	v_mfma_f32_16x16x32_bf16 v[36:39], v[182:185], v[198:201], v[36:39]
	v_mfma_f32_16x16x32_bf16 v[28:31], v[174:177], v[206:209], v[28:31]
	v_mfma_f32_16x16x32_bf16 v[20:23], v[182:185], v[206:209], v[20:23]
	v_mfma_f32_16x16x32_bf16 v[12:15], v[174:177], v[222:225], v[12:15]
	v_mfma_f32_16x16x32_bf16 v[4:7], v[182:185], v[222:225], v[4:7]
	v_mfma_f32_16x16x32_bf16 v[60:63], v[178:181], v[194:197], v[60:63]
	v_mfma_f32_16x16x32_bf16 v[52:55], v[186:189], v[194:197], v[52:55]
	v_mfma_f32_16x16x32_bf16 v[44:47], v[178:181], v[202:205], v[44:47]
	v_mfma_f32_16x16x32_bf16 v[36:39], v[186:189], v[202:205], v[36:39]
	v_mfma_f32_16x16x32_bf16 v[28:31], v[178:181], v[218:221], v[28:31]
	v_mfma_f32_16x16x32_bf16 v[20:23], v[186:189], v[218:221], v[20:23]
	v_mfma_f32_16x16x32_bf16 v[12:15], v[178:181], v[226:229], v[12:15]
	v_mfma_f32_16x16x32_bf16 v[4:7], v[186:189], v[226:229], v[4:7]
	s_barrier
	s_setprio 0
	s_add_i32 s22, 0, 0x18000
	v_add_u32_e32 v2, s22, v147
	s_add_i32 s23, 0, 0x1c000
	ds_read_b128 v[158:161], v2
	ds_read_b128 v[162:165], v2 offset:1024
	ds_read_b128 v[166:169], v2 offset:2048
	ds_read_b128 v[170:173], v2 offset:3072
	v_add_u32_e32 v2, s23, v147
	ds_read_b128 v[174:177], v2
	ds_read_b128 v[178:181], v2 offset:1024
	ds_read_b128 v[182:185], v2 offset:2048
	ds_read_b128 v[186:189], v2 offset:3072
	s_mov_b32 m0, s51
	ds_read_b128 v[190:193], v153 offset:32768
	ds_read_b128 v[194:197], v153 offset:33792
	ds_read_b128 v[198:201], v153 offset:34816
	ds_read_b128 v[202:205], v153 offset:35840
	ds_read_b128 v[206:209], v153 offset:36864
	ds_read_b128 v[218:221], v153 offset:37888
	ds_read_b128 v[222:225], v153 offset:38912
	ds_read_b128 v[226:229], v153 offset:39936
	global_load_lds_dwordx4 v141, s[40:41]
	s_mov_b32 m0, s52
	s_nop 0
	global_load_lds_dwordx4 v145, s[40:41]
	s_waitcnt vmcnt(8)
	s_waitcnt lgkmcnt(0)
	s_barrier
	s_setprio 1
	v_mfma_f32_16x16x32_bf16 v[124:127], v[158:161], v[190:193], v[124:127]
	v_mfma_f32_16x16x32_bf16 v[120:123], v[166:169], v[190:193], v[120:123]
	v_mfma_f32_16x16x32_bf16 v[112:115], v[158:161], v[198:201], v[112:115]
	v_mfma_f32_16x16x32_bf16 v[104:107], v[166:169], v[198:201], v[104:107]
	v_mfma_f32_16x16x32_bf16 v[96:99], v[158:161], v[206:209], v[96:99]
	v_mfma_f32_16x16x32_bf16 v[88:91], v[166:169], v[206:209], v[88:91]
	v_mfma_f32_16x16x32_bf16 v[80:83], v[158:161], v[222:225], v[80:83]
	v_mfma_f32_16x16x32_bf16 v[72:75], v[166:169], v[222:225], v[72:75]
	v_mfma_f32_16x16x32_bf16 v[124:127], v[162:165], v[194:197], v[124:127]
	v_mfma_f32_16x16x32_bf16 v[120:123], v[170:173], v[194:197], v[120:123]
	v_mfma_f32_16x16x32_bf16 v[112:115], v[162:165], v[202:205], v[112:115]
	v_mfma_f32_16x16x32_bf16 v[104:107], v[170:173], v[202:205], v[104:107]
	v_mfma_f32_16x16x32_bf16 v[96:99], v[162:165], v[218:221], v[96:99]
	v_mfma_f32_16x16x32_bf16 v[88:91], v[170:173], v[218:221], v[88:91]
	v_mfma_f32_16x16x32_bf16 v[80:83], v[162:165], v[226:229], v[80:83]
	v_mfma_f32_16x16x32_bf16 v[72:75], v[170:173], v[226:229], v[72:75]
	s_setprio 0
	s_setprio 1
	v_mfma_f32_16x16x32_bf16 v[128:131], v[174:177], v[190:193], v[128:131]
	v_mfma_f32_16x16x32_bf16 v[116:119], v[182:185], v[190:193], v[116:119]
	v_mfma_f32_16x16x32_bf16 v[108:111], v[174:177], v[198:201], v[108:111]
	v_mfma_f32_16x16x32_bf16 v[100:103], v[182:185], v[198:201], v[100:103]
	v_mfma_f32_16x16x32_bf16 v[92:95], v[174:177], v[206:209], v[92:95]
	v_mfma_f32_16x16x32_bf16 v[84:87], v[182:185], v[206:209], v[84:87]
	v_mfma_f32_16x16x32_bf16 v[76:79], v[174:177], v[222:225], v[76:79]
	v_mfma_f32_16x16x32_bf16 v[68:71], v[182:185], v[222:225], v[68:71]
	v_mfma_f32_16x16x32_bf16 v[128:131], v[178:181], v[194:197], v[128:131]
	v_mfma_f32_16x16x32_bf16 v[116:119], v[186:189], v[194:197], v[116:119]
	v_mfma_f32_16x16x32_bf16 v[108:111], v[178:181], v[202:205], v[108:111]
	v_mfma_f32_16x16x32_bf16 v[100:103], v[186:189], v[202:205], v[100:103]
	v_mfma_f32_16x16x32_bf16 v[92:95], v[178:181], v[218:221], v[92:95]
	v_mfma_f32_16x16x32_bf16 v[84:87], v[186:189], v[218:221], v[84:87]
	v_mfma_f32_16x16x32_bf16 v[76:79], v[178:181], v[226:229], v[76:79]
	v_mfma_f32_16x16x32_bf16 v[68:71], v[186:189], v[226:229], v[68:71]
	s_barrier
	s_setprio 0
	s_add_i32 s22, s22, s47
	v_lshl_add_u64 v[212:213], v[212:213], 0, s[24:25]
	s_mov_b32 m0, s22
	ds_read_b128 v[190:193], v153 offset:49152
	ds_read_b128 v[194:197], v153 offset:50176
	ds_read_b128 v[198:201], v153 offset:51200
	ds_read_b128 v[202:205], v153 offset:52224
	ds_read_b128 v[206:209], v153 offset:53248
	ds_read_b128 v[218:221], v153 offset:54272
	ds_read_b128 v[222:225], v153 offset:55296
	ds_read_b128 v[226:229], v153 offset:56320
	global_load_lds_dwordx4 v[212:213], off
	v_lshl_add_u64 v[212:213], v[214:215], 0, s[24:25]
	s_add_i32 m0, s22, 0x2000
	s_add_i32 s22, s23, s47
	global_load_lds_dwordx4 v[212:213], off
	v_lshl_add_u64 v[212:213], v[230:231], 0, s[24:25]
	s_mov_b32 m0, s22
	v_lshl_add_u64 v[210:211], v[210:211], 0, s[24:25]
	global_load_lds_dwordx4 v[212:213], off
	v_lshl_add_u64 v[212:213], v[240:241], 0, s[24:25]
	s_add_i32 m0, s22, 0x2000
	s_nop 0
	global_load_lds_dwordx4 v[212:213], off
	v_lshl_add_u64 v[212:213], v[242:243], 0, s[24:25]
	s_mov_b32 m0, s53
	s_nop 0
	global_load_lds_dwordx4 v[212:213], off
	s_mov_b32 m0, s54
	s_nop 0
	global_load_lds_dwordx4 v[210:211], off
	s_waitcnt vmcnt(8)
	s_waitcnt lgkmcnt(0)
	s_barrier
	s_setprio 1
	v_mfma_f32_16x16x32_bf16 v[64:67], v[158:161], v[190:193], v[64:67]
	v_mfma_f32_16x16x32_bf16 v[56:59], v[166:169], v[190:193], v[56:59]
	v_mfma_f32_16x16x32_bf16 v[48:51], v[158:161], v[198:201], v[48:51]
	v_mfma_f32_16x16x32_bf16 v[40:43], v[166:169], v[198:201], v[40:43]
	v_mfma_f32_16x16x32_bf16 v[32:35], v[158:161], v[206:209], v[32:35]
	v_mfma_f32_16x16x32_bf16 v[24:27], v[166:169], v[206:209], v[24:27]
	v_mfma_f32_16x16x32_bf16 v[16:19], v[158:161], v[222:225], v[16:19]
	v_mfma_f32_16x16x32_bf16 v[8:11], v[166:169], v[222:225], v[8:11]
	v_mfma_f32_16x16x32_bf16 v[64:67], v[162:165], v[194:197], v[64:67]
	v_mfma_f32_16x16x32_bf16 v[56:59], v[170:173], v[194:197], v[56:59]
	v_mfma_f32_16x16x32_bf16 v[48:51], v[162:165], v[202:205], v[48:51]
	v_mfma_f32_16x16x32_bf16 v[40:43], v[170:173], v[202:205], v[40:43]
	v_mfma_f32_16x16x32_bf16 v[32:35], v[162:165], v[218:221], v[32:35]
	v_mfma_f32_16x16x32_bf16 v[24:27], v[170:173], v[218:221], v[24:27]
	v_mfma_f32_16x16x32_bf16 v[16:19], v[162:165], v[226:229], v[16:19]
	v_mfma_f32_16x16x32_bf16 v[8:11], v[170:173], v[226:229], v[8:11]
	s_setprio 0
	s_setprio 1
	v_mfma_f32_16x16x32_bf16 v[60:63], v[174:177], v[190:193], v[60:63]
	v_mfma_f32_16x16x32_bf16 v[52:55], v[182:185], v[190:193], v[52:55]
	v_mfma_f32_16x16x32_bf16 v[44:47], v[174:177], v[198:201], v[44:47]
	v_mfma_f32_16x16x32_bf16 v[36:39], v[182:185], v[198:201], v[36:39]
	v_mfma_f32_16x16x32_bf16 v[28:31], v[174:177], v[206:209], v[28:31]
	v_mfma_f32_16x16x32_bf16 v[20:23], v[182:185], v[206:209], v[20:23]
	v_mfma_f32_16x16x32_bf16 v[12:15], v[174:177], v[222:225], v[12:15]
	v_mfma_f32_16x16x32_bf16 v[4:7], v[182:185], v[222:225], v[4:7]
	v_mfma_f32_16x16x32_bf16 v[60:63], v[178:181], v[194:197], v[60:63]
	v_mfma_f32_16x16x32_bf16 v[52:55], v[186:189], v[194:197], v[52:55]
	v_mfma_f32_16x16x32_bf16 v[44:47], v[178:181], v[202:205], v[44:47]
	v_mfma_f32_16x16x32_bf16 v[36:39], v[186:189], v[202:205], v[36:39]
	v_mfma_f32_16x16x32_bf16 v[28:31], v[178:181], v[218:221], v[28:31]
	v_mfma_f32_16x16x32_bf16 v[20:23], v[186:189], v[218:221], v[20:23]
	v_mfma_f32_16x16x32_bf16 v[12:15], v[178:181], v[226:229], v[12:15]
	v_mfma_f32_16x16x32_bf16 v[4:7], v[186:189], v[226:229], v[4:7]
	s_barrier
	s_setprio 0
	s_cmp_ge_i32 s21, s55
	s_mov_b64 s[26:27], s[30:31]
	s_cbranch_scc0 .LBB0_3267

.LBB0_3497:
	s_andn2_b64 vcc, exec, s[10:11]
	s_cbranch_vccnz .LBB0_3500
	s_add_u32 s26, s26, 0x80
	s_addc_u32 s27, s27, 0
	s_add_u32 s19, s30, 0x100
	s_addc_u32 s20, s31, 0
	s_mov_b32 s21, 0
	s_add_i32 s22, s21, 2
	s_add_u32 s23, s26, 0x80
	s_addc_u32 s28, s27, 0
	s_add_i32 s55, 0, 0x10000
	s_cmp_eq_u32 s49, s21
	s_cselect_b32 s31, s15, s28
	s_cselect_b32 s30, s14, s23
	v_add_u32_e32 v2, s55, v145
	s_cselect_b32 s29, s17, s20
	s_cselect_b32 s28, s16, s19
	s_add_i32 s21, 0, 0x14000
	ds_read_b128 v[148:151], v2
	ds_read_b128 v[152:155], v2 offset:1024
	ds_read_b128 v[156:159], v2 offset:2048
	ds_read_b128 v[160:163], v2 offset:3072
	v_add_u32_e32 v2, s21, v145
	ds_read_b128 v[164:167], v2
	ds_read_b128 v[168:171], v2 offset:1024
	ds_read_b128 v[172:175], v2 offset:2048
	ds_read_b128 v[176:179], v2 offset:3072
	v_lshl_add_u64 v[212:213], s[26:27], 0, v[140:141]
	s_add_i32 m0, s42, 0xc000
	ds_read_b128 v[180:183], v147
	ds_read_b128 v[184:187], v147 offset:1024
	ds_read_b128 v[188:191], v147 offset:2048
	ds_read_b128 v[192:195], v147 offset:3072
	ds_read_b128 v[196:199], v147 offset:4096
	ds_read_b128 v[200:203], v147 offset:5120
	ds_read_b128 v[204:207], v147 offset:6144
	ds_read_b128 v[208:211], v147 offset:7168
	global_load_lds_dwordx4 v[212:213], off
	v_lshl_add_u64 v[212:213], s[26:27], 0, v[142:143]
	s_add_i32 m0, s42, 0xe000
	s_nop 0
	global_load_lds_dwordx4 v[212:213], off
	s_waitcnt vmcnt(8)
	s_waitcnt lgkmcnt(0)
	s_barrier
	s_setprio 1
	v_mfma_f32_16x16x32_bf16 v[124:127], v[148:151], v[180:183], 0
	v_mfma_f32_16x16x32_bf16 v[128:131], v[156:159], v[180:183], 0
	v_mfma_f32_16x16x32_bf16 v[112:115], v[148:151], v[188:191], 0
	v_mfma_f32_16x16x32_bf16 v[108:111], v[156:159], v[188:191], 0
	v_mfma_f32_16x16x32_bf16 v[96:99], v[148:151], v[196:199], 0
	v_mfma_f32_16x16x32_bf16 v[92:95], v[156:159], v[196:199], 0
	v_mfma_f32_16x16x32_bf16 v[80:83], v[148:151], v[204:207], 0
	v_mfma_f32_16x16x32_bf16 v[76:79], v[156:159], v[204:207], 0
	v_mfma_f32_16x16x32_bf16 v[124:127], v[152:155], v[184:187], v[124:127]
	v_mfma_f32_16x16x32_bf16 v[128:131], v[160:163], v[184:187], v[128:131]
	v_mfma_f32_16x16x32_bf16 v[112:115], v[152:155], v[192:195], v[112:115]
	v_mfma_f32_16x16x32_bf16 v[108:111], v[160:163], v[192:195], v[108:111]
	v_mfma_f32_16x16x32_bf16 v[96:99], v[152:155], v[200:203], v[96:99]
	v_mfma_f32_16x16x32_bf16 v[92:95], v[160:163], v[200:203], v[92:95]
	v_mfma_f32_16x16x32_bf16 v[80:83], v[152:155], v[208:211], v[80:83]
	v_mfma_f32_16x16x32_bf16 v[76:79], v[160:163], v[208:211], v[76:79]
	s_setprio 0
	s_setprio 1
	v_mfma_f32_16x16x32_bf16 v[120:123], v[164:167], v[180:183], 0
	v_mfma_f32_16x16x32_bf16 v[116:119], v[172:175], v[180:183], 0
	v_mfma_f32_16x16x32_bf16 v[104:107], v[164:167], v[188:191], 0
	v_mfma_f32_16x16x32_bf16 v[100:103], v[172:175], v[188:191], 0
	v_mfma_f32_16x16x32_bf16 v[88:91], v[164:167], v[196:199], 0
	v_mfma_f32_16x16x32_bf16 v[84:87], v[172:175], v[196:199], 0
	v_mfma_f32_16x16x32_bf16 v[72:75], v[164:167], v[204:207], 0
	v_mfma_f32_16x16x32_bf16 v[68:71], v[172:175], v[204:207], 0
	v_mfma_f32_16x16x32_bf16 v[120:123], v[168:171], v[184:187], v[120:123]
	v_mfma_f32_16x16x32_bf16 v[116:119], v[176:179], v[184:187], v[116:119]
	v_mfma_f32_16x16x32_bf16 v[104:107], v[168:171], v[192:195], v[104:107]
	v_mfma_f32_16x16x32_bf16 v[100:103], v[176:179], v[192:195], v[100:103]
	v_mfma_f32_16x16x32_bf16 v[88:91], v[168:171], v[200:203], v[88:91]
	v_mfma_f32_16x16x32_bf16 v[84:87], v[176:179], v[200:203], v[84:87]
	v_mfma_f32_16x16x32_bf16 v[72:75], v[168:171], v[208:211], v[72:75]
	v_mfma_f32_16x16x32_bf16 v[68:71], v[176:179], v[208:211], v[68:71]
	s_barrier
	s_setprio 0
	s_add_i32 s23, s55, s41
	v_lshl_add_u64 v[212:213], s[28:29], 0, v[136:137]
	s_mov_b32 m0, s23
	ds_read_b128 v[180:183], v147 offset:16384
	ds_read_b128 v[184:187], v147 offset:17408
	ds_read_b128 v[188:191], v147 offset:18432
	ds_read_b128 v[192:195], v147 offset:19456
	ds_read_b128 v[196:199], v147 offset:20480
	ds_read_b128 v[200:203], v147 offset:21504
	ds_read_b128 v[204:207], v147 offset:22528
	ds_read_b128 v[208:211], v147 offset:23552
	global_load_lds_dwordx4 v[212:213], off
	s_add_i32 m0, s23, 0x2000
	v_lshl_add_u64 v[214:215], s[28:29], 0, v[132:133]
	s_add_u32 s28, s28, s2
	s_addc_u32 s29, s29, s3
	s_add_i32 s21, s21, s41
	global_load_lds_dwordx4 v[214:215], off
	v_lshl_add_u64 v[218:219], s[28:29], 0, v[136:137]
	s_mov_b32 m0, s21
	v_lshl_add_u64 v[220:221], s[28:29], 0, v[132:133]
	global_load_lds_dwordx4 v[218:219], off
	s_add_i32 m0, s21, 0x2000
	v_lshl_add_u64 v[222:223], s[30:31], 0, v[138:139]
	global_load_lds_dwordx4 v[220:221], off
	s_mov_b32 m0, s42
	v_lshl_add_u64 v[224:225], s[30:31], 0, v[134:135]
	global_load_lds_dwordx4 v[222:223], off
	s_mov_b32 m0, s43
	s_nop 0
	global_load_lds_dwordx4 v[224:225], off
	s_waitcnt vmcnt(8)
	s_waitcnt lgkmcnt(0)
	s_barrier
	s_setprio 1
	v_mfma_f32_16x16x32_bf16 v[64:67], v[148:151], v[180:183], 0
	v_mfma_f32_16x16x32_bf16 v[60:63], v[156:159], v[180:183], 0
	v_mfma_f32_16x16x32_bf16 v[48:51], v[148:151], v[188:191], 0
	v_mfma_f32_16x16x32_bf16 v[44:47], v[156:159], v[188:191], 0
	v_mfma_f32_16x16x32_bf16 v[32:35], v[148:151], v[196:199], 0
	v_mfma_f32_16x16x32_bf16 v[28:31], v[156:159], v[196:199], 0
	v_mfma_f32_16x16x32_bf16 v[16:19], v[148:151], v[204:207], 0
	v_mfma_f32_16x16x32_bf16 v[12:15], v[156:159], v[204:207], 0
	v_mfma_f32_16x16x32_bf16 v[64:67], v[152:155], v[184:187], v[64:67]
	v_mfma_f32_16x16x32_bf16 v[60:63], v[160:163], v[184:187], v[60:63]
	v_mfma_f32_16x16x32_bf16 v[48:51], v[152:155], v[192:195], v[48:51]
	v_mfma_f32_16x16x32_bf16 v[44:47], v[160:163], v[192:195], v[44:47]
	v_mfma_f32_16x16x32_bf16 v[32:35], v[152:155], v[200:203], v[32:35]
	v_mfma_f32_16x16x32_bf16 v[28:31], v[160:163], v[200:203], v[28:31]
	v_mfma_f32_16x16x32_bf16 v[16:19], v[152:155], v[208:211], v[16:19]
	v_mfma_f32_16x16x32_bf16 v[12:15], v[160:163], v[208:211], v[12:15]
	s_setprio 0
	s_setprio 1
	v_mfma_f32_16x16x32_bf16 v[56:59], v[164:167], v[180:183], 0
	v_mfma_f32_16x16x32_bf16 v[52:55], v[172:175], v[180:183], 0
	v_mfma_f32_16x16x32_bf16 v[40:43], v[164:167], v[188:191], 0
	v_mfma_f32_16x16x32_bf16 v[36:39], v[172:175], v[188:191], 0
	v_mfma_f32_16x16x32_bf16 v[24:27], v[164:167], v[196:199], 0
	v_mfma_f32_16x16x32_bf16 v[20:23], v[172:175], v[196:199], 0
	v_mfma_f32_16x16x32_bf16 v[8:11], v[164:167], v[204:207], 0
	v_mfma_f32_16x16x32_bf16 v[4:7], v[172:175], v[204:207], 0
	v_mfma_f32_16x16x32_bf16 v[56:59], v[168:171], v[184:187], v[56:59]
	v_mfma_f32_16x16x32_bf16 v[52:55], v[176:179], v[184:187], v[52:55]
	v_mfma_f32_16x16x32_bf16 v[40:43], v[168:171], v[192:195], v[40:43]
	v_mfma_f32_16x16x32_bf16 v[36:39], v[176:179], v[192:195], v[36:39]
	v_mfma_f32_16x16x32_bf16 v[24:27], v[168:171], v[200:203], v[24:27]
	v_mfma_f32_16x16x32_bf16 v[20:23], v[176:179], v[200:203], v[20:23]
	v_mfma_f32_16x16x32_bf16 v[8:11], v[168:171], v[208:211], v[8:11]
	v_mfma_f32_16x16x32_bf16 v[4:7], v[176:179], v[208:211], v[4:7]
	s_barrier
	s_setprio 0
	s_add_i32 s21, 0, 0x18000
	v_add_u32_e32 v2, s21, v145
	s_add_i32 s23, 0, 0x1c000
	ds_read_b128 v[148:151], v2
	ds_read_b128 v[152:155], v2 offset:1024
	ds_read_b128 v[156:159], v2 offset:2048
	ds_read_b128 v[160:163], v2 offset:3072
	v_add_u32_e32 v2, s23, v145
	ds_read_b128 v[164:167], v2
	ds_read_b128 v[168:171], v2 offset:1024
	ds_read_b128 v[172:175], v2 offset:2048
	ds_read_b128 v[176:179], v2 offset:3072
	s_add_u32 s28, s30, s2
	s_addc_u32 s29, s31, s3
	s_mov_b32 m0, s44
	v_lshl_add_u64 v[226:227], s[28:29], 0, v[138:139]
	ds_read_b128 v[180:183], v147 offset:32768
	ds_read_b128 v[184:187], v147 offset:33792
	ds_read_b128 v[188:191], v147 offset:34816
	ds_read_b128 v[192:195], v147 offset:35840
	ds_read_b128 v[196:199], v147 offset:36864
	ds_read_b128 v[200:203], v147 offset:37888
	ds_read_b128 v[204:207], v147 offset:38912
	ds_read_b128 v[208:211], v147 offset:39936
	global_load_lds_dwordx4 v[226:227], off
	v_lshl_add_u64 v[226:227], s[28:29], 0, v[134:135]
	s_mov_b32 m0, s45
	s_nop 0
	global_load_lds_dwordx4 v[226:227], off
	s_waitcnt vmcnt(8)
	s_waitcnt lgkmcnt(0)
	s_barrier
	s_setprio 1
	v_mfma_f32_16x16x32_bf16 v[124:127], v[148:151], v[180:183], v[124:127]
	v_mfma_f32_16x16x32_bf16 v[128:131], v[156:159], v[180:183], v[128:131]
	v_mfma_f32_16x16x32_bf16 v[112:115], v[148:151], v[188:191], v[112:115]
	v_mfma_f32_16x16x32_bf16 v[108:111], v[156:159], v[188:191], v[108:111]
	v_mfma_f32_16x16x32_bf16 v[96:99], v[148:151], v[196:199], v[96:99]
	v_mfma_f32_16x16x32_bf16 v[92:95], v[156:159], v[196:199], v[92:95]
	v_mfma_f32_16x16x32_bf16 v[80:83], v[148:151], v[204:207], v[80:83]
	v_mfma_f32_16x16x32_bf16 v[76:79], v[156:159], v[204:207], v[76:79]
	v_mfma_f32_16x16x32_bf16 v[124:127], v[152:155], v[184:187], v[124:127]
	v_mfma_f32_16x16x32_bf16 v[128:131], v[160:163], v[184:187], v[128:131]
	v_mfma_f32_16x16x32_bf16 v[112:115], v[152:155], v[192:195], v[112:115]
	v_mfma_f32_16x16x32_bf16 v[108:111], v[160:163], v[192:195], v[108:111]
	v_mfma_f32_16x16x32_bf16 v[96:99], v[152:155], v[200:203], v[96:99]
	v_mfma_f32_16x16x32_bf16 v[92:95], v[160:163], v[200:203], v[92:95]
	v_mfma_f32_16x16x32_bf16 v[80:83], v[152:155], v[208:211], v[80:83]
	v_mfma_f32_16x16x32_bf16 v[76:79], v[160:163], v[208:211], v[76:79]
	s_setprio 0
	s_setprio 1
	v_mfma_f32_16x16x32_bf16 v[120:123], v[164:167], v[180:183], v[120:123]
	v_mfma_f32_16x16x32_bf16 v[116:119], v[172:175], v[180:183], v[116:119]
	v_mfma_f32_16x16x32_bf16 v[104:107], v[164:167], v[188:191], v[104:107]
	v_mfma_f32_16x16x32_bf16 v[100:103], v[172:175], v[188:191], v[100:103]
	v_mfma_f32_16x16x32_bf16 v[88:91], v[164:167], v[196:199], v[88:91]
	v_mfma_f32_16x16x32_bf16 v[84:87], v[172:175], v[196:199], v[84:87]
	v_mfma_f32_16x16x32_bf16 v[72:75], v[164:167], v[204:207], v[72:75]
	v_mfma_f32_16x16x32_bf16 v[68:71], v[172:175], v[204:207], v[68:71]
	v_mfma_f32_16x16x32_bf16 v[120:123], v[168:171], v[184:187], v[120:123]
	v_mfma_f32_16x16x32_bf16 v[116:119], v[176:179], v[184:187], v[116:119]
	v_mfma_f32_16x16x32_bf16 v[104:107], v[168:171], v[192:195], v[104:107]
	v_mfma_f32_16x16x32_bf16 v[100:103], v[176:179], v[192:195], v[100:103]
	v_mfma_f32_16x16x32_bf16 v[88:91], v[168:171], v[200:203], v[88:91]
	v_mfma_f32_16x16x32_bf16 v[84:87], v[176:179], v[200:203], v[84:87]
	v_mfma_f32_16x16x32_bf16 v[72:75], v[168:171], v[208:211], v[72:75]
	v_mfma_f32_16x16x32_bf16 v[68:71], v[176:179], v[208:211], v[68:71]
	s_barrier
	s_setprio 0
	s_add_i32 s21, s21, s41
	v_lshl_add_u64 v[212:213], v[212:213], 0, s[24:25]
	s_mov_b32 m0, s21
	ds_read_b128 v[180:183], v147 offset:49152
	ds_read_b128 v[184:187], v147 offset:50176
	ds_read_b128 v[188:191], v147 offset:51200
	ds_read_b128 v[192:195], v147 offset:52224
	ds_read_b128 v[196:199], v147 offset:53248
	ds_read_b128 v[200:203], v147 offset:54272
	ds_read_b128 v[204:207], v147 offset:55296
	ds_read_b128 v[208:211], v147 offset:56320
	global_load_lds_dwordx4 v[212:213], off
	v_lshl_add_u64 v[212:213], v[214:215], 0, s[24:25]
	s_add_i32 m0, s21, 0x2000
	s_add_i32 s21, s23, s41
	global_load_lds_dwordx4 v[212:213], off
	v_lshl_add_u64 v[212:213], v[218:219], 0, s[24:25]
	s_mov_b32 m0, s21
	s_nop 0
	global_load_lds_dwordx4 v[212:213], off
	v_lshl_add_u64 v[212:213], v[220:221], 0, s[24:25]
	s_add_i32 m0, s21, 0x2000
	s_nop 0
	global_load_lds_dwordx4 v[212:213], off
	v_lshl_add_u64 v[212:213], v[222:223], 0, s[24:25]
	s_mov_b32 m0, s47
	s_nop 0
	global_load_lds_dwordx4 v[212:213], off
	v_lshl_add_u64 v[212:213], v[224:225], 0, s[24:25]
	s_mov_b32 m0, s48
	s_nop 0
	global_load_lds_dwordx4 v[212:213], off
	s_waitcnt vmcnt(8)
	s_waitcnt lgkmcnt(0)
	s_barrier
	s_setprio 1
	v_mfma_f32_16x16x32_bf16 v[64:67], v[148:151], v[180:183], v[64:67]
	v_mfma_f32_16x16x32_bf16 v[60:63], v[156:159], v[180:183], v[60:63]
	v_mfma_f32_16x16x32_bf16 v[48:51], v[148:151], v[188:191], v[48:51]
	v_mfma_f32_16x16x32_bf16 v[44:47], v[156:159], v[188:191], v[44:47]
	v_mfma_f32_16x16x32_bf16 v[32:35], v[148:151], v[196:199], v[32:35]
	v_mfma_f32_16x16x32_bf16 v[28:31], v[156:159], v[196:199], v[28:31]
	v_mfma_f32_16x16x32_bf16 v[16:19], v[148:151], v[204:207], v[16:19]
	v_mfma_f32_16x16x32_bf16 v[12:15], v[156:159], v[204:207], v[12:15]
	v_mfma_f32_16x16x32_bf16 v[64:67], v[152:155], v[184:187], v[64:67]
	v_mfma_f32_16x16x32_bf16 v[60:63], v[160:163], v[184:187], v[60:63]
	v_mfma_f32_16x16x32_bf16 v[48:51], v[152:155], v[192:195], v[48:51]
	v_mfma_f32_16x16x32_bf16 v[44:47], v[160:163], v[192:195], v[44:47]
	v_mfma_f32_16x16x32_bf16 v[32:35], v[152:155], v[200:203], v[32:35]
	v_mfma_f32_16x16x32_bf16 v[28:31], v[160:163], v[200:203], v[28:31]
	v_mfma_f32_16x16x32_bf16 v[16:19], v[152:155], v[208:211], v[16:19]
	v_mfma_f32_16x16x32_bf16 v[12:15], v[160:163], v[208:211], v[12:15]
	s_setprio 0
	s_setprio 1
	v_mfma_f32_16x16x32_bf16 v[56:59], v[164:167], v[180:183], v[56:59]
	v_mfma_f32_16x16x32_bf16 v[52:55], v[172:175], v[180:183], v[52:55]
	v_mfma_f32_16x16x32_bf16 v[40:43], v[164:167], v[188:191], v[40:43]
	v_mfma_f32_16x16x32_bf16 v[36:39], v[172:175], v[188:191], v[36:39]
	v_mfma_f32_16x16x32_bf16 v[24:27], v[164:167], v[196:199], v[24:27]
	v_mfma_f32_16x16x32_bf16 v[20:23], v[172:175], v[196:199], v[20:23]
	v_mfma_f32_16x16x32_bf16 v[8:11], v[164:167], v[204:207], v[8:11]
	v_mfma_f32_16x16x32_bf16 v[4:7], v[172:175], v[204:207], v[4:7]
	v_mfma_f32_16x16x32_bf16 v[56:59], v[168:171], v[184:187], v[56:59]
	v_mfma_f32_16x16x32_bf16 v[52:55], v[176:179], v[184:187], v[52:55]
	v_mfma_f32_16x16x32_bf16 v[40:43], v[168:171], v[192:195], v[40:43]
	v_mfma_f32_16x16x32_bf16 v[36:39], v[176:179], v[192:195], v[36:39]
	v_mfma_f32_16x16x32_bf16 v[24:27], v[168:171], v[200:203], v[24:27]
	v_mfma_f32_16x16x32_bf16 v[20:23], v[176:179], v[200:203], v[20:23]
	v_mfma_f32_16x16x32_bf16 v[8:11], v[168:171], v[208:211], v[8:11]
	v_mfma_f32_16x16x32_bf16 v[4:7], v[176:179], v[208:211], v[4:7]
	s_barrier
	s_setprio 0
	s_add_u32 s26, s26, 0x100
	s_addc_u32 s27, s27, 0
	s_add_u32 s19, s19, 0x100
	s_addc_u32 s20, s20, 0
	s_cmp_ge_i32 s22, s46
	s_mov_b32 s21, s22
	s_cbranch_scc1 .LBB0_3500
.LBB0_3499:
	s_add_i32 s22, s21, 2
	s_add_u32 s23, s26, 0x80
	s_addc_u32 s28, s27, 0
	s_add_i32 s55, 0, 0x10000
	s_cmp_eq_u32 s49, s21
	s_cselect_b32 s31, s15, s28
	s_cselect_b32 s30, s14, s23
	v_add_u32_e32 v2, s55, v145
	s_cselect_b32 s29, s17, s20
	s_cselect_b32 s28, s16, s19
	s_add_i32 s21, 0, 0x14000
	ds_read_b128 v[148:151], v2
	ds_read_b128 v[152:155], v2 offset:1024
	ds_read_b128 v[156:159], v2 offset:2048
	ds_read_b128 v[160:163], v2 offset:3072
	v_add_u32_e32 v2, s21, v145
	ds_read_b128 v[164:167], v2
	ds_read_b128 v[168:171], v2 offset:1024
	ds_read_b128 v[172:175], v2 offset:2048
	ds_read_b128 v[176:179], v2 offset:3072
	v_lshl_add_u64 v[212:213], s[26:27], 0, v[140:141]
	s_add_i32 m0, s42, 0xc000
	ds_read_b128 v[180:183], v147
	ds_read_b128 v[184:187], v147 offset:1024
	ds_read_b128 v[188:191], v147 offset:2048
	ds_read_b128 v[192:195], v147 offset:3072
	ds_read_b128 v[196:199], v147 offset:4096
	ds_read_b128 v[200:203], v147 offset:5120
	ds_read_b128 v[204:207], v147 offset:6144
	ds_read_b128 v[208:211], v147 offset:7168
	global_load_lds_dwordx4 v[212:213], off
	v_lshl_add_u64 v[212:213], s[26:27], 0, v[142:143]
	s_add_i32 m0, s42, 0xe000
	s_nop 0
	global_load_lds_dwordx4 v[212:213], off
	s_waitcnt vmcnt(8)
	s_waitcnt lgkmcnt(0)
	s_barrier
	s_setprio 1
	v_mfma_f32_16x16x32_bf16 v[124:127], v[148:151], v[180:183], v[124:127]
	v_mfma_f32_16x16x32_bf16 v[128:131], v[156:159], v[180:183], v[128:131]
	v_mfma_f32_16x16x32_bf16 v[112:115], v[148:151], v[188:191], v[112:115]
	v_mfma_f32_16x16x32_bf16 v[108:111], v[156:159], v[188:191], v[108:111]
	v_mfma_f32_16x16x32_bf16 v[96:99], v[148:151], v[196:199], v[96:99]
	v_mfma_f32_16x16x32_bf16 v[92:95], v[156:159], v[196:199], v[92:95]
	v_mfma_f32_16x16x32_bf16 v[80:83], v[148:151], v[204:207], v[80:83]
	v_mfma_f32_16x16x32_bf16 v[76:79], v[156:159], v[204:207], v[76:79]
	v_mfma_f32_16x16x32_bf16 v[124:127], v[152:155], v[184:187], v[124:127]
	v_mfma_f32_16x16x32_bf16 v[128:131], v[160:163], v[184:187], v[128:131]
	v_mfma_f32_16x16x32_bf16 v[112:115], v[152:155], v[192:195], v[112:115]
	v_mfma_f32_16x16x32_bf16 v[108:111], v[160:163], v[192:195], v[108:111]
	v_mfma_f32_16x16x32_bf16 v[96:99], v[152:155], v[200:203], v[96:99]
	v_mfma_f32_16x16x32_bf16 v[92:95], v[160:163], v[200:203], v[92:95]
	v_mfma_f32_16x16x32_bf16 v[80:83], v[152:155], v[208:211], v[80:83]
	v_mfma_f32_16x16x32_bf16 v[76:79], v[160:163], v[208:211], v[76:79]
	s_setprio 0
	s_setprio 1
	v_mfma_f32_16x16x32_bf16 v[120:123], v[164:167], v[180:183], v[120:123]
	v_mfma_f32_16x16x32_bf16 v[116:119], v[172:175], v[180:183], v[116:119]
	v_mfma_f32_16x16x32_bf16 v[104:107], v[164:167], v[188:191], v[104:107]
	v_mfma_f32_16x16x32_bf16 v[100:103], v[172:175], v[188:191], v[100:103]
	v_mfma_f32_16x16x32_bf16 v[88:91], v[164:167], v[196:199], v[88:91]
	v_mfma_f32_16x16x32_bf16 v[84:87], v[172:175], v[196:199], v[84:87]
	v_mfma_f32_16x16x32_bf16 v[72:75], v[164:167], v[204:207], v[72:75]
	v_mfma_f32_16x16x32_bf16 v[68:71], v[172:175], v[204:207], v[68:71]
	v_mfma_f32_16x16x32_bf16 v[120:123], v[168:171], v[184:187], v[120:123]
	v_mfma_f32_16x16x32_bf16 v[116:119], v[176:179], v[184:187], v[116:119]
	v_mfma_f32_16x16x32_bf16 v[104:107], v[168:171], v[192:195], v[104:107]
	v_mfma_f32_16x16x32_bf16 v[100:103], v[176:179], v[192:195], v[100:103]
	v_mfma_f32_16x16x32_bf16 v[88:91], v[168:171], v[200:203], v[88:91]
	v_mfma_f32_16x16x32_bf16 v[84:87], v[176:179], v[200:203], v[84:87]
	v_mfma_f32_16x16x32_bf16 v[72:75], v[168:171], v[208:211], v[72:75]
	v_mfma_f32_16x16x32_bf16 v[68:71], v[176:179], v[208:211], v[68:71]
	s_barrier
	s_setprio 0
	s_add_i32 s23, s55, s41
	v_lshl_add_u64 v[212:213], s[28:29], 0, v[136:137]
	s_mov_b32 m0, s23
	ds_read_b128 v[180:183], v147 offset:16384
	ds_read_b128 v[184:187], v147 offset:17408
	ds_read_b128 v[188:191], v147 offset:18432
	ds_read_b128 v[192:195], v147 offset:19456
	ds_read_b128 v[196:199], v147 offset:20480
	ds_read_b128 v[200:203], v147 offset:21504
	ds_read_b128 v[204:207], v147 offset:22528
	ds_read_b128 v[208:211], v147 offset:23552
	global_load_lds_dwordx4 v[212:213], off
	s_add_i32 m0, s23, 0x2000
	v_lshl_add_u64 v[214:215], s[28:29], 0, v[132:133]
	s_add_u32 s28, s28, s2
	s_addc_u32 s29, s29, s3
	s_add_i32 s21, s21, s41
	global_load_lds_dwordx4 v[214:215], off
	v_lshl_add_u64 v[218:219], s[28:29], 0, v[136:137]
	s_mov_b32 m0, s21
	v_lshl_add_u64 v[220:221], s[28:29], 0, v[132:133]
	global_load_lds_dwordx4 v[218:219], off
	s_add_i32 m0, s21, 0x2000
	v_lshl_add_u64 v[222:223], s[30:31], 0, v[138:139]
	global_load_lds_dwordx4 v[220:221], off
	s_mov_b32 m0, s42
	v_lshl_add_u64 v[224:225], s[30:31], 0, v[134:135]
	global_load_lds_dwordx4 v[222:223], off
	s_mov_b32 m0, s43
	s_nop 0
	global_load_lds_dwordx4 v[224:225], off
	s_waitcnt vmcnt(8)
	s_waitcnt lgkmcnt(0)
	s_barrier
	s_setprio 1
	v_mfma_f32_16x16x32_bf16 v[64:67], v[148:151], v[180:183], v[64:67]
	v_mfma_f32_16x16x32_bf16 v[60:63], v[156:159], v[180:183], v[60:63]
	v_mfma_f32_16x16x32_bf16 v[48:51], v[148:151], v[188:191], v[48:51]
	v_mfma_f32_16x16x32_bf16 v[44:47], v[156:159], v[188:191], v[44:47]
	v_mfma_f32_16x16x32_bf16 v[32:35], v[148:151], v[196:199], v[32:35]
	v_mfma_f32_16x16x32_bf16 v[28:31], v[156:159], v[196:199], v[28:31]
	v_mfma_f32_16x16x32_bf16 v[16:19], v[148:151], v[204:207], v[16:19]
	v_mfma_f32_16x16x32_bf16 v[12:15], v[156:159], v[204:207], v[12:15]
	v_mfma_f32_16x16x32_bf16 v[64:67], v[152:155], v[184:187], v[64:67]
	v_mfma_f32_16x16x32_bf16 v[60:63], v[160:163], v[184:187], v[60:63]
	v_mfma_f32_16x16x32_bf16 v[48:51], v[152:155], v[192:195], v[48:51]
	v_mfma_f32_16x16x32_bf16 v[44:47], v[160:163], v[192:195], v[44:47]
	v_mfma_f32_16x16x32_bf16 v[32:35], v[152:155], v[200:203], v[32:35]
	v_mfma_f32_16x16x32_bf16 v[28:31], v[160:163], v[200:203], v[28:31]
	v_mfma_f32_16x16x32_bf16 v[16:19], v[152:155], v[208:211], v[16:19]
	v_mfma_f32_16x16x32_bf16 v[12:15], v[160:163], v[208:211], v[12:15]
	s_setprio 0
	s_setprio 1
	v_mfma_f32_16x16x32_bf16 v[56:59], v[164:167], v[180:183], v[56:59]
	v_mfma_f32_16x16x32_bf16 v[52:55], v[172:175], v[180:183], v[52:55]
	v_mfma_f32_16x16x32_bf16 v[40:43], v[164:167], v[188:191], v[40:43]
	v_mfma_f32_16x16x32_bf16 v[36:39], v[172:175], v[188:191], v[36:39]
	v_mfma_f32_16x16x32_bf16 v[24:27], v[164:167], v[196:199], v[24:27]
	v_mfma_f32_16x16x32_bf16 v[20:23], v[172:175], v[196:199], v[20:23]
	v_mfma_f32_16x16x32_bf16 v[8:11], v[164:167], v[204:207], v[8:11]
	v_mfma_f32_16x16x32_bf16 v[4:7], v[172:175], v[204:207], v[4:7]
	v_mfma_f32_16x16x32_bf16 v[56:59], v[168:171], v[184:187], v[56:59]
	v_mfma_f32_16x16x32_bf16 v[52:55], v[176:179], v[184:187], v[52:55]
	v_mfma_f32_16x16x32_bf16 v[40:43], v[168:171], v[192:195], v[40:43]
	v_mfma_f32_16x16x32_bf16 v[36:39], v[176:179], v[192:195], v[36:39]
	v_mfma_f32_16x16x32_bf16 v[24:27], v[168:171], v[200:203], v[24:27]
	v_mfma_f32_16x16x32_bf16 v[20:23], v[176:179], v[200:203], v[20:23]
	v_mfma_f32_16x16x32_bf16 v[8:11], v[168:171], v[208:211], v[8:11]
	v_mfma_f32_16x16x32_bf16 v[4:7], v[176:179], v[208:211], v[4:7]
	s_barrier
	s_setprio 0
	s_add_i32 s21, 0, 0x18000
	v_add_u32_e32 v2, s21, v145
	s_add_i32 s23, 0, 0x1c000
	ds_read_b128 v[148:151], v2
	ds_read_b128 v[152:155], v2 offset:1024
	ds_read_b128 v[156:159], v2 offset:2048
	ds_read_b128 v[160:163], v2 offset:3072
	v_add_u32_e32 v2, s23, v145
	ds_read_b128 v[164:167], v2
	ds_read_b128 v[168:171], v2 offset:1024
	ds_read_b128 v[172:175], v2 offset:2048
	ds_read_b128 v[176:179], v2 offset:3072
	s_add_u32 s28, s30, s2
	s_addc_u32 s29, s31, s3
	s_mov_b32 m0, s44
	v_lshl_add_u64 v[226:227], s[28:29], 0, v[138:139]
	ds_read_b128 v[180:183], v147 offset:32768
	ds_read_b128 v[184:187], v147 offset:33792
	ds_read_b128 v[188:191], v147 offset:34816
	ds_read_b128 v[192:195], v147 offset:35840
	ds_read_b128 v[196:199], v147 offset:36864
	ds_read_b128 v[200:203], v147 offset:37888
	ds_read_b128 v[204:207], v147 offset:38912
	ds_read_b128 v[208:211], v147 offset:39936
	global_load_lds_dwordx4 v[226:227], off
	v_lshl_add_u64 v[226:227], s[28:29], 0, v[134:135]
	s_mov_b32 m0, s45
	s_nop 0
	global_load_lds_dwordx4 v[226:227], off
	s_waitcnt vmcnt(8)
	s_waitcnt lgkmcnt(0)
	s_barrier
	s_setprio 1
	v_mfma_f32_16x16x32_bf16 v[124:127], v[148:151], v[180:183], v[124:127]
	v_mfma_f32_16x16x32_bf16 v[128:131], v[156:159], v[180:183], v[128:131]
	v_mfma_f32_16x16x32_bf16 v[112:115], v[148:151], v[188:191], v[112:115]
	v_mfma_f32_16x16x32_bf16 v[108:111], v[156:159], v[188:191], v[108:111]
	v_mfma_f32_16x16x32_bf16 v[96:99], v[148:151], v[196:199], v[96:99]
	v_mfma_f32_16x16x32_bf16 v[92:95], v[156:159], v[196:199], v[92:95]
	v_mfma_f32_16x16x32_bf16 v[80:83], v[148:151], v[204:207], v[80:83]
	v_mfma_f32_16x16x32_bf16 v[76:79], v[156:159], v[204:207], v[76:79]
	v_mfma_f32_16x16x32_bf16 v[124:127], v[152:155], v[184:187], v[124:127]
	v_mfma_f32_16x16x32_bf16 v[128:131], v[160:163], v[184:187], v[128:131]
	v_mfma_f32_16x16x32_bf16 v[112:115], v[152:155], v[192:195], v[112:115]
	v_mfma_f32_16x16x32_bf16 v[108:111], v[160:163], v[192:195], v[108:111]
	v_mfma_f32_16x16x32_bf16 v[96:99], v[152:155], v[200:203], v[96:99]
	v_mfma_f32_16x16x32_bf16 v[92:95], v[160:163], v[200:203], v[92:95]
	v_mfma_f32_16x16x32_bf16 v[80:83], v[152:155], v[208:211], v[80:83]
	v_mfma_f32_16x16x32_bf16 v[76:79], v[160:163], v[208:211], v[76:79]
	s_setprio 0
	s_setprio 1
	v_mfma_f32_16x16x32_bf16 v[120:123], v[164:167], v[180:183], v[120:123]
	v_mfma_f32_16x16x32_bf16 v[116:119], v[172:175], v[180:183], v[116:119]
	v_mfma_f32_16x16x32_bf16 v[104:107], v[164:167], v[188:191], v[104:107]
	v_mfma_f32_16x16x32_bf16 v[100:103], v[172:175], v[188:191], v[100:103]
	v_mfma_f32_16x16x32_bf16 v[88:91], v[164:167], v[196:199], v[88:91]
	v_mfma_f32_16x16x32_bf16 v[84:87], v[172:175], v[196:199], v[84:87]
	v_mfma_f32_16x16x32_bf16 v[72:75], v[164:167], v[204:207], v[72:75]
	v_mfma_f32_16x16x32_bf16 v[68:71], v[172:175], v[204:207], v[68:71]
	v_mfma_f32_16x16x32_bf16 v[120:123], v[168:171], v[184:187], v[120:123]
	v_mfma_f32_16x16x32_bf16 v[116:119], v[176:179], v[184:187], v[116:119]
	v_mfma_f32_16x16x32_bf16 v[104:107], v[168:171], v[192:195], v[104:107]
	v_mfma_f32_16x16x32_bf16 v[100:103], v[176:179], v[192:195], v[100:103]
	v_mfma_f32_16x16x32_bf16 v[88:91], v[168:171], v[200:203], v[88:91]
	v_mfma_f32_16x16x32_bf16 v[84:87], v[176:179], v[200:203], v[84:87]
	v_mfma_f32_16x16x32_bf16 v[72:75], v[168:171], v[208:211], v[72:75]
	v_mfma_f32_16x16x32_bf16 v[68:71], v[176:179], v[208:211], v[68:71]
	s_barrier
	s_setprio 0
	s_add_i32 s21, s21, s41
	v_lshl_add_u64 v[212:213], v[212:213], 0, s[24:25]
	s_mov_b32 m0, s21
	ds_read_b128 v[180:183], v147 offset:49152
	ds_read_b128 v[184:187], v147 offset:50176
	ds_read_b128 v[188:191], v147 offset:51200
	ds_read_b128 v[192:195], v147 offset:52224
	ds_read_b128 v[196:199], v147 offset:53248
	ds_read_b128 v[200:203], v147 offset:54272
	ds_read_b128 v[204:207], v147 offset:55296
	ds_read_b128 v[208:211], v147 offset:56320
	global_load_lds_dwordx4 v[212:213], off
	v_lshl_add_u64 v[212:213], v[214:215], 0, s[24:25]
	s_add_i32 m0, s21, 0x2000
	s_add_i32 s21, s23, s41
	global_load_lds_dwordx4 v[212:213], off
	v_lshl_add_u64 v[212:213], v[218:219], 0, s[24:25]
	s_mov_b32 m0, s21
	s_nop 0
	global_load_lds_dwordx4 v[212:213], off
	v_lshl_add_u64 v[212:213], v[220:221], 0, s[24:25]
	s_add_i32 m0, s21, 0x2000
	s_nop 0
	global_load_lds_dwordx4 v[212:213], off
	v_lshl_add_u64 v[212:213], v[222:223], 0, s[24:25]
	s_mov_b32 m0, s47
	s_nop 0
	global_load_lds_dwordx4 v[212:213], off
	v_lshl_add_u64 v[212:213], v[224:225], 0, s[24:25]
	s_mov_b32 m0, s48
	s_nop 0
	global_load_lds_dwordx4 v[212:213], off
	s_waitcnt vmcnt(8)
	s_waitcnt lgkmcnt(0)
	s_barrier
	s_setprio 1
	v_mfma_f32_16x16x32_bf16 v[64:67], v[148:151], v[180:183], v[64:67]
	v_mfma_f32_16x16x32_bf16 v[60:63], v[156:159], v[180:183], v[60:63]
	v_mfma_f32_16x16x32_bf16 v[48:51], v[148:151], v[188:191], v[48:51]
	v_mfma_f32_16x16x32_bf16 v[44:47], v[156:159], v[188:191], v[44:47]
	v_mfma_f32_16x16x32_bf16 v[32:35], v[148:151], v[196:199], v[32:35]
	v_mfma_f32_16x16x32_bf16 v[28:31], v[156:159], v[196:199], v[28:31]
	v_mfma_f32_16x16x32_bf16 v[16:19], v[148:151], v[204:207], v[16:19]
	v_mfma_f32_16x16x32_bf16 v[12:15], v[156:159], v[204:207], v[12:15]
	v_mfma_f32_16x16x32_bf16 v[64:67], v[152:155], v[184:187], v[64:67]
	v_mfma_f32_16x16x32_bf16 v[60:63], v[160:163], v[184:187], v[60:63]
	v_mfma_f32_16x16x32_bf16 v[48:51], v[152:155], v[192:195], v[48:51]
	v_mfma_f32_16x16x32_bf16 v[44:47], v[160:163], v[192:195], v[44:47]
	v_mfma_f32_16x16x32_bf16 v[32:35], v[152:155], v[200:203], v[32:35]
	v_mfma_f32_16x16x32_bf16 v[28:31], v[160:163], v[200:203], v[28:31]
	v_mfma_f32_16x16x32_bf16 v[16:19], v[152:155], v[208:211], v[16:19]
	v_mfma_f32_16x16x32_bf16 v[12:15], v[160:163], v[208:211], v[12:15]
	s_setprio 0
	s_setprio 1
	v_mfma_f32_16x16x32_bf16 v[56:59], v[164:167], v[180:183], v[56:59]
	v_mfma_f32_16x16x32_bf16 v[52:55], v[172:175], v[180:183], v[52:55]
	v_mfma_f32_16x16x32_bf16 v[40:43], v[164:167], v[188:191], v[40:43]
	v_mfma_f32_16x16x32_bf16 v[36:39], v[172:175], v[188:191], v[36:39]
	v_mfma_f32_16x16x32_bf16 v[24:27], v[164:167], v[196:199], v[24:27]
	v_mfma_f32_16x16x32_bf16 v[20:23], v[172:175], v[196:199], v[20:23]
	v_mfma_f32_16x16x32_bf16 v[8:11], v[164:167], v[204:207], v[8:11]
	v_mfma_f32_16x16x32_bf16 v[4:7], v[172:175], v[204:207], v[4:7]
	v_mfma_f32_16x16x32_bf16 v[56:59], v[168:171], v[184:187], v[56:59]
	v_mfma_f32_16x16x32_bf16 v[52:55], v[176:179], v[184:187], v[52:55]
	v_mfma_f32_16x16x32_bf16 v[40:43], v[168:171], v[192:195], v[40:43]
	v_mfma_f32_16x16x32_bf16 v[36:39], v[176:179], v[192:195], v[36:39]
	v_mfma_f32_16x16x32_bf16 v[24:27], v[168:171], v[200:203], v[24:27]
	v_mfma_f32_16x16x32_bf16 v[20:23], v[176:179], v[200:203], v[20:23]
	v_mfma_f32_16x16x32_bf16 v[8:11], v[168:171], v[208:211], v[8:11]
	v_mfma_f32_16x16x32_bf16 v[4:7], v[176:179], v[208:211], v[4:7]
	s_barrier
	s_setprio 0
	s_add_u32 s26, s26, 0x100
	s_addc_u32 s27, s27, 0
	s_add_u32 s19, s19, 0x100
	s_addc_u32 s20, s20, 0
	s_cmp_ge_i32 s22, s46
	s_mov_b32 s21, s22
	s_cbranch_scc0 .LBB0_3499
